# plus route-phase shift/scale table loads batched and hoisted above the x1 row loads; kernarg s_loads issued together at entry
# baseline (speedup 1.0000x reference)
_Z4mega4Args:
	s_load_dword s33, s[0:1], 0xb0
	s_load_dwordx2 s[10:11], s[0:1], 0xa0
	s_load_dwordx8 s[52:59], s[0:1], 0x80
	s_load_dwordx2 s[28:29], s[0:1], 0xa8
	s_load_dwordx16 s[36:51], s[0:1], 0x0
	s_load_dwordx16 s[12:27], s[0:1], 0x40
	s_add_u32 s4, s0, 0xb0
	s_addc_u32 s5, s1, 0
	v_readfirstlane_b32 s87, v0
	v_writelane_b32 v255, s4, 0
	s_waitcnt lgkmcnt(0)
	s_and_b32 s3, s33, 7
	s_cmp_lg_u32 s3, 0
	v_writelane_b32 v255, s5, 1
	s_cselect_b64 s[4:5], -1, 0
	v_writelane_b32 v255, s4, 2
	s_and_b64 vcc, exec, s[4:5]
	s_mov_b32 s76, s2
	v_writelane_b32 v255, s5, 3
	s_cbranch_vccnz .LBB0_2
	s_ashr_i32 s4, s2, 31
	s_lshr_b32 s4, s4, 29
	s_add_i32 s4, s2, s4
	s_and_b32 s5, s4, -8
	s_ashr_i32 s3, s33, 3
	s_sub_i32 s5, s2, s5
	s_mul_i32 s3, s3, s5
	s_ashr_i32 s4, s4, 3
	s_add_i32 s76, s3, s4
.LBB0_2:
	s_add_i32 s3, 0, 0x20000
	v_lshl_add_u32 v1, v0, 2, s3
	v_mov_b32_e32 v2, 0
	v_or_b32_e32 v196, 0x400, v0
	ds_write2st64_b32 v1, v2, v2 offset1:8
	v_lshl_add_u32 v1, v196, 2, s3
	ds_write2st64_b32 v1, v2, v2 offset1:8
	v_or_b32_e32 v1, 0x800, v0
	s_mov_b64 s[4:5], -1
	s_and_saveexec_b64 s[6:7], s[4:5]
	v_lshl_add_u32 v3, v1, 2, 0
	v_add_u32_e32 v3, 0x20000, v3
	ds_write_b32 v3, v2
	s_or_b64 exec, exec, s[6:7]
	s_and_saveexec_b64 s[6:7], s[4:5]
	v_lshl_add_u32 v2, v1, 2, s3
	v_mov_b32_e32 v3, 0
	ds_write_b32 v2, v3 offset:2048
	s_or_b64 exec, exec, s[6:7]
	v_or_b32_e32 v197, 0xc00, v0
	v_cmp_gt_u32_e64 s[4:5], 7, 6
	v_cmp_gt_u32_e64 s[8:9], 7, 5
	s_and_saveexec_b64 s[6:7], s[8:9]
	v_lshl_add_u32 v2, v197, 2, 0
	v_add_u32_e32 v2, 0x20000, v2
	v_mov_b32_e32 v3, 0
	ds_write_b32 v2, v3
	s_or_b64 exec, exec, s[6:7]
	s_and_saveexec_b64 s[6:7], s[4:5]
	v_lshl_add_u32 v2, v197, 2, s3
	v_mov_b32_e32 v3, 0
	ds_write_b32 v2, v3 offset:2048
	s_or_b64 exec, exec, s[6:7]
	s_waitcnt lgkmcnt(0)
	s_mul_i32 s4, s28, 0xd80
	s_ashr_i32 s5, s4, 31
	s_lshl_b64 s[4:5], s[4:5], 2
	s_add_u32 s3, s10, s4
	s_addc_u32 s4, s11, s5
	s_add_u32 s30, s3, 0x4000
	s_addc_u32 s31, s4, 0
	s_sub_i32 s3, s29, s28
	s_mov_b32 s75, 0
	s_cmp_lt_i32 s3, 2
	v_cmp_eq_u32_e32 vcc, 0, v0
	s_mov_b32 s88, 0
	s_waitcnt lgkmcnt(0)
	s_barrier
	s_cbranch_scc1 .LBB0_15
	s_getreg_b32 s3, hwreg(HW_REG_XCC_ID, 0, 4)
	s_and_b32 s75, s3, 15
	s_and_saveexec_b64 s[4:5], vcc
	s_cbranch_execz .LBB0_14
	s_mov_b64 s[6:7], exec
	v_mbcnt_lo_u32_b32 v2, s6, 0
	v_mbcnt_hi_u32_b32 v2, s7, v2
	v_cmp_eq_u32_e32 vcc, 0, v2
	s_and_b64 s[8:9], exec, vcc
	s_mov_b64 exec, s[8:9]
	s_cbranch_execz .LBB0_14
	s_lshl_b32 s3, s75, 8
	s_bcnt1_i32_b64 s6, s[6:7]
	v_mov_b32_e32 v2, s3
	v_mov_b32_e32 v3, s6
	global_atomic_add v2, v3, s[30:31] offset:1024

.LBB0_15:
	s_lshr_b32 s86, s87, 6
	s_cmp_lt_i32 s28, 1
	s_cselect_b64 s[62:63], -1, 0
	s_cmp_gt_i32 s28, 0
	s_cselect_b64 s[0:1], -1, 0
	s_cmp_lt_i32 s29, 1
	s_cselect_b64 s[4:5], -1, 0
	v_writelane_b32 v255, s86, 4
	s_or_b64 s[0:1], s[0:1], s[4:5]
	v_writelane_b32 v255, s87, 5
	v_and_b32_e32 v254, 63, v0
	s_and_b64 vcc, exec, s[0:1]
	v_writelane_b32 v255, s88, 6
	s_cbranch_vccnz .LBB0_57
	v_lshlrev_b32_e32 v2, 2, v0
	v_add_u32_e32 v5, 0x18000, v2
	v_add_u32_e32 v3, 0x1000, v2
	v_add_u32_e32 v4, 0x2000, v2
	v_add_u32_e32 v22, 0x3000, v2
	global_load_dword v6, v2, s[38:39]
	global_load_dword v7, v2, s[38:39] offset:2048
	global_load_dword v8, v3, s[38:39]
	global_load_dword v9, v3, s[38:39] offset:2048
	global_load_dword v10, v4, s[38:39]
	global_load_dword v11, v4, s[38:39] offset:2048
	global_load_dword v12, v22, s[38:39]
	global_load_dword v13, v22, s[38:39] offset:2048
	v_add_u32_e32 v3, 0x4000, v2
	v_add_u32_e32 v4, 0x5000, v2
	v_add_u32_e32 v22, 0x6000, v2
	v_add_u32_e32 v23, 0x7000, v2
	global_load_dword v14, v3, s[38:39]
	global_load_dword v15, v3, s[38:39] offset:2048
	global_load_dword v16, v4, s[38:39]
	global_load_dword v17, v4, s[38:39] offset:2048
	global_load_dword v18, v22, s[38:39]
	global_load_dword v19, v22, s[38:39] offset:2048
	global_load_dword v20, v23, s[38:39]
	global_load_dword v21, v23, s[38:39] offset:2048
	s_waitcnt vmcnt(12)
	v_mul_f32_e32 v3, 0xbfb8aa3b, v6
	v_mul_f32_e32 v4, 0xbfb8aa3b, v7
	v_mul_f32_e32 v22, 0xbfb8aa3b, v8
	v_mul_f32_e32 v23, 0xbfb8aa3b, v9
	v_exp_f32_e32 v3, v3
	v_exp_f32_e32 v4, v4
	v_exp_f32_e32 v22, v22
	v_exp_f32_e32 v23, v23
	s_nop 0
	v_add_f32_e32 v3, 1.0, v3
	v_add_f32_e32 v4, 1.0, v4
	v_add_f32_e32 v22, 1.0, v22
	v_add_f32_e32 v23, 1.0, v23
	v_rcp_f32_e32 v3, v3
	v_rcp_f32_e32 v4, v4
	v_rcp_f32_e32 v22, v22
	v_rcp_f32_e32 v23, v23
	s_nop 0
	v_mul_f32_e32 v6, v6, v3
	v_mul_f32_e32 v7, v7, v4
	v_mul_f32_e32 v8, v8, v22
	v_mul_f32_e32 v9, v9, v23
	ds_write_b32 v5, v6 offset:0
	ds_write_b32 v5, v7 offset:2048
	ds_write_b32 v5, v8 offset:4096
	ds_write_b32 v5, v9 offset:6144
	s_waitcnt vmcnt(8)
	v_mul_f32_e32 v3, 0xbfb8aa3b, v10
	v_mul_f32_e32 v4, 0xbfb8aa3b, v11
	v_mul_f32_e32 v22, 0xbfb8aa3b, v12
	v_mul_f32_e32 v23, 0xbfb8aa3b, v13
	v_exp_f32_e32 v3, v3
	v_exp_f32_e32 v4, v4
	v_exp_f32_e32 v22, v22
	v_exp_f32_e32 v23, v23
	s_nop 0
	v_add_f32_e32 v3, 1.0, v3
	v_add_f32_e32 v4, 1.0, v4
	v_add_f32_e32 v22, 1.0, v22
	v_add_f32_e32 v23, 1.0, v23
	v_rcp_f32_e32 v3, v3
	v_rcp_f32_e32 v4, v4
	v_rcp_f32_e32 v22, v22
	v_rcp_f32_e32 v23, v23
	s_nop 0
	v_mul_f32_e32 v10, v10, v3
	v_mul_f32_e32 v11, v11, v4
	v_mul_f32_e32 v12, v12, v22
	v_mul_f32_e32 v13, v13, v23
	ds_write_b32 v5, v10 offset:8192
	ds_write_b32 v5, v11 offset:10240
	ds_write_b32 v5, v12 offset:12288
	ds_write_b32 v5, v13 offset:14336
	s_waitcnt vmcnt(4)
	v_mul_f32_e32 v3, 0xbfb8aa3b, v14
	v_mul_f32_e32 v4, 0xbfb8aa3b, v15
	v_mul_f32_e32 v22, 0xbfb8aa3b, v16
	v_mul_f32_e32 v23, 0xbfb8aa3b, v17
	v_exp_f32_e32 v3, v3
	v_exp_f32_e32 v4, v4
	v_exp_f32_e32 v22, v22
	v_exp_f32_e32 v23, v23
	s_nop 0
	v_add_f32_e32 v3, 1.0, v3
	v_add_f32_e32 v4, 1.0, v4
	v_add_f32_e32 v22, 1.0, v22
	v_add_f32_e32 v23, 1.0, v23
	v_rcp_f32_e32 v3, v3
	v_rcp_f32_e32 v4, v4
	v_rcp_f32_e32 v22, v22
	v_rcp_f32_e32 v23, v23
	s_nop 0
	v_mul_f32_e32 v14, v14, v3
	v_mul_f32_e32 v15, v15, v4
	v_mul_f32_e32 v16, v16, v22
	v_mul_f32_e32 v17, v17, v23
	ds_write_b32 v5, v14 offset:16384
	ds_write_b32 v5, v15 offset:18432
	ds_write_b32 v5, v16 offset:20480
	ds_write_b32 v5, v17 offset:22528
	s_waitcnt vmcnt(0)
	v_mul_f32_e32 v3, 0xbfb8aa3b, v18
	v_mul_f32_e32 v4, 0xbfb8aa3b, v19
	v_mul_f32_e32 v22, 0xbfb8aa3b, v20
	v_mul_f32_e32 v23, 0xbfb8aa3b, v21
	v_exp_f32_e32 v3, v3
	v_exp_f32_e32 v4, v4
	v_exp_f32_e32 v22, v22
	v_exp_f32_e32 v23, v23
	s_nop 0
	v_add_f32_e32 v3, 1.0, v3
	v_add_f32_e32 v4, 1.0, v4
	v_add_f32_e32 v22, 1.0, v22
	v_add_f32_e32 v23, 1.0, v23
	v_rcp_f32_e32 v3, v3
	v_rcp_f32_e32 v4, v4
	v_rcp_f32_e32 v22, v22
	v_rcp_f32_e32 v23, v23
	s_nop 0
	v_mul_f32_e32 v18, v18, v3
	v_mul_f32_e32 v19, v19, v4
	v_mul_f32_e32 v20, v20, v22
	v_mul_f32_e32 v21, v21, v23
	ds_write_b32 v5, v18 offset:24576
	ds_write_b32 v5, v19 offset:26624
	ds_write_b32 v5, v20 offset:28672
	ds_write_b32 v5, v21 offset:30720
	s_cmpk_gt_u32 s87, 0xbf
	s_mov_b64 s[0:1], -1
	s_waitcnt lgkmcnt(0)
	s_barrier
	s_cbranch_scc0 .LBB0_27
	s_add_i32 s0, s86, -3
	s_mul_i32 s1, s76, 5
	s_add_i32 s91, s1, s0
	s_cmpk_gt_i32 s91, 0x19ff
	s_cbranch_scc1 .LBB0_26
	s_mul_hi_i32 s1, s91, 0x4ec4ec4f
	s_lshr_b32 s3, s1, 31
	s_ashr_i32 s1, s1, 6
	s_add_i32 s1, s1, s3
	s_mulk_i32 s0, 0x4200
	s_mul_i32 s3, s1, 0xd0
	s_add_i32 s0, s0, 0
	s_sub_i32 s3, s91, s3
	s_lshl_b32 s4, s1, 6
	s_mul_i32 s1, s1, 0x340000
	s_mul_hi_i32 s4, s4, 0xd000
	s_add_u32 s1, s46, s1
	s_addc_u32 s6, s47, s4
	s_lshl_b32 s4, s3, 6
	s_ashr_i32 s5, s4, 31
	s_lshl_b64 s[4:5], s[4:5], 2
	v_lshlrev_b32_e32 v2, 1, v0
	s_add_u32 s4, s1, s4
	v_and_b32_e32 v4, 62, v2
	v_lshrrev_b32_e32 v5, 5, v254
	s_addc_u32 s5, s6, s5
	v_mov_b32_e32 v3, 0
	v_lshlrev_b32_e32 v2, 2, v4
	v_mul_u32_u24_e32 v8, 0x3400, v5
	v_lshl_add_u64 v[6:7], s[4:5], 0, v[2:3]
	v_lshlrev_b32_e32 v10, 2, v8
	v_mov_b32_e32 v11, v3
	v_lshl_add_u64 v[6:7], v[6:7], 0, v[10:11]
	s_mov_b32 s3, 0x1a000
	v_add_co_u32_e32 v10, vcc, s3, v6
	s_mov_b32 s6, 0x34000
	s_nop 0
	v_addc_co_u32_e32 v11, vcc, 0, v7, vcc
	v_add_co_u32_e32 v12, vcc, s6, v6
	s_mov_b32 s7, 0x4e000
	s_nop 0
	v_addc_co_u32_e32 v13, vcc, 0, v7, vcc
	v_add_co_u32_e32 v14, vcc, s7, v6
	s_mov_b32 s8, 0x68000
	s_nop 0
	v_addc_co_u32_e32 v15, vcc, 0, v7, vcc
	global_load_dwordx2 v[84:85], v[6:7], off
	global_load_dwordx2 v[76:77], v[10:11], off
	global_load_dwordx2 v[74:75], v[12:13], off
	global_load_dwordx2 v[72:73], v[14:15], off
	v_add_co_u32_e32 v10, vcc, s8, v6
	s_mov_b32 s9, 0x82000
	s_nop 0
	v_addc_co_u32_e32 v11, vcc, 0, v7, vcc
	v_add_co_u32_e32 v12, vcc, s9, v6
	s_mov_b32 s34, 0x9c000
	s_nop 0
	v_addc_co_u32_e32 v13, vcc, 0, v7, vcc
	v_add_co_u32_e32 v14, vcc, s34, v6
	s_mov_b32 s35, 0xb6000
	s_nop 0
	v_addc_co_u32_e32 v15, vcc, 0, v7, vcc
	v_add_co_u32_e32 v16, vcc, s35, v6
	s_mov_b32 s38, 0xd0000
	s_nop 0
	v_addc_co_u32_e32 v17, vcc, 0, v7, vcc
	global_load_dwordx2 v[94:95], v[10:11], off
	global_load_dwordx2 v[92:93], v[12:13], off
	global_load_dwordx2 v[90:91], v[14:15], off
	global_load_dwordx2 v[88:89], v[16:17], off
	v_add_co_u32_e32 v10, vcc, s38, v6
	s_mov_b32 s39, 0xea000
	s_nop 0
	v_addc_co_u32_e32 v11, vcc, 0, v7, vcc
	v_add_co_u32_e32 v12, vcc, s39, v6
	s_mov_b32 s60, 0x104000
	s_nop 0
	v_addc_co_u32_e32 v13, vcc, 0, v7, vcc
	v_add_co_u32_e32 v14, vcc, s60, v6
	s_mov_b32 s61, 0x11e000
	s_nop 0
	v_addc_co_u32_e32 v15, vcc, 0, v7, vcc
	v_add_co_u32_e32 v16, vcc, s61, v6
	s_mov_b32 s64, 0x138000
	s_nop 0
	v_addc_co_u32_e32 v17, vcc, 0, v7, vcc
	global_load_dwordx2 v[110:111], v[10:11], off
	global_load_dwordx2 v[108:109], v[12:13], off
	global_load_dwordx2 v[106:107], v[14:15], off
	global_load_dwordx2 v[104:105], v[16:17], off
	v_add_co_u32_e32 v10, vcc, s64, v6
	s_mov_b32 s65, 0x152000
	s_nop 0
	v_addc_co_u32_e32 v11, vcc, 0, v7, vcc
	v_add_co_u32_e32 v12, vcc, s65, v6
	s_mov_b32 s66, 0x16c000
	s_nop 0
	v_addc_co_u32_e32 v13, vcc, 0, v7, vcc
	v_add_co_u32_e32 v14, vcc, s66, v6
	s_mov_b32 s67, 0x186000
	s_nop 0
	v_addc_co_u32_e32 v15, vcc, 0, v7, vcc
	v_add_co_u32_e32 v16, vcc, s67, v6
	s_mov_b32 s68, 0x1a0000
	s_nop 0
	v_addc_co_u32_e32 v17, vcc, 0, v7, vcc
	global_load_dwordx2 v[118:119], v[10:11], off
	global_load_dwordx2 v[116:117], v[12:13], off
	global_load_dwordx2 v[114:115], v[14:15], off
	global_load_dwordx2 v[112:113], v[16:17], off
	v_add_co_u32_e32 v10, vcc, s68, v6
	s_mov_b32 s69, 0x1ba000
	s_nop 0
	v_addc_co_u32_e32 v11, vcc, 0, v7, vcc
	v_add_co_u32_e32 v12, vcc, s69, v6
	s_mov_b32 s70, 0x1d4000
	s_nop 0
	v_addc_co_u32_e32 v13, vcc, 0, v7, vcc
	v_add_co_u32_e32 v14, vcc, s70, v6
	s_mov_b32 s71, 0x1ee000
	s_nop 0
	v_addc_co_u32_e32 v15, vcc, 0, v7, vcc
	v_add_co_u32_e32 v16, vcc, s71, v6
	s_mov_b32 s77, 0x208000
	s_nop 0
	v_addc_co_u32_e32 v17, vcc, 0, v7, vcc
	global_load_dwordx2 v[126:127], v[10:11], off
	global_load_dwordx2 v[124:125], v[12:13], off
	global_load_dwordx2 v[122:123], v[14:15], off
	global_load_dwordx2 v[120:121], v[16:17], off
	v_add_co_u32_e32 v10, vcc, s77, v6
	s_mov_b32 s78, 0x222000
	s_nop 0
	v_addc_co_u32_e32 v11, vcc, 0, v7, vcc
	v_add_co_u32_e32 v12, vcc, s78, v6
	s_mov_b32 s79, 0x23c000
	s_nop 0
	v_addc_co_u32_e32 v13, vcc, 0, v7, vcc
	v_add_co_u32_e32 v14, vcc, s79, v6
	s_mov_b32 s80, 0x256000
	s_nop 0
	v_addc_co_u32_e32 v15, vcc, 0, v7, vcc
	v_add_co_u32_e32 v16, vcc, s80, v6
	s_mov_b32 s81, 0x270000
	s_nop 0
	v_addc_co_u32_e32 v17, vcc, 0, v7, vcc
	global_load_dwordx2 v[134:135], v[10:11], off
	global_load_dwordx2 v[132:133], v[12:13], off
	global_load_dwordx2 v[130:131], v[14:15], off
	global_load_dwordx2 v[128:129], v[16:17], off
	v_add_co_u32_e32 v10, vcc, s81, v6
	s_mov_b32 s82, 0x28a000
	s_nop 0
	v_addc_co_u32_e32 v11, vcc, 0, v7, vcc
	v_add_co_u32_e32 v12, vcc, s82, v6
	s_mov_b32 s83, 0x2a4000
	s_nop 0
	v_addc_co_u32_e32 v13, vcc, 0, v7, vcc
	v_add_co_u32_e32 v14, vcc, s83, v6
	s_mov_b32 s84, 0x2be000
	s_nop 0
	v_addc_co_u32_e32 v15, vcc, 0, v7, vcc
	v_add_co_u32_e32 v16, vcc, s84, v6
	s_mov_b32 s1, 0x2d8000
	s_nop 0
	v_addc_co_u32_e32 v17, vcc, 0, v7, vcc
	global_load_dwordx2 v[142:143], v[10:11], off
	global_load_dwordx2 v[140:141], v[12:13], off
	global_load_dwordx2 v[138:139], v[14:15], off
	global_load_dwordx2 v[136:137], v[16:17], off
	v_add_co_u32_e32 v10, vcc, s1, v6
	s_mov_b32 s1, 0x2f2000
	s_nop 0
	v_addc_co_u32_e32 v11, vcc, 0, v7, vcc
	v_add_co_u32_e32 v12, vcc, s1, v6
	s_mov_b32 s1, 0x30c000
	s_nop 0
	v_addc_co_u32_e32 v13, vcc, 0, v7, vcc
	v_add_co_u32_e32 v14, vcc, s1, v6
	s_mov_b32 s1, 0x326000
	s_nop 0
	v_addc_co_u32_e32 v15, vcc, 0, v7, vcc
	v_add_co_u32_e32 v6, vcc, s1, v6
	s_mul_i32 s85, s33, 5
	s_nop 0
	v_addc_co_u32_e32 v7, vcc, 0, v7, vcc
	global_load_dwordx2 v[150:151], v[10:11], off
	global_load_dwordx2 v[148:149], v[12:13], off
	global_load_dwordx2 v[146:147], v[14:15], off
	global_load_dwordx2 v[144:145], v[6:7], off
	v_add_u32_e32 v7, s0, v2
	v_lshlrev_b32_e32 v2, 3, v0
	v_lshrrev_b32_e32 v6, 3, v254
	v_and_b32_e32 v2, 56, v2
	v_mul_u32_u24_e32 v9, 0x104, v2
	v_lshlrev_b32_e32 v10, 2, v6
	v_add3_u32 v152, s0, v9, v10
	v_lshlrev_b32_e32 v10, 11, v6
	s_add_u32 s86, s10, 0x590000
	v_mul_u32_u24_e32 v5, 0x104, v5
	v_or_b32_e32 v12, 0x4000, v10
	v_or_b32_e32 v14, 0x8000, v10
	v_or_b32_e32 v16, 0xc000, v10
	v_or_b32_e32 v18, 0x10000, v10
	v_or_b32_e32 v20, 0x14000, v10
	v_or_b32_e32 v22, 0x18000, v10
	v_or_b32_e32 v24, 0x1c000, v10
	s_addc_u32 s87, s11, 0
	s_lshl_b32 s93, s91, 6
	s_lshl_b32 s88, s85, 6
	v_lshlrev_b32_e32 v4, 2, v4
	v_lshlrev_b32_e32 v6, 2, v8
	v_add_u32_e32 v153, v7, v5
	v_lshlrev_b32_e32 v2, 1, v2
	s_movk_i32 s89, 0x7fff
	s_mov_b32 s90, 0xffff0000
	v_lshlrev_b32_e32 v8, 1, v10
	v_lshlrev_b32_e32 v10, 1, v12
	v_lshlrev_b32_e32 v12, 1, v14
	v_lshlrev_b32_e32 v14, 1, v16
	v_lshlrev_b32_e32 v16, 1, v18
	v_lshlrev_b32_e32 v18, 1, v20
	v_lshlrev_b32_e32 v20, 1, v22
	v_lshlrev_b32_e32 v22, 1, v24
	s_branch .LBB0_22

.LBB0_611:
	s_ashr_i32 s4, s2, 31
	s_lshr_b32 s4, s4, 26
	s_add_i32 s4, s2, s4
	s_ashr_i32 s4, s4, 6
	s_mul_hi_i32 s5, s4, 0xc000
	s_mul_i32 s4, s4, 0xc000
	s_add_u32 s4, s10, s4
	s_addc_u32 s5, s11, s5
	s_add_u32 s4, s4, 0x406000
	s_addc_u32 s5, s5, 0
	v_lshl_add_u64 v[2:3], s[4:5], 0, v[170:171]
	s_mov_b64 s[4:5], 0
	v_mov_b32_e32 v4, v184
	v_mov_b32_e32 v5, v183
	s_waitcnt vmcnt(0)
	s_barrier
	v_lshl_add_u64 v[14:15], v[2:3], 0, s[40:41]
	v_lshl_add_u64 v[14:15], v[14:15], 0, s[40:41]
	v_lshl_add_u64 v[16:17], v[14:15], 0, s[40:41]
	v_lshl_add_u64 v[16:17], v[16:17], 0, s[40:41]
	v_lshl_add_u64 v[18:19], v[16:17], 0, s[40:41]
	v_lshl_add_u64 v[18:19], v[18:19], 0, s[40:41]
	global_load_dword v6, v[2:3], off
	global_load_dword v7, v[2:3], off offset:2048
	global_load_dword v8, v[14:15], off
	global_load_dword v9, v[14:15], off offset:2048
	global_load_dword v10, v[16:17], off
	global_load_dword v11, v[16:17], off offset:2048
	global_load_dword v12, v[18:19], off
	global_load_dword v13, v[18:19], off offset:2048
	s_lshl_b32 s69, s2, 5
	s_add_i32 s46, s69, s50
	s_ashr_i32 s47, s46, 31
	s_lshl_b64 s[4:5], s[46:47], 13
	s_add_u32 s4, s3, s4
	s_addc_u32 s5, s43, s5
	s_add_u32 s6, s4, 0x400
	v_lshl_add_u64 v[2:3], s[4:5], 0, v[162:163]
	s_addc_u32 s7, s5, 0
	global_load_dwordx4 v[158:161], v[2:3], off
	v_lshl_add_u64 v[2:3], s[6:7], 0, v[162:163]
	global_load_dwordx4 v[154:157], v[2:3], off
	s_add_u32 s6, s4, 0x800
	s_addc_u32 s7, s5, 0
	v_lshl_add_u64 v[2:3], s[6:7], 0, v[162:163]
	s_add_u32 s6, s4, 0xc00
	s_addc_u32 s7, s5, 0
	global_load_dwordx4 v[150:153], v[2:3], off
	v_lshl_add_u64 v[2:3], s[6:7], 0, v[162:163]
	s_add_u32 s6, s4, 0x1000
	s_addc_u32 s7, s5, 0
	global_load_dwordx4 v[146:149], v[2:3], off
	v_lshl_add_u64 v[2:3], s[6:7], 0, v[162:163]
	global_load_dwordx4 v[142:145], v[2:3], off
	s_add_u32 s6, s4, 0x1400
	s_addc_u32 s7, s5, 0
	v_lshl_add_u64 v[2:3], s[6:7], 0, v[162:163]
	s_add_u32 s6, s4, 0x1800
	s_addc_u32 s7, s5, 0
	s_add_u32 s4, s4, 0x1c00
	global_load_dwordx4 v[138:141], v[2:3], off
	s_addc_u32 s5, s5, 0
	s_or_b32 s8, s46, 1
	v_lshl_add_u64 v[2:3], s[6:7], 0, v[162:163]
	s_ashr_i32 s9, s8, 31
	global_load_dwordx4 v[134:137], v[2:3], off
	v_lshl_add_u64 v[2:3], s[4:5], 0, v[162:163]
	s_lshl_b64 s[4:5], s[8:9], 13
	global_load_dwordx4 v[130:133], v[2:3], off
	s_add_u32 s4, s3, s4
	s_addc_u32 s5, s43, s5
	s_add_u32 s6, s4, 0x400
	v_lshl_add_u64 v[2:3], s[4:5], 0, v[162:163]
	s_addc_u32 s7, s5, 0
	global_load_dwordx4 v[126:129], v[2:3], off
	v_lshl_add_u64 v[2:3], s[6:7], 0, v[162:163]
	global_load_dwordx4 v[122:125], v[2:3], off
	s_add_u32 s6, s4, 0x800
	s_addc_u32 s7, s5, 0
	v_lshl_add_u64 v[2:3], s[6:7], 0, v[162:163]
	s_add_u32 s6, s4, 0xc00
	s_addc_u32 s7, s5, 0
	global_load_dwordx4 v[118:121], v[2:3], off
	v_lshl_add_u64 v[2:3], s[6:7], 0, v[162:163]
	s_add_u32 s6, s4, 0x1000
	s_addc_u32 s7, s5, 0
	global_load_dwordx4 v[114:117], v[2:3], off
	v_lshl_add_u64 v[2:3], s[6:7], 0, v[162:163]
	global_load_dwordx4 v[110:113], v[2:3], off
	s_add_u32 s6, s4, 0x1400
	s_addc_u32 s7, s5, 0
	v_lshl_add_u64 v[2:3], s[6:7], 0, v[162:163]
	s_add_u32 s6, s4, 0x1800
	s_addc_u32 s7, s5, 0
	global_load_dwordx4 v[106:109], v[2:3], off
	s_add_u32 s4, s4, 0x1c00
	v_lshl_add_u64 v[2:3], s[6:7], 0, v[162:163]
	s_addc_u32 s5, s5, 0
	global_load_dwordx4 v[102:105], v[2:3], off
	v_lshl_add_u64 v[2:3], s[4:5], 0, v[162:163]
	global_load_dwordx4 v[98:101], v[2:3], off
	s_or_b32 s6, s46, 2
	s_ashr_i32 s7, s6, 31
	s_lshl_b64 s[4:5], s[6:7], 13
	s_add_u32 s4, s3, s4
	s_addc_u32 s5, s43, s5
	s_add_u32 s34, s4, 0x400
	v_lshl_add_u64 v[2:3], s[4:5], 0, v[162:163]
	s_addc_u32 s35, s5, 0
	global_load_dwordx4 v[94:97], v[2:3], off
	v_lshl_add_u64 v[2:3], s[34:35], 0, v[162:163]
	s_add_u32 s34, s4, 0x800
	s_addc_u32 s35, s5, 0
	global_load_dwordx4 v[90:93], v[2:3], off
	v_lshl_add_u64 v[2:3], s[34:35], 0, v[162:163]
	s_add_u32 s34, s4, 0xc00
	s_addc_u32 s35, s5, 0
	global_load_dwordx4 v[86:89], v[2:3], off
	v_lshl_add_u64 v[2:3], s[34:35], 0, v[162:163]
	s_add_u32 s34, s4, 0x1000
	s_addc_u32 s35, s5, 0
	global_load_dwordx4 v[82:85], v[2:3], off
	v_lshl_add_u64 v[2:3], s[34:35], 0, v[162:163]
	s_add_u32 s34, s4, 0x1400
	s_addc_u32 s35, s5, 0
	global_load_dwordx4 v[78:81], v[2:3], off
	v_lshl_add_u64 v[2:3], s[34:35], 0, v[162:163]
	s_add_u32 s34, s4, 0x1800
	s_addc_u32 s35, s5, 0
	s_add_u32 s4, s4, 0x1c00
	global_load_dwordx4 v[74:77], v[2:3], off
	v_lshl_add_u64 v[2:3], s[34:35], 0, v[162:163]
	s_addc_u32 s5, s5, 0
	global_load_dwordx4 v[70:73], v[2:3], off
	v_lshl_add_u64 v[2:3], s[4:5], 0, v[162:163]
	s_or_b32 s4, s46, 3
	s_ashr_i32 s5, s4, 31
	s_lshl_b64 s[34:35], s[4:5], 13
	s_add_u32 s34, s3, s34
	v_cmp_lt_i32_e32 vcc, v192, v191
	s_addc_u32 s35, s43, s35
	s_waitcnt vmcnt(23)
	v_add_f32_e32 v10, 1.0, v10
	v_add_f32_e32 v11, 1.0, v11
	v_add_f32_e32 v12, 1.0, v12
	v_add_f32_e32 v13, 1.0, v13
	ds_write2st64_b32 v5, v10, v6 offset1:32
	ds_write2st64_b32 v5, v11, v7 offset0:8 offset1:40
	ds_write2st64_b32 v5, v12, v8 offset0:16 offset1:48
	ds_write2st64_b32 v5, v13, v9 offset0:24 offset1:56
	s_waitcnt lgkmcnt(0)
	s_barrier
	s_waitcnt vmcnt(22)
	v_mov_b32_e32 v174, v159
	v_cndmask_b32_e32 v60, v190, v192, vcc
	s_waitcnt vmcnt(21)
	v_mov_b32_e32 v175, v155
	s_add_u32 s60, s34, 0x400
	v_lshlrev_b32_e32 v164, 2, v60
	v_mov_b32_e32 v60, v158
	v_mov_b32_e32 v61, v154
	v_pk_mul_f32 v[174:175], v[174:175], v[174:175]
	v_mov_b32_e32 v176, v161
	v_mov_b32_e32 v177, v157
	global_load_dwordx4 v[66:69], v[2:3], off
	v_lshl_add_u64 v[2:3], s[34:35], 0, v[162:163]
	s_addc_u32 s61, s35, 0
	v_pk_fma_f32 v[60:61], v[60:61], v[60:61], v[174:175]
	v_mov_b32_e32 v174, v160
	v_mov_b32_e32 v175, v156
	v_pk_mul_f32 v[176:177], v[176:177], v[176:177]
	global_load_dwordx4 v[50:53], v[2:3], off
	v_lshl_add_u64 v[2:3], s[60:61], 0, v[162:163]
	s_add_u32 s60, s34, 0x800
	v_pk_fma_f32 v[174:175], v[174:175], v[174:175], v[176:177]
	s_addc_u32 s61, s35, 0
	v_pk_add_f32 v[60:61], v[60:61], v[174:175]
	s_waitcnt vmcnt(22)
	v_pk_mul_f32 v[174:175], v[152:153], v[152:153]
	v_pk_mul_f32 v[176:177], v[150:151], v[150:151]
	global_load_dwordx4 v[42:45], v[2:3], off
	v_lshl_add_u64 v[2:3], s[60:61], 0, v[162:163]
	s_add_u32 s60, s34, 0xc00
	v_pk_mov_b32 v[178:179], v[176:177], v[174:175] op_sel:[1,0]
	v_mov_b32_e32 v177, v175
	s_addc_u32 s61, s35, 0
	v_pk_add_f32 v[174:175], v[178:179], v[176:177]
	global_load_dwordx4 v[34:37], v[2:3], off
	v_lshl_add_u64 v[2:3], s[60:61], 0, v[162:163]
	s_add_u32 s60, s34, 0x1000
	s_waitcnt vmcnt(22)
	v_mul_f32_e32 v176, v142, v142
	v_mul_f32_e32 v177, v143, v143
	v_pk_add_f32 v[60:61], v[60:61], v[60:61] op_sel:[0,1] op_sel_hi:[1,0]
	v_pk_add_f32 v[174:175], v[174:175], v[174:175] op_sel:[0,1] op_sel_hi:[1,0]
	s_addc_u32 s61, s35, 0
	v_mov_b32_e32 v61, v176
	v_mov_b32_e32 v175, v177
	global_load_dwordx4 v[26:29], v[2:3], off
	v_lshl_add_u64 v[2:3], s[60:61], 0, v[162:163]
	s_add_u32 s60, s34, 0x1400
	v_pk_add_f32 v[60:61], v[60:61], v[174:175]
	v_mul_f32_e32 v174, v147, v147
	v_mul_f32_e32 v176, v149, v149
	s_addc_u32 s61, s35, 0
	v_mul_f32_e32 v178, v144, v144
	v_mul_f32_e32 v179, v145, v145
	v_pk_fma_f32 v[174:175], v[146:147], v[146:147], v[174:175] op_sel_hi:[1,1,0]
	v_pk_fma_f32 v[176:177], v[148:149], v[148:149], v[176:177] op_sel_hi:[1,1,0]
	global_load_dwordx4 v[18:21], v[2:3], off
	v_lshl_add_u64 v[2:3], s[60:61], 0, v[162:163]
	s_add_u32 s60, s34, 0x1800
	v_lshl_add_u64 v[14:15], s[16:17], 0, v[162:163]
	v_mov_b32_e32 v175, v178
	v_mov_b32_e32 v177, v179
	s_addc_u32 s61, s35, 0
	global_load_dwordx4 v[62:65], v[14:15], off
	v_pk_add_f32 v[174:175], v[174:175], v[176:177]
	s_add_u32 s34, s34, 0x1c00
	v_pk_add_f32 v[60:61], v[60:61], v[174:175]
	s_waitcnt vmcnt(24)
	v_pk_mul_f32 v[174:175], v[140:141], v[140:141]
	v_pk_mul_f32 v[176:177], v[138:139], v[138:139]
	global_load_dwordx4 v[10:13], v[2:3], off
	v_lshl_add_u64 v[2:3], s[60:61], 0, v[162:163]
	s_addc_u32 s35, s35, 0
	v_pk_mov_b32 v[178:179], v[176:177], v[174:175] op_sel:[1,0]
	v_mov_b32_e32 v177, v175
	global_load_dwordx4 v[6:9], v[2:3], off
	v_lshl_add_u64 v[2:3], s[34:35], 0, v[162:163]
	s_add_u32 s34, s16, 0x400
	v_pk_add_f32 v[174:175], v[178:179], v[176:177]
	s_addc_u32 s35, s17, 0
	s_waitcnt vmcnt(24)
	v_mul_f32_e32 v176, v130, v130
	v_mul_f32_e32 v177, v131, v131
	v_pk_add_f32 v[60:61], v[60:61], v[60:61] op_sel:[0,1] op_sel_hi:[1,0]
	v_pk_add_f32 v[174:175], v[174:175], v[174:175] op_sel:[0,1] op_sel_hi:[1,0]
	v_lshl_add_u64 v[14:15], s[34:35], 0, v[162:163]
	v_mov_b32_e32 v61, v176
	v_mov_b32_e32 v175, v177
	global_load_dwordx4 v[54:57], v[14:15], off
	v_pk_add_f32 v[60:61], v[60:61], v[174:175]
	v_mul_f32_e32 v174, v135, v135
	v_mul_f32_e32 v176, v137, v137
	v_mul_f32_e32 v178, v132, v132
	v_mul_f32_e32 v179, v133, v133
	v_pk_fma_f32 v[174:175], v[134:135], v[134:135], v[174:175] op_sel_hi:[1,1,0]
	v_pk_fma_f32 v[176:177], v[136:137], v[136:137], v[176:177] op_sel_hi:[1,1,0]
	v_mov_b32_e32 v175, v178
	v_mov_b32_e32 v177, v179
	s_add_u32 s34, s16, 0x800
	v_pk_add_f32 v[174:175], v[174:175], v[176:177]
	s_waitcnt vmcnt(24)
	v_mov_b32_e32 v176, v127
	s_waitcnt vmcnt(23)
	v_mov_b32_e32 v177, v123
	s_addc_u32 s35, s17, 0
	v_pk_add_f32 v[60:61], v[60:61], v[174:175]
	v_mov_b32_e32 v174, v126
	v_mov_b32_e32 v175, v122
	v_pk_mul_f32 v[176:177], v[176:177], v[176:177]
	v_mov_b32_e32 v178, v129
	v_mov_b32_e32 v179, v125
	v_lshl_add_u64 v[14:15], s[34:35], 0, v[162:163]
	v_pk_fma_f32 v[174:175], v[174:175], v[174:175], v[176:177]
	v_mov_b32_e32 v176, v128
	v_mov_b32_e32 v177, v124
	v_pk_mul_f32 v[178:179], v[178:179], v[178:179]
	global_load_dwordx4 v[46:49], v[14:15], off
	v_pk_fma_f32 v[176:177], v[176:177], v[176:177], v[178:179]
	s_waitcnt vmcnt(23)
	v_pk_mul_f32 v[178:179], v[118:119], v[118:119]
	v_pk_add_f32 v[174:175], v[174:175], v[176:177]
	v_pk_mul_f32 v[176:177], v[120:121], v[120:121]
	v_pk_add_f32 v[174:175], v[174:175], v[174:175] op_sel:[0,1] op_sel_hi:[1,0]
	v_pk_mov_b32 v[180:181], v[178:179], v[176:177] op_sel:[1,0]
	v_mov_b32_e32 v179, v177
	v_pk_add_f32 v[176:177], v[180:181], v[178:179]
	s_waitcnt vmcnt(21)
	v_mul_f32_e32 v178, v110, v110
	v_mul_f32_e32 v179, v111, v111
	v_pk_add_f32 v[176:177], v[176:177], v[176:177] op_sel:[0,1] op_sel_hi:[1,0]
	v_mov_b32_e32 v175, v178
	v_mov_b32_e32 v177, v179
	s_add_u32 s34, s16, 0xc00
	v_pk_add_f32 v[174:175], v[174:175], v[176:177]
	v_mul_f32_e32 v176, v115, v115
	v_mul_f32_e32 v178, v117, v117
	s_addc_u32 s35, s17, 0
	v_mul_f32_e32 v180, v112, v112
	v_mul_f32_e32 v181, v113, v113
	v_pk_fma_f32 v[176:177], v[114:115], v[114:115], v[176:177] op_sel_hi:[1,1,0]
	v_pk_fma_f32 v[178:179], v[116:117], v[116:117], v[178:179] op_sel_hi:[1,1,0]
	v_lshl_add_u64 v[14:15], s[34:35], 0, v[162:163]
	v_mov_b32_e32 v177, v180
	v_mov_b32_e32 v179, v181
	global_load_dwordx4 v[38:41], v[14:15], off
	v_pk_add_f32 v[176:177], v[176:177], v[178:179]
	s_waitcnt vmcnt(21)
	v_pk_mul_f32 v[178:179], v[106:107], v[106:107]
	v_pk_add_f32 v[174:175], v[174:175], v[176:177]
	v_pk_mul_f32 v[176:177], v[108:109], v[108:109]
	v_pk_add_f32 v[174:175], v[174:175], v[174:175] op_sel:[0,1] op_sel_hi:[1,0]
	v_pk_mov_b32 v[180:181], v[178:179], v[176:177] op_sel:[1,0]
	v_mov_b32_e32 v179, v177
	v_pk_add_f32 v[176:177], v[180:181], v[178:179]
	s_waitcnt vmcnt(19)
	v_mul_f32_e32 v178, v98, v98
	v_mul_f32_e32 v179, v99, v99
	v_pk_add_f32 v[176:177], v[176:177], v[176:177] op_sel:[0,1] op_sel_hi:[1,0]
	v_mov_b32_e32 v175, v178
	v_mov_b32_e32 v177, v179
	s_add_u32 s34, s16, 0x1000
	v_pk_add_f32 v[174:175], v[174:175], v[176:177]
	v_mul_f32_e32 v176, v103, v103
	v_mul_f32_e32 v178, v105, v105
	s_addc_u32 s35, s17, 0
	v_mul_f32_e32 v180, v100, v100
	v_mul_f32_e32 v181, v101, v101
	v_pk_fma_f32 v[176:177], v[102:103], v[102:103], v[176:177] op_sel_hi:[1,1,0]
	v_pk_fma_f32 v[178:179], v[104:105], v[104:105], v[178:179] op_sel_hi:[1,1,0]
	v_lshl_add_u64 v[14:15], s[34:35], 0, v[162:163]
	v_mov_b32_e32 v177, v180
	v_mov_b32_e32 v179, v181
	global_load_dwordx4 v[30:33], v[14:15], off
	v_pk_add_f32 v[176:177], v[176:177], v[178:179]
	s_add_u32 s34, s16, 0x1400
	v_pk_add_f32 v[174:175], v[174:175], v[176:177]
	v_mov_b32_e32 v177, v60
	v_mov_b32_e32 v176, v174
	v_mov_b32_e32 v60, v175
	v_pk_add_f32 v[174:175], v[176:177], v[60:61]
	ds_bpermute_b32 v177, v164, v175
	ds_bpermute_b32 v176, v164, v174
	s_addc_u32 s35, s17, 0
	v_cmp_lt_i32_e32 vcc, v193, v191
	v_lshl_add_u64 v[14:15], s[34:35], 0, v[162:163]
	global_load_dwordx4 v[22:25], v[14:15], off
	v_cndmask_b32_e32 v178, v190, v193, vcc
	v_lshlrev_b32_e32 v180, 2, v178
	s_waitcnt lgkmcnt(0)
	v_pk_add_f32 v[174:175], v[174:175], v[176:177]
	ds_bpermute_b32 v177, v180, v175
	ds_bpermute_b32 v176, v180, v174
	v_cmp_lt_i32_e32 vcc, v194, v191
	s_add_u32 s34, s16, 0x1800
	s_addc_u32 s35, s17, 0
	v_cndmask_b32_e32 v178, v190, v194, vcc
	v_lshlrev_b32_e32 v181, 2, v178
	s_waitcnt lgkmcnt(0)
	v_pk_add_f32 v[174:175], v[174:175], v[176:177]
	ds_bpermute_b32 v177, v181, v175
	ds_bpermute_b32 v176, v181, v174
	v_lshl_add_u64 v[14:15], s[34:35], 0, v[162:163]
	global_load_dwordx4 v[14:17], v[14:15], off
	v_cmp_lt_i32_e32 vcc, v195, v191
	s_add_u32 s34, s16, 0x1c00
	s_waitcnt lgkmcnt(0)
	v_pk_add_f32 v[174:175], v[174:175], v[176:177]
	v_cndmask_b32_e32 v178, v190, v195, vcc
	v_lshlrev_b32_e32 v206, 2, v178
	ds_bpermute_b32 v177, v206, v175
	ds_bpermute_b32 v176, v206, v174
	s_addc_u32 s35, s17, 0
	v_cmp_lt_i32_e32 vcc, v196, v191
	v_lshl_add_u64 v[58:59], s[34:35], 0, v[162:163]
	global_load_dwordx4 v[58:61], v[58:59], off
	v_cndmask_b32_e32 v178, v190, v196, vcc
	v_lshlrev_b32_e32 v178, 2, v178
	s_waitcnt lgkmcnt(0)
	v_pk_add_f32 v[174:175], v[174:175], v[176:177]
	ds_bpermute_b32 v217, v178, v175
	ds_bpermute_b32 v216, v178, v174
	v_cmp_lt_i32_e32 vcc, v197, v191
	global_load_dwordx4 v[2:5], v[2:3], off
	ds_read_b128 v[208:211], v1
	ds_read_b128 v[212:215], v1 offset:1024
	v_cndmask_b32_e32 v179, v190, v197, vcc
	v_lshlrev_b32_e32 v179, 2, v179
	s_waitcnt lgkmcnt(2)
	v_pk_add_f32 v[174:175], v[174:175], v[216:217]
	ds_bpermute_b32 v221, v179, v175
	ds_bpermute_b32 v220, v179, v174
	ds_read_b128 v[216:219], v1 offset:8192
	ds_read_b128 v[224:227], v1 offset:9216
	ds_read_b128 v[228:231], v1 offset:2048
	ds_read_b128 v[232:235], v1 offset:3072
	s_lshl_b64 s[34:35], s[46:47], 12
	s_add_u32 s34, s48, s34
	s_addc_u32 s35, s49, s35
	s_waitcnt lgkmcnt(4)
	v_pk_add_f32 v[174:175], v[174:175], v[220:221]
	v_lshl_add_u64 v[176:177], s[34:35], 0, v[166:167]
	v_pk_fma_f32 v[174:175], v[174:175], s[42:43], v[172:173] op_sel_hi:[1,0,0]
	ds_read_b128 v[236:239], v1 offset:10240
	ds_read_b128 v[240:243], v1 offset:11264
	ds_read_b128 v[244:247], v1 offset:4096
	ds_read_b128 v[248:251], v1 offset:5120
	v_mul_f32_e32 v207, 0x4b800000, v175
	v_cmp_gt_f32_e32 vcc, s63, v175
	s_lshl_b64 s[8:9], s[8:9], 12
	s_add_u32 s8, s48, s8
	v_cndmask_b32_e32 v175, v175, v207, vcc
	v_rsq_f32_e32 v175, v175
	s_addc_u32 s9, s49, s9
	s_lshl_b64 s[6:7], s[6:7], 12
	s_add_u32 s6, s48, s6
	v_mul_f32_e32 v207, 0x45800000, v175
	v_cndmask_b32_e32 v220, v175, v207, vcc
	v_pk_mul_f32 v[158:159], v[158:159], v[220:221] op_sel_hi:[1,0]
	v_pk_mul_f32 v[160:161], v[160:161], v[220:221] op_sel_hi:[1,0]
	s_waitcnt vmcnt(10)
	v_pk_mul_f32 v[252:253], v[62:63], v[158:159]
	v_pk_mul_f32 v[158:159], v[64:65], v[160:161]
	s_waitcnt lgkmcnt(7)
	v_pk_fma_f32 v[160:161], v[208:209], v[252:253], v[216:217]
	v_pk_fma_f32 v[158:159], v[210:211], v[158:159], v[218:219]
	v_bfe_u32 v175, v160, 16, 1
	v_add3_u32 v175, v160, v175, s64
	v_bfe_u32 v207, v161, 16, 1
	v_lshrrev_b32_e32 v175, 16, v175
	v_add3_u32 v207, v161, v207, s64
	v_and_or_b32 v252, v207, s65, v175
	v_bfe_u32 v175, v158, 16, 1
	v_pk_mul_f32 v[154:155], v[154:155], v[220:221] op_sel_hi:[1,0]
	v_add3_u32 v175, v158, v175, s64
	v_bfe_u32 v207, v159, 16, 1
	v_pk_mul_f32 v[156:157], v[156:157], v[220:221] op_sel_hi:[1,0]
	s_waitcnt vmcnt(7)
	v_pk_mul_f32 v[222:223], v[54:55], v[154:155]
	v_lshrrev_b32_e32 v175, 16, v175
	v_add3_u32 v207, v159, v207, s64
	v_pk_mul_f32 v[154:155], v[56:57], v[156:157]
	s_waitcnt lgkmcnt(6)
	v_pk_fma_f32 v[156:157], v[212:213], v[222:223], v[224:225]
	v_and_or_b32 v253, v207, s65, v175
	v_bfe_u32 v175, v156, 16, 1
	v_add3_u32 v175, v156, v175, s64
	v_bfe_u32 v207, v157, 16, 1
	v_pk_fma_f32 v[154:155], v[214:215], v[154:155], v[226:227]
	v_lshrrev_b32_e32 v175, 16, v175
	v_add3_u32 v207, v157, v207, s64
	v_and_or_b32 v222, v207, s65, v175
	v_bfe_u32 v175, v154, 16, 1
	v_pk_mul_f32 v[150:151], v[150:151], v[220:221] op_sel_hi:[1,0]
	ds_read_b128 v[208:211], v1 offset:12288
	ds_read_b128 v[216:219], v1 offset:13312
	global_store_dwordx2 v[176:177], v[252:253], off
	v_add3_u32 v175, v154, v175, s64
	v_bfe_u32 v207, v155, 16, 1
	v_pk_mul_f32 v[152:153], v[152:153], v[220:221] op_sel_hi:[1,0]
	s_waitcnt vmcnt(7)
	v_pk_mul_f32 v[252:253], v[46:47], v[150:151]
	v_lshrrev_b32_e32 v175, 16, v175
	v_add3_u32 v207, v155, v207, s64
	v_pk_mul_f32 v[150:151], v[48:49], v[152:153]
	s_waitcnt lgkmcnt(5)
	v_pk_fma_f32 v[152:153], v[228:229], v[252:253], v[236:237]
	v_and_or_b32 v223, v207, s65, v175
	v_bfe_u32 v175, v152, 16, 1
	v_add3_u32 v175, v152, v175, s64
	v_bfe_u32 v207, v153, 16, 1
	v_pk_fma_f32 v[150:151], v[230:231], v[150:151], v[238:239]
	v_lshrrev_b32_e32 v175, 16, v175
	v_add3_u32 v207, v153, v207, s64
	ds_read_b128 v[212:215], v1 offset:6144
	ds_read_b128 v[224:227], v1 offset:7168
	global_store_dwordx2 v[176:177], v[222:223], off offset:512
	v_and_or_b32 v222, v207, s65, v175
	v_bfe_u32 v175, v150, 16, 1
	v_add3_u32 v175, v150, v175, s64
	v_bfe_u32 v207, v151, 16, 1
	v_lshrrev_b32_e32 v175, 16, v175
	v_add3_u32 v207, v151, v207, s64
	v_and_or_b32 v223, v207, s65, v175
	v_pk_mul_f32 v[146:147], v[146:147], v[220:221] op_sel_hi:[1,0]
	ds_read_b128 v[228:231], v1 offset:14336
	ds_read_b128 v[236:239], v1 offset:15360
	global_store_dwordx2 v[176:177], v[222:223], off offset:1024
	v_pk_mul_f32 v[148:149], v[148:149], v[220:221] op_sel_hi:[1,0]
	s_waitcnt vmcnt(8)
	v_pk_mul_f32 v[222:223], v[38:39], v[146:147]
	v_pk_mul_f32 v[146:147], v[40:41], v[148:149]
	s_waitcnt lgkmcnt(8)
	v_pk_fma_f32 v[148:149], v[232:233], v[222:223], v[240:241]
	v_pk_fma_f32 v[146:147], v[234:235], v[146:147], v[242:243]
	v_bfe_u32 v175, v148, 16, 1
	v_add3_u32 v175, v148, v175, s64
	v_bfe_u32 v207, v149, 16, 1
	v_lshrrev_b32_e32 v175, 16, v175
	v_add3_u32 v207, v149, v207, s64
	v_and_or_b32 v222, v207, s65, v175
	v_bfe_u32 v175, v146, 16, 1
	v_add3_u32 v175, v146, v175, s64
	v_bfe_u32 v207, v147, 16, 1
	v_lshrrev_b32_e32 v175, 16, v175
	v_add3_u32 v207, v147, v207, s64
	v_and_or_b32 v223, v207, s65, v175
	v_pk_mul_f32 v[142:143], v[142:143], v[220:221] op_sel_hi:[1,0]
	global_store_dwordx2 v[176:177], v[222:223], off offset:1536
	v_pk_mul_f32 v[144:145], v[144:145], v[220:221] op_sel_hi:[1,0]
	s_waitcnt vmcnt(8)
	v_pk_mul_f32 v[222:223], v[30:31], v[142:143]
	v_pk_mul_f32 v[142:143], v[32:33], v[144:145]
	s_waitcnt lgkmcnt(5)
	v_pk_fma_f32 v[144:145], v[222:223], v[244:245], v[208:209]
	v_pk_fma_f32 v[142:143], v[142:143], v[246:247], v[210:211]
	v_bfe_u32 v175, v144, 16, 1
	v_add3_u32 v175, v144, v175, s64
	v_bfe_u32 v207, v145, 16, 1
	v_lshrrev_b32_e32 v175, 16, v175
	v_add3_u32 v207, v145, v207, s64
	v_and_or_b32 v208, v207, s65, v175
	v_bfe_u32 v175, v142, 16, 1
	v_add3_u32 v175, v142, v175, s64
	v_bfe_u32 v207, v143, 16, 1
	v_lshrrev_b32_e32 v175, 16, v175
	v_add3_u32 v207, v143, v207, s64
	v_and_or_b32 v209, v207, s65, v175
	v_pk_mul_f32 v[138:139], v[138:139], v[220:221] op_sel_hi:[1,0]
	global_store_dwordx2 v[176:177], v[208:209], off offset:2048
	v_pk_mul_f32 v[140:141], v[140:141], v[220:221] op_sel_hi:[1,0]
	s_waitcnt vmcnt(8)
	v_pk_mul_f32 v[208:209], v[22:23], v[138:139]
	v_pk_mul_f32 v[138:139], v[24:25], v[140:141]
	s_waitcnt lgkmcnt(4)
	v_pk_fma_f32 v[140:141], v[208:209], v[248:249], v[216:217]
	v_pk_fma_f32 v[138:139], v[138:139], v[250:251], v[218:219]
	v_bfe_u32 v175, v140, 16, 1
	v_add3_u32 v175, v140, v175, s64
	v_bfe_u32 v207, v141, 16, 1
	v_lshrrev_b32_e32 v175, 16, v175
	v_add3_u32 v207, v141, v207, s64
	v_and_or_b32 v208, v207, s65, v175
	v_bfe_u32 v175, v138, 16, 1
	v_add3_u32 v175, v138, v175, s64
	v_bfe_u32 v207, v139, 16, 1
	v_lshrrev_b32_e32 v175, 16, v175
	v_add3_u32 v207, v139, v207, s64
	v_and_or_b32 v209, v207, s65, v175
	v_pk_mul_f32 v[134:135], v[134:135], v[220:221] op_sel_hi:[1,0]
	global_store_dwordx2 v[176:177], v[208:209], off offset:2560
	v_pk_mul_f32 v[136:137], v[136:137], v[220:221] op_sel_hi:[1,0]
	s_waitcnt vmcnt(8)
	v_pk_mul_f32 v[208:209], v[14:15], v[134:135]
	v_pk_mul_f32 v[134:135], v[16:17], v[136:137]
	s_waitcnt lgkmcnt(1)
	v_pk_fma_f32 v[136:137], v[208:209], v[212:213], v[228:229]
	v_pk_fma_f32 v[134:135], v[134:135], v[214:215], v[230:231]
	v_bfe_u32 v175, v136, 16, 1
	v_add3_u32 v175, v136, v175, s64
	v_bfe_u32 v207, v137, 16, 1
	v_lshrrev_b32_e32 v175, 16, v175
	v_add3_u32 v207, v137, v207, s64
	v_and_or_b32 v208, v207, s65, v175
	v_bfe_u32 v175, v134, 16, 1
	v_add3_u32 v175, v134, v175, s64
	v_bfe_u32 v207, v135, 16, 1
	v_lshrrev_b32_e32 v175, 16, v175
	v_add3_u32 v207, v135, v207, s64
	v_and_or_b32 v209, v207, s65, v175
	v_pk_mul_f32 v[130:131], v[130:131], v[220:221] op_sel_hi:[1,0]
	global_store_dwordx2 v[176:177], v[208:209], off offset:3072
	v_pk_mul_f32 v[132:133], v[132:133], v[220:221] op_sel_hi:[1,0]
	s_waitcnt vmcnt(8)
	v_pk_mul_f32 v[208:209], v[58:59], v[130:131]
	v_pk_mul_f32 v[130:131], v[60:61], v[132:133]
	s_waitcnt lgkmcnt(0)
	v_pk_fma_f32 v[132:133], v[208:209], v[224:225], v[236:237]
	v_pk_fma_f32 v[130:131], v[130:131], v[226:227], v[238:239]
	v_bfe_u32 v175, v132, 16, 1
	v_add3_u32 v175, v132, v175, s64
	v_bfe_u32 v207, v133, 16, 1
	v_lshrrev_b32_e32 v175, 16, v175
	v_add3_u32 v207, v133, v207, s64
	v_and_or_b32 v208, v207, s65, v175
	v_bfe_u32 v175, v130, 16, 1
	v_add3_u32 v175, v130, v175, s64
	v_bfe_u32 v207, v131, 16, 1
	v_lshrrev_b32_e32 v175, 16, v175
	v_add3_u32 v207, v131, v207, s64
	v_and_or_b32 v209, v207, s65, v175
	v_and_b32_sdwa v207, v160, v202 dst_sel:DWORD dst_unused:UNUSED_PAD src0_sel:WORD_1 src1_sel:DWORD
	global_store_dwordx2 v[176:177], v[208:209], off offset:3584
	v_mov_b32_e32 v176, v160
	v_and_b32_sdwa v175, v158, v202 dst_sel:DWORD dst_unused:UNUSED_PAD src0_sel:WORD_1 src1_sel:DWORD
	v_add3_u32 v207, v160, v207, s64
	v_and_b32_sdwa v160, v159, v202 dst_sel:DWORD dst_unused:UNUSED_PAD src0_sel:WORD_1 src1_sel:DWORD
	v_and_b32_sdwa v208, v161, v202 dst_sel:DWORD dst_unused:UNUSED_PAD src0_sel:WORD_1 src1_sel:DWORD
	v_add3_u32 v175, v158, v175, s64
	v_add3_u32 v160, v159, v160, s64
	v_add3_u32 v208, v161, v208, s64
	v_mov_b32_e32 v177, v158
	v_mov_b32_e32 v158, v161
	v_and_b32_e32 v161, 0xffff0000, v160
	v_and_b32_e32 v160, 0xffff0000, v208
	v_and_b32_e32 v209, 0xffff0000, v175
	v_and_b32_e32 v208, 0xffff0000, v207
	v_pk_add_f32 v[176:177], v[176:177], v[208:209] neg_lo:[0,1] neg_hi:[0,1]
	v_pk_add_f32 v[158:159], v[158:159], v[160:161] neg_lo:[0,1] neg_hi:[0,1]
	v_or_b32_sdwa v160, v207, v160 dst_sel:DWORD dst_unused:UNUSED_PAD src0_sel:WORD_1 src1_sel:DWORD
	v_or_b32_sdwa v161, v175, v161 dst_sel:DWORD dst_unused:UNUSED_PAD src0_sel:WORD_1 src1_sel:DWORD
	v_and_b32_sdwa v175, v177, v202 dst_sel:DWORD dst_unused:UNUSED_PAD src0_sel:WORD_1 src1_sel:DWORD
	v_and_b32_sdwa v207, v176, v202 dst_sel:DWORD dst_unused:UNUSED_PAD src0_sel:WORD_1 src1_sel:DWORD
	v_add3_u32 v176, v176, v207, s64
	v_add3_u32 v175, v177, v175, s64
	v_and_b32_sdwa v177, v159, v202 dst_sel:DWORD dst_unused:UNUSED_PAD src0_sel:WORD_1 src1_sel:DWORD
	v_and_b32_sdwa v207, v158, v202 dst_sel:DWORD dst_unused:UNUSED_PAD src0_sel:WORD_1 src1_sel:DWORD
	v_add3_u32 v159, v159, v177, s64
	v_add3_u32 v158, v158, v207, s64
	v_and_b32_e32 v159, 0xffff0000, v159
	v_and_b32_e32 v158, 0xffff0000, v158
	v_and_b32_sdwa v207, v156, v202 dst_sel:DWORD dst_unused:UNUSED_PAD src0_sel:WORD_1 src1_sel:DWORD
	v_or_b32_sdwa v159, v159, v175 dst_sel:DWORD dst_unused:UNUSED_PAD src0_sel:DWORD src1_sel:WORD_1
	v_or_b32_sdwa v158, v158, v176 dst_sel:DWORD dst_unused:UNUSED_PAD src0_sel:DWORD src1_sel:WORD_1
	v_mov_b32_e32 v176, v156
	v_and_b32_sdwa v175, v154, v202 dst_sel:DWORD dst_unused:UNUSED_PAD src0_sel:WORD_1 src1_sel:DWORD
	v_add3_u32 v207, v156, v207, s64
	v_and_b32_sdwa v156, v155, v202 dst_sel:DWORD dst_unused:UNUSED_PAD src0_sel:WORD_1 src1_sel:DWORD
	v_and_b32_sdwa v208, v157, v202 dst_sel:DWORD dst_unused:UNUSED_PAD src0_sel:WORD_1 src1_sel:DWORD
	v_add3_u32 v175, v154, v175, s64
	v_add3_u32 v156, v155, v156, s64
	v_add3_u32 v208, v157, v208, s64
	v_mov_b32_e32 v177, v154
	v_mov_b32_e32 v154, v157
	v_and_b32_e32 v157, 0xffff0000, v156
	v_and_b32_e32 v156, 0xffff0000, v208
	v_and_b32_e32 v209, 0xffff0000, v175
	v_and_b32_e32 v208, 0xffff0000, v207
	v_pk_add_f32 v[176:177], v[176:177], v[208:209] neg_lo:[0,1] neg_hi:[0,1]
	v_pk_add_f32 v[154:155], v[154:155], v[156:157] neg_lo:[0,1] neg_hi:[0,1]
	v_or_b32_sdwa v157, v175, v157 dst_sel:DWORD dst_unused:UNUSED_PAD src0_sel:WORD_1 src1_sel:DWORD
	v_and_b32_sdwa v175, v177, v202 dst_sel:DWORD dst_unused:UNUSED_PAD src0_sel:WORD_1 src1_sel:DWORD
	v_add3_u32 v175, v177, v175, s64
	v_and_b32_sdwa v177, v155, v202 dst_sel:DWORD dst_unused:UNUSED_PAD src0_sel:WORD_1 src1_sel:DWORD
	v_add3_u32 v155, v155, v177, s64
	v_and_b32_e32 v155, 0xffff0000, v155
	v_or_b32_sdwa v155, v155, v175 dst_sel:DWORD dst_unused:UNUSED_PAD src0_sel:DWORD src1_sel:WORD_1
	v_mul_f32_e32 v175, 0x4b800000, v174
	v_cmp_gt_f32_e32 vcc, s63, v174
	v_or_b32_sdwa v156, v207, v156 dst_sel:DWORD dst_unused:UNUSED_PAD src0_sel:WORD_1 src1_sel:DWORD
	v_and_b32_sdwa v207, v176, v202 dst_sel:DWORD dst_unused:UNUSED_PAD src0_sel:WORD_1 src1_sel:DWORD
	v_cndmask_b32_e32 v174, v174, v175, vcc
	v_add3_u32 v176, v176, v207, s64
	v_and_b32_sdwa v207, v154, v202 dst_sel:DWORD dst_unused:UNUSED_PAD src0_sel:WORD_1 src1_sel:DWORD
	v_rsq_f32_e32 v174, v174
	v_add3_u32 v154, v154, v207, s64
	v_and_b32_e32 v154, 0xffff0000, v154
	v_or_b32_sdwa v154, v154, v176 dst_sel:DWORD dst_unused:UNUSED_PAD src0_sel:DWORD src1_sel:WORD_1
	ds_write2st64_b64 v198, v[160:161], v[156:157] offset0:32 offset1:33
	ds_write2st64_b64 v198, v[158:159], v[154:155] offset0:97 offset1:98
	v_mul_f32_e32 v154, 0x45800000, v174
	v_cndmask_b32_e32 v156, v174, v154, vcc
	ds_read_b128 v[158:161], v1
	ds_read_b128 v[174:177], v1 offset:8192
	v_pk_mul_f32 v[126:127], v[126:127], v[156:157] op_sel_hi:[1,0]
	v_pk_mul_f32 v[128:129], v[128:129], v[156:157] op_sel_hi:[1,0]
	v_pk_mul_f32 v[216:217], v[62:63], v[126:127]
	v_pk_mul_f32 v[126:127], v[64:65], v[128:129]
	s_waitcnt lgkmcnt(0)
	v_pk_fma_f32 v[128:129], v[158:159], v[216:217], v[174:175]
	v_pk_fma_f32 v[126:127], v[160:161], v[126:127], v[176:177]
	v_bfe_u32 v157, v128, 16, 1
	v_add3_u32 v157, v128, v157, s64
	v_bfe_u32 v158, v129, 16, 1
	v_lshrrev_b32_e32 v157, 16, v157
	v_add3_u32 v158, v129, v158, s64
	ds_read_b128 v[208:211], v1 offset:1024
	ds_read_b128 v[212:215], v1 offset:9216
	v_and_or_b32 v158, v158, s65, v157
	v_bfe_u32 v157, v126, 16, 1
	v_add3_u32 v157, v126, v157, s64
	v_bfe_u32 v159, v127, 16, 1
	v_lshrrev_b32_e32 v157, 16, v157
	v_add3_u32 v159, v127, v159, s64
	v_lshl_add_u64 v[154:155], s[8:9], 0, v[166:167]
	v_and_or_b32 v159, v159, s65, v157
	v_pk_mul_f32 v[122:123], v[122:123], v[156:157] op_sel_hi:[1,0]
	global_store_dwordx2 v[154:155], v[158:159], off
	v_pk_mul_f32 v[124:125], v[124:125], v[156:157] op_sel_hi:[1,0]
	v_pk_mul_f32 v[158:159], v[54:55], v[122:123]
	v_pk_mul_f32 v[122:123], v[56:57], v[124:125]
	s_waitcnt lgkmcnt(0)
	v_pk_fma_f32 v[124:125], v[208:209], v[158:159], v[212:213]
	v_pk_fma_f32 v[122:123], v[210:211], v[122:123], v[214:215]
	v_bfe_u32 v157, v124, 16, 1
	v_add3_u32 v157, v124, v157, s64
	v_bfe_u32 v158, v125, 16, 1
	v_lshrrev_b32_e32 v157, 16, v157
	v_add3_u32 v158, v125, v158, s64
	v_and_or_b32 v158, v158, s65, v157
	v_bfe_u32 v157, v122, 16, 1
	v_add3_u32 v157, v122, v157, s64
	v_bfe_u32 v159, v123, 16, 1
	v_lshrrev_b32_e32 v157, 16, v157
	v_add3_u32 v159, v123, v159, s64
	v_and_or_b32 v159, v159, s65, v157
	global_store_dwordx2 v[154:155], v[158:159], off offset:512
	ds_read_b128 v[158:161], v1 offset:2048
	ds_read_b128 v[174:177], v1 offset:10240
	v_pk_mul_f32 v[118:119], v[118:119], v[156:157] op_sel_hi:[1,0]
	v_pk_mul_f32 v[120:121], v[120:121], v[156:157] op_sel_hi:[1,0]
	v_pk_mul_f32 v[216:217], v[46:47], v[118:119]
	v_pk_mul_f32 v[118:119], v[48:49], v[120:121]
	s_waitcnt lgkmcnt(0)
	v_pk_fma_f32 v[120:121], v[158:159], v[216:217], v[174:175]
	v_pk_fma_f32 v[118:119], v[160:161], v[118:119], v[176:177]
	v_bfe_u32 v157, v120, 16, 1
	v_add3_u32 v157, v120, v157, s64
	v_bfe_u32 v158, v121, 16, 1
	v_lshrrev_b32_e32 v157, 16, v157
	v_add3_u32 v158, v121, v158, s64
	ds_read_b128 v[208:211], v1 offset:3072
	ds_read_b128 v[212:215], v1 offset:11264
	v_and_or_b32 v158, v158, s65, v157
	v_bfe_u32 v157, v118, 16, 1
	v_add3_u32 v157, v118, v157, s64
	v_bfe_u32 v159, v119, 16, 1
	v_lshrrev_b32_e32 v157, 16, v157
	v_add3_u32 v159, v119, v159, s64
	v_and_or_b32 v159, v159, s65, v157
	v_pk_mul_f32 v[114:115], v[114:115], v[156:157] op_sel_hi:[1,0]
	global_store_dwordx2 v[154:155], v[158:159], off offset:1024
	v_pk_mul_f32 v[116:117], v[116:117], v[156:157] op_sel_hi:[1,0]
	v_pk_mul_f32 v[158:159], v[38:39], v[114:115]
	v_pk_mul_f32 v[114:115], v[40:41], v[116:117]
	s_waitcnt lgkmcnt(0)
	v_pk_fma_f32 v[116:117], v[208:209], v[158:159], v[212:213]
	v_pk_fma_f32 v[114:115], v[210:211], v[114:115], v[214:215]
	v_bfe_u32 v157, v116, 16, 1
	v_add3_u32 v157, v116, v157, s64
	v_bfe_u32 v158, v117, 16, 1
	v_lshrrev_b32_e32 v157, 16, v157
	v_add3_u32 v158, v117, v158, s64
	v_and_or_b32 v158, v158, s65, v157
	v_bfe_u32 v157, v114, 16, 1
	v_add3_u32 v157, v114, v157, s64
	v_bfe_u32 v159, v115, 16, 1
	v_lshrrev_b32_e32 v157, 16, v157
	v_add3_u32 v159, v115, v159, s64
	v_and_or_b32 v159, v159, s65, v157
	global_store_dwordx2 v[154:155], v[158:159], off offset:1536
	ds_read_b128 v[158:161], v1 offset:4096
	ds_read_b128 v[174:177], v1 offset:12288
	v_pk_mul_f32 v[110:111], v[110:111], v[156:157] op_sel_hi:[1,0]
	v_pk_mul_f32 v[112:113], v[112:113], v[156:157] op_sel_hi:[1,0]
	v_pk_mul_f32 v[216:217], v[30:31], v[110:111]
	v_pk_mul_f32 v[110:111], v[32:33], v[112:113]
	s_waitcnt lgkmcnt(0)
	v_pk_fma_f32 v[112:113], v[216:217], v[158:159], v[174:175]
	v_pk_fma_f32 v[110:111], v[110:111], v[160:161], v[176:177]
	v_bfe_u32 v157, v112, 16, 1
	v_add3_u32 v157, v112, v157, s64
	v_bfe_u32 v158, v113, 16, 1
	v_lshrrev_b32_e32 v157, 16, v157
	v_add3_u32 v158, v113, v158, s64
	ds_read_b128 v[208:211], v1 offset:5120
	ds_read_b128 v[212:215], v1 offset:13312
	v_and_or_b32 v158, v158, s65, v157
	v_bfe_u32 v157, v110, 16, 1
	v_add3_u32 v157, v110, v157, s64
	v_bfe_u32 v159, v111, 16, 1
	v_lshrrev_b32_e32 v157, 16, v157
	v_add3_u32 v159, v111, v159, s64
	v_and_or_b32 v159, v159, s65, v157
	v_pk_mul_f32 v[106:107], v[106:107], v[156:157] op_sel_hi:[1,0]
	global_store_dwordx2 v[154:155], v[158:159], off offset:2048
	v_pk_mul_f32 v[108:109], v[108:109], v[156:157] op_sel_hi:[1,0]
	v_pk_mul_f32 v[158:159], v[22:23], v[106:107]
	v_pk_mul_f32 v[106:107], v[24:25], v[108:109]
	s_waitcnt lgkmcnt(0)
	v_pk_fma_f32 v[108:109], v[158:159], v[208:209], v[212:213]
	v_pk_fma_f32 v[106:107], v[106:107], v[210:211], v[214:215]
	v_bfe_u32 v157, v108, 16, 1
	v_add3_u32 v157, v108, v157, s64
	v_bfe_u32 v158, v109, 16, 1
	v_lshrrev_b32_e32 v157, 16, v157
	v_add3_u32 v158, v109, v158, s64
	v_and_or_b32 v158, v158, s65, v157
	v_bfe_u32 v157, v106, 16, 1
	v_add3_u32 v157, v106, v157, s64
	v_bfe_u32 v159, v107, 16, 1
	v_lshrrev_b32_e32 v157, 16, v157
	v_add3_u32 v159, v107, v159, s64
	v_and_or_b32 v159, v159, s65, v157
	global_store_dwordx2 v[154:155], v[158:159], off offset:2560
	ds_read_b128 v[158:161], v1 offset:6144
	ds_read_b128 v[174:177], v1 offset:14336
	v_pk_mul_f32 v[102:103], v[102:103], v[156:157] op_sel_hi:[1,0]
	v_pk_mul_f32 v[104:105], v[104:105], v[156:157] op_sel_hi:[1,0]
	v_pk_mul_f32 v[216:217], v[14:15], v[102:103]
	v_pk_mul_f32 v[102:103], v[16:17], v[104:105]
	s_waitcnt lgkmcnt(0)
	v_pk_fma_f32 v[104:105], v[216:217], v[158:159], v[174:175]
	v_pk_fma_f32 v[102:103], v[102:103], v[160:161], v[176:177]
	v_bfe_u32 v157, v104, 16, 1
	v_add3_u32 v157, v104, v157, s64
	v_bfe_u32 v158, v105, 16, 1
	v_lshrrev_b32_e32 v157, 16, v157
	v_add3_u32 v158, v105, v158, s64
	ds_read_b128 v[208:211], v1 offset:7168
	ds_read_b128 v[212:215], v1 offset:15360
	v_and_or_b32 v158, v158, s65, v157
	v_bfe_u32 v157, v102, 16, 1
	v_add3_u32 v157, v102, v157, s64
	v_lshrrev_b32_e32 v157, 16, v157
	v_bfe_u32 v159, v103, 16, 1
	v_add3_u32 v159, v103, v159, s64
	v_pk_mul_f32 v[98:99], v[98:99], v[156:157] op_sel_hi:[1,0]
	v_and_or_b32 v159, v159, s65, v157
	v_pk_mul_f32 v[100:101], v[100:101], v[156:157] op_sel_hi:[1,0]
	v_pk_mul_f32 v[156:157], v[58:59], v[98:99]
	v_pk_mul_f32 v[98:99], v[60:61], v[100:101]
	s_waitcnt lgkmcnt(0)
	v_pk_fma_f32 v[100:101], v[156:157], v[208:209], v[212:213]
	v_pk_fma_f32 v[98:99], v[98:99], v[210:211], v[214:215]
	v_bfe_u32 v156, v100, 16, 1
	v_add3_u32 v156, v100, v156, s64
	v_bfe_u32 v157, v101, 16, 1
	v_lshrrev_b32_e32 v156, 16, v156
	v_add3_u32 v157, v101, v157, s64
	v_and_or_b32 v156, v157, s65, v156
	v_bfe_u32 v157, v98, 16, 1
	global_store_dwordx2 v[154:155], v[158:159], off offset:3072
	v_add3_u32 v157, v98, v157, s64
	v_bfe_u32 v158, v99, 16, 1
	v_lshrrev_b32_e32 v157, 16, v157
	v_add3_u32 v158, v99, v158, s64
	v_and_or_b32 v157, v158, s65, v157
	global_store_dwordx2 v[154:155], v[156:157], off offset:3584
	v_and_b32_sdwa v156, v126, v202 dst_sel:DWORD dst_unused:UNUSED_PAD src0_sel:WORD_1 src1_sel:DWORD
	v_and_b32_sdwa v157, v128, v202 dst_sel:DWORD dst_unused:UNUSED_PAD src0_sel:WORD_1 src1_sel:DWORD
	v_mov_b32_e32 v154, v128
	v_add3_u32 v158, v126, v156, s64
	v_add3_u32 v159, v128, v157, s64
	v_and_b32_sdwa v128, v127, v202 dst_sel:DWORD dst_unused:UNUSED_PAD src0_sel:WORD_1 src1_sel:DWORD
	v_and_b32_sdwa v156, v129, v202 dst_sel:DWORD dst_unused:UNUSED_PAD src0_sel:WORD_1 src1_sel:DWORD
	v_add3_u32 v128, v127, v128, s64
	v_add3_u32 v156, v129, v156, s64
	v_mov_b32_e32 v155, v126
	v_mov_b32_e32 v126, v129
	v_and_b32_e32 v129, 0xffff0000, v128
	v_and_b32_e32 v128, 0xffff0000, v156
	v_and_b32_e32 v157, 0xffff0000, v158
	v_and_b32_e32 v156, 0xffff0000, v159
	v_pk_add_f32 v[154:155], v[154:155], v[156:157] neg_lo:[0,1] neg_hi:[0,1]
	v_pk_add_f32 v[156:157], v[126:127], v[128:129] neg_lo:[0,1] neg_hi:[0,1]
	v_or_b32_sdwa v126, v159, v128 dst_sel:DWORD dst_unused:UNUSED_PAD src0_sel:WORD_1 src1_sel:DWORD
	v_or_b32_sdwa v127, v158, v129 dst_sel:DWORD dst_unused:UNUSED_PAD src0_sel:WORD_1 src1_sel:DWORD
	v_and_b32_sdwa v128, v155, v202 dst_sel:DWORD dst_unused:UNUSED_PAD src0_sel:WORD_1 src1_sel:DWORD
	v_and_b32_sdwa v129, v154, v202 dst_sel:DWORD dst_unused:UNUSED_PAD src0_sel:WORD_1 src1_sel:DWORD
	v_add3_u32 v154, v154, v129, s64
	v_add3_u32 v128, v155, v128, s64
	v_and_b32_sdwa v129, v157, v202 dst_sel:DWORD dst_unused:UNUSED_PAD src0_sel:WORD_1 src1_sel:DWORD
	v_and_b32_sdwa v155, v156, v202 dst_sel:DWORD dst_unused:UNUSED_PAD src0_sel:WORD_1 src1_sel:DWORD
	v_add3_u32 v129, v157, v129, s64
	v_add3_u32 v155, v156, v155, s64
	v_and_b32_e32 v129, 0xffff0000, v129
	v_and_b32_e32 v155, 0xffff0000, v155
	v_and_b32_sdwa v156, v122, v202 dst_sel:DWORD dst_unused:UNUSED_PAD src0_sel:WORD_1 src1_sel:DWORD
	v_and_b32_sdwa v157, v124, v202 dst_sel:DWORD dst_unused:UNUSED_PAD src0_sel:WORD_1 src1_sel:DWORD
	v_or_b32_sdwa v129, v129, v128 dst_sel:DWORD dst_unused:UNUSED_PAD src0_sel:DWORD src1_sel:WORD_1
	v_or_b32_sdwa v128, v155, v154 dst_sel:DWORD dst_unused:UNUSED_PAD src0_sel:DWORD src1_sel:WORD_1
	v_mov_b32_e32 v154, v124
	v_add3_u32 v158, v122, v156, s64
	v_add3_u32 v159, v124, v157, s64
	v_and_b32_sdwa v124, v123, v202 dst_sel:DWORD dst_unused:UNUSED_PAD src0_sel:WORD_1 src1_sel:DWORD
	v_and_b32_sdwa v156, v125, v202 dst_sel:DWORD dst_unused:UNUSED_PAD src0_sel:WORD_1 src1_sel:DWORD
	v_add3_u32 v124, v123, v124, s64
	v_add3_u32 v156, v125, v156, s64
	v_mov_b32_e32 v155, v122
	v_mov_b32_e32 v122, v125
	v_and_b32_e32 v125, 0xffff0000, v124
	v_and_b32_e32 v124, 0xffff0000, v156
	v_and_b32_e32 v157, 0xffff0000, v158
	v_and_b32_e32 v156, 0xffff0000, v159
	v_pk_add_f32 v[154:155], v[154:155], v[156:157] neg_lo:[0,1] neg_hi:[0,1]
	v_pk_add_f32 v[122:123], v[122:123], v[124:125] neg_lo:[0,1] neg_hi:[0,1]
	v_and_b32_sdwa v156, v155, v202 dst_sel:DWORD dst_unused:UNUSED_PAD src0_sel:WORD_1 src1_sel:DWORD
	v_and_b32_sdwa v157, v154, v202 dst_sel:DWORD dst_unused:UNUSED_PAD src0_sel:WORD_1 src1_sel:DWORD
	v_add3_u32 v176, v154, v157, s64
	v_add3_u32 v177, v155, v156, s64
	v_mov_b32_e32 v156, v95
	v_mov_b32_e32 v157, v91
	v_or_b32_sdwa v124, v159, v124 dst_sel:DWORD dst_unused:UNUSED_PAD src0_sel:WORD_1 src1_sel:DWORD
	v_or_b32_sdwa v125, v158, v125 dst_sel:DWORD dst_unused:UNUSED_PAD src0_sel:WORD_1 src1_sel:DWORD
	v_mov_b32_e32 v154, v94
	v_mov_b32_e32 v155, v90
	v_pk_mul_f32 v[156:157], v[156:157], v[156:157]
	v_mov_b32_e32 v158, v97
	v_mov_b32_e32 v159, v93
	v_pk_fma_f32 v[154:155], v[154:155], v[154:155], v[156:157]
	v_mov_b32_e32 v156, v96
	v_mov_b32_e32 v157, v92
	v_pk_mul_f32 v[158:159], v[158:159], v[158:159]
	s_addc_u32 s7, s49, s7
	v_pk_fma_f32 v[156:157], v[156:157], v[156:157], v[158:159]
	v_pk_mul_f32 v[158:159], v[86:87], v[86:87]
	v_pk_add_f32 v[154:155], v[154:155], v[156:157]
	v_pk_mul_f32 v[156:157], v[88:89], v[88:89]
	v_pk_add_f32 v[154:155], v[154:155], v[154:155] op_sel:[0,1] op_sel_hi:[1,0]
	v_pk_mov_b32 v[160:161], v[158:159], v[156:157] op_sel:[1,0]
	v_mov_b32_e32 v159, v157
	v_pk_add_f32 v[156:157], v[160:161], v[158:159]
	v_mul_f32_e32 v158, v78, v78
	v_mul_f32_e32 v159, v79, v79
	v_pk_add_f32 v[156:157], v[156:157], v[156:157] op_sel:[0,1] op_sel_hi:[1,0]
	v_mov_b32_e32 v155, v158
	v_mov_b32_e32 v157, v159
	v_pk_add_f32 v[154:155], v[154:155], v[156:157]
	v_mul_f32_e32 v156, v83, v83
	v_mul_f32_e32 v158, v85, v85
	v_mul_f32_e32 v160, v80, v80
	v_mul_f32_e32 v161, v81, v81
	v_pk_fma_f32 v[156:157], v[82:83], v[82:83], v[156:157] op_sel_hi:[1,1,0]
	v_pk_fma_f32 v[158:159], v[84:85], v[84:85], v[158:159] op_sel_hi:[1,1,0]
	v_mov_b32_e32 v157, v160
	v_mov_b32_e32 v159, v161
	v_pk_add_f32 v[156:157], v[156:157], v[158:159]
	v_pk_mul_f32 v[158:159], v[74:75], v[74:75]
	v_pk_add_f32 v[154:155], v[154:155], v[156:157]
	v_pk_mul_f32 v[156:157], v[76:77], v[76:77]
	v_pk_add_f32 v[154:155], v[154:155], v[154:155] op_sel:[0,1] op_sel_hi:[1,0]
	v_pk_mov_b32 v[160:161], v[158:159], v[156:157] op_sel:[1,0]
	v_mov_b32_e32 v159, v157
	v_pk_add_f32 v[156:157], v[160:161], v[158:159]
	v_mul_f32_e32 v158, v66, v66
	v_mul_f32_e32 v159, v67, v67
	v_pk_add_f32 v[156:157], v[156:157], v[156:157] op_sel:[0,1] op_sel_hi:[1,0]
	v_mov_b32_e32 v155, v158
	v_mov_b32_e32 v157, v159
	v_pk_add_f32 v[154:155], v[154:155], v[156:157]
	v_mul_f32_e32 v156, v71, v71
	v_mul_f32_e32 v158, v73, v73
	v_mul_f32_e32 v160, v68, v68
	v_mul_f32_e32 v161, v69, v69
	v_pk_fma_f32 v[156:157], v[70:71], v[70:71], v[156:157] op_sel_hi:[1,1,0]
	v_pk_fma_f32 v[158:159], v[72:73], v[72:73], v[158:159] op_sel_hi:[1,1,0]
	v_mov_b32_e32 v157, v160
	v_mov_b32_e32 v159, v161
	v_pk_add_f32 v[156:157], v[156:157], v[158:159]
	v_mov_b32_e32 v158, v51
	v_mov_b32_e32 v159, v43
	v_pk_add_f32 v[154:155], v[154:155], v[156:157]
	v_mov_b32_e32 v156, v50
	v_mov_b32_e32 v157, v42
	v_pk_mul_f32 v[158:159], v[158:159], v[158:159]
	v_mov_b32_e32 v160, v53
	v_mov_b32_e32 v161, v45
	v_pk_fma_f32 v[156:157], v[156:157], v[156:157], v[158:159]
	v_mov_b32_e32 v158, v52
	v_mov_b32_e32 v159, v44
	v_pk_mul_f32 v[160:161], v[160:161], v[160:161]
	s_lshl_b64 s[4:5], s[4:5], 12
	v_pk_fma_f32 v[158:159], v[158:159], v[158:159], v[160:161]
	v_pk_mul_f32 v[160:161], v[34:35], v[34:35]
	v_pk_add_f32 v[156:157], v[156:157], v[158:159]
	v_pk_mul_f32 v[158:159], v[36:37], v[36:37]
	v_pk_add_f32 v[156:157], v[156:157], v[156:157] op_sel:[0,1] op_sel_hi:[1,0]
	v_pk_mov_b32 v[174:175], v[160:161], v[158:159] op_sel:[1,0]
	v_mov_b32_e32 v161, v159
	v_pk_add_f32 v[158:159], v[174:175], v[160:161]
	v_mul_f32_e32 v160, v18, v18
	v_mul_f32_e32 v161, v19, v19
	v_pk_add_f32 v[158:159], v[158:159], v[158:159] op_sel:[0,1] op_sel_hi:[1,0]
	v_mov_b32_e32 v157, v160
	v_mov_b32_e32 v159, v161
	v_pk_add_f32 v[156:157], v[156:157], v[158:159]
	v_mul_f32_e32 v158, v27, v27
	v_mul_f32_e32 v160, v29, v29
	v_mul_f32_e32 v174, v20, v20
	v_mul_f32_e32 v175, v21, v21
	v_pk_fma_f32 v[158:159], v[26:27], v[26:27], v[158:159] op_sel_hi:[1,1,0]
	v_pk_fma_f32 v[160:161], v[28:29], v[28:29], v[160:161] op_sel_hi:[1,1,0]
	v_mov_b32_e32 v159, v174
	v_mov_b32_e32 v161, v175
	v_pk_add_f32 v[158:159], v[158:159], v[160:161]
	v_pk_mul_f32 v[160:161], v[10:11], v[10:11]
	v_pk_add_f32 v[156:157], v[156:157], v[158:159]
	v_pk_mul_f32 v[158:159], v[12:13], v[12:13]
	v_pk_add_f32 v[156:157], v[156:157], v[156:157] op_sel:[0,1] op_sel_hi:[1,0]
	v_pk_mov_b32 v[174:175], v[160:161], v[158:159] op_sel:[1,0]
	v_mov_b32_e32 v161, v159
	v_pk_add_f32 v[158:159], v[174:175], v[160:161]
	s_waitcnt vmcnt(16)
	v_mul_f32_e32 v160, v2, v2
	v_mul_f32_e32 v161, v3, v3
	v_pk_add_f32 v[158:159], v[158:159], v[158:159] op_sel:[0,1] op_sel_hi:[1,0]
	v_mov_b32_e32 v157, v160
	v_mov_b32_e32 v159, v161
	v_pk_add_f32 v[156:157], v[156:157], v[158:159]
	v_mul_f32_e32 v158, v7, v7
	v_mul_f32_e32 v160, v9, v9
	v_mul_f32_e32 v174, v4, v4
	v_mul_f32_e32 v175, v5, v5
	v_pk_fma_f32 v[158:159], v[6:7], v[6:7], v[158:159] op_sel_hi:[1,1,0]
	v_pk_fma_f32 v[160:161], v[8:9], v[8:9], v[160:161] op_sel_hi:[1,1,0]
	v_mov_b32_e32 v159, v174
	v_mov_b32_e32 v161, v175
	v_pk_add_f32 v[158:159], v[158:159], v[160:161]
	s_add_u32 s4, s48, s4
	v_pk_add_f32 v[156:157], v[156:157], v[158:159]
	v_mov_b32_e32 v159, v154
	v_mov_b32_e32 v158, v156
	v_mov_b32_e32 v154, v157
	v_pk_add_f32 v[154:155], v[158:159], v[154:155]
	ds_bpermute_b32 v157, v164, v155
	ds_bpermute_b32 v156, v164, v154
	v_and_b32_sdwa v158, v123, v202 dst_sel:DWORD dst_unused:UNUSED_PAD src0_sel:WORD_1 src1_sel:DWORD
	v_and_b32_sdwa v159, v122, v202 dst_sel:DWORD dst_unused:UNUSED_PAD src0_sel:WORD_1 src1_sel:DWORD
	v_add3_u32 v158, v123, v158, s64
	v_add3_u32 v159, v122, v159, s64
	s_waitcnt lgkmcnt(0)
	v_pk_add_f32 v[122:123], v[154:155], v[156:157]
	ds_bpermute_b32 v155, v180, v123
	ds_bpermute_b32 v154, v180, v122
	v_and_b32_e32 v156, 0xffff0000, v158
	v_and_b32_e32 v158, 0xffff0000, v159
	v_or_b32_sdwa v157, v156, v177 dst_sel:DWORD dst_unused:UNUSED_PAD src0_sel:DWORD src1_sel:WORD_1
	v_or_b32_sdwa v156, v158, v176 dst_sel:DWORD dst_unused:UNUSED_PAD src0_sel:DWORD src1_sel:WORD_1
	s_waitcnt lgkmcnt(0)
	v_pk_add_f32 v[122:123], v[122:123], v[154:155]
	ds_bpermute_b32 v155, v181, v123
	ds_bpermute_b32 v154, v181, v122
	ds_write2st64_b64 v203, v[126:127], v[124:125] offset0:34 offset1:35
	ds_write2st64_b64 v203, v[128:129], v[156:157] offset0:99 offset1:100
	v_lshl_add_u64 v[124:125], s[6:7], 0, v[166:167]
	s_addc_u32 s5, s49, s5
	s_waitcnt lgkmcnt(2)
	v_pk_add_f32 v[122:123], v[122:123], v[154:155]
	ds_bpermute_b32 v159, v206, v123
	ds_bpermute_b32 v158, v206, v122
	ds_read_b128 v[126:129], v1
	ds_read_b128 v[154:157], v1 offset:1024
	s_waitcnt lgkmcnt(2)
	v_pk_add_f32 v[122:123], v[122:123], v[158:159]
	ds_bpermute_b32 v181, v178, v123
	ds_bpermute_b32 v180, v178, v122
	ds_read_b128 v[158:161], v1 offset:8192
	ds_read_b128 v[174:177], v1 offset:9216
	ds_read_b128 v[206:209], v1 offset:2048
	ds_read_b128 v[210:213], v1 offset:3072
	s_waitcnt lgkmcnt(4)
	v_pk_add_f32 v[122:123], v[122:123], v[180:181]
	ds_bpermute_b32 v223, v179, v123
	ds_bpermute_b32 v222, v179, v122
	ds_read_b128 v[178:181], v1 offset:10240
	ds_read_b128 v[214:217], v1 offset:11264
	ds_read_b128 v[218:221], v1 offset:4096
	ds_read_b128 v[224:227], v1 offset:5120
	ds_read_b128 v[228:231], v1 offset:12288
	ds_read_b128 v[232:235], v1 offset:13312
	ds_read_b128 v[236:239], v1 offset:6144
	ds_read_b128 v[240:243], v1 offset:7168
	ds_read_b128 v[244:247], v1 offset:14336
	ds_read_b128 v[248:251], v1 offset:15360
	s_waitcnt lgkmcnt(10)
	v_pk_add_f32 v[122:123], v[122:123], v[222:223]
	s_nop 0
	v_pk_fma_f32 v[122:123], v[122:123], s[42:43], v[172:173] op_sel_hi:[1,0,0]
	s_nop 0
	v_mul_f32_e32 v164, 0x4b800000, v123
	v_cmp_gt_f32_e32 vcc, s63, v123
	s_nop 1
	v_cndmask_b32_e32 v123, v123, v164, vcc
	v_rsq_f32_e32 v123, v123
	s_nop 0
	v_mul_f32_e32 v164, 0x45800000, v123
	v_cndmask_b32_e32 v164, v123, v164, vcc
	v_pk_mul_f32 v[90:91], v[90:91], v[164:165] op_sel_hi:[1,0]
	v_pk_mul_f32 v[94:95], v[94:95], v[164:165] op_sel_hi:[1,0]
	v_pk_mul_f32 v[90:91], v[54:55], v[90:91]
	v_pk_mul_f32 v[94:95], v[62:63], v[94:95]
	v_pk_fma_f32 v[174:175], v[154:155], v[90:91], v[174:175]
	v_pk_fma_f32 v[126:127], v[126:127], v[94:95], v[158:159]
	v_pk_mul_f32 v[92:93], v[92:93], v[164:165] op_sel_hi:[1,0]
	v_bfe_u32 v90, v174, 16, 1
	v_pk_mul_f32 v[96:97], v[96:97], v[164:165] op_sel_hi:[1,0]
	v_bfe_u32 v94, v126, 16, 1
	v_pk_mul_f32 v[92:93], v[56:57], v[92:93]
	v_add3_u32 v90, v174, v90, s64
	v_bfe_u32 v91, v175, 16, 1
	v_pk_mul_f32 v[96:97], v[64:65], v[96:97]
	v_add3_u32 v94, v126, v94, s64
	v_bfe_u32 v95, v127, 16, 1
	v_pk_fma_f32 v[176:177], v[156:157], v[92:93], v[176:177]
	v_lshrrev_b32_e32 v90, 16, v90
	v_add3_u32 v91, v175, v91, s64
	v_pk_fma_f32 v[128:129], v[128:129], v[96:97], v[160:161]
	v_lshrrev_b32_e32 v94, 16, v94
	v_add3_u32 v95, v127, v95, s64
	v_and_or_b32 v90, v91, s65, v90
	v_bfe_u32 v91, v176, 16, 1
	v_and_or_b32 v94, v95, s65, v94
	v_bfe_u32 v95, v128, 16, 1
	v_add3_u32 v91, v176, v91, s64
	v_bfe_u32 v92, v177, 16, 1
	v_pk_mul_f32 v[74:75], v[74:75], v[164:165] op_sel_hi:[1,0]
	v_add3_u32 v95, v128, v95, s64
	v_bfe_u32 v96, v129, 16, 1
	v_lshrrev_b32_e32 v91, 16, v91
	v_add3_u32 v92, v177, v92, s64
	v_pk_mul_f32 v[78:79], v[78:79], v[164:165] op_sel_hi:[1,0]
	v_pk_mul_f32 v[74:75], v[22:23], v[74:75]
	v_lshrrev_b32_e32 v95, 16, v95
	v_add3_u32 v96, v129, v96, s64
	v_and_or_b32 v91, v92, s65, v91
	v_pk_mul_f32 v[78:79], v[30:31], v[78:79]
	s_waitcnt lgkmcnt(4)
	v_pk_fma_f32 v[92:93], v[74:75], v[224:225], v[232:233]
	v_and_or_b32 v95, v96, s65, v95
	v_pk_fma_f32 v[96:97], v[78:79], v[218:219], v[228:229]
	v_pk_mul_f32 v[76:77], v[76:77], v[164:165] op_sel_hi:[1,0]
	v_bfe_u32 v74, v92, 16, 1
	v_pk_mul_f32 v[80:81], v[80:81], v[164:165] op_sel_hi:[1,0]
	v_bfe_u32 v78, v96, 16, 1
	v_pk_mul_f32 v[76:77], v[24:25], v[76:77]
	v_add3_u32 v74, v92, v74, s64
	v_bfe_u32 v75, v93, 16, 1
	global_store_dwordx2 v[124:125], v[90:91], off offset:512
	v_pk_mul_f32 v[80:81], v[32:33], v[80:81]
	v_add3_u32 v78, v96, v78, s64
	v_bfe_u32 v79, v97, 16, 1
	v_pk_fma_f32 v[90:91], v[76:77], v[226:227], v[234:235]
	v_lshrrev_b32_e32 v74, 16, v74
	v_add3_u32 v75, v93, v75, s64
	global_store_dwordx2 v[124:125], v[94:95], off
	v_pk_fma_f32 v[94:95], v[80:81], v[220:221], v[230:231]
	v_lshrrev_b32_e32 v78, 16, v78
	v_add3_u32 v79, v97, v79, s64
	v_and_or_b32 v74, v75, s65, v74
	v_bfe_u32 v75, v90, 16, 1
	v_and_or_b32 v78, v79, s65, v78
	v_bfe_u32 v79, v94, 16, 1
	v_add3_u32 v75, v90, v75, s64
	v_bfe_u32 v76, v91, 16, 1
	v_pk_mul_f32 v[66:67], v[66:67], v[164:165] op_sel_hi:[1,0]
	v_add3_u32 v79, v94, v79, s64
	v_bfe_u32 v80, v95, 16, 1
	v_lshrrev_b32_e32 v75, 16, v75
	v_add3_u32 v76, v91, v76, s64
	v_pk_mul_f32 v[70:71], v[70:71], v[164:165] op_sel_hi:[1,0]
	v_pk_mul_f32 v[66:67], v[58:59], v[66:67]
	v_lshrrev_b32_e32 v79, 16, v79
	v_add3_u32 v80, v95, v80, s64
	v_and_or_b32 v75, v76, s65, v75
	v_pk_mul_f32 v[70:71], v[14:15], v[70:71]
	s_waitcnt lgkmcnt(0)
	v_pk_fma_f32 v[76:77], v[66:67], v[240:241], v[248:249]
	v_and_or_b32 v79, v80, s65, v79
	v_pk_fma_f32 v[80:81], v[70:71], v[236:237], v[244:245]
	v_pk_mul_f32 v[68:69], v[68:69], v[164:165] op_sel_hi:[1,0]
	v_bfe_u32 v66, v76, 16, 1
	v_pk_mul_f32 v[72:73], v[72:73], v[164:165] op_sel_hi:[1,0]
	v_bfe_u32 v70, v80, 16, 1
	v_pk_mul_f32 v[68:69], v[60:61], v[68:69]
	v_add3_u32 v66, v76, v66, s64
	v_bfe_u32 v67, v77, 16, 1
	global_store_dwordx2 v[124:125], v[74:75], off offset:2560
	v_pk_mul_f32 v[72:73], v[16:17], v[72:73]
	v_add3_u32 v70, v80, v70, s64
	v_bfe_u32 v71, v81, 16, 1
	v_pk_fma_f32 v[74:75], v[68:69], v[242:243], v[250:251]
	v_lshrrev_b32_e32 v66, 16, v66
	v_add3_u32 v67, v77, v67, s64
	global_store_dwordx2 v[124:125], v[78:79], off offset:2048
	v_pk_fma_f32 v[78:79], v[72:73], v[238:239], v[246:247]
	v_lshrrev_b32_e32 v70, 16, v70
	v_add3_u32 v71, v81, v71, s64
	v_and_or_b32 v66, v67, s65, v66
	v_bfe_u32 v67, v74, 16, 1
	v_and_or_b32 v70, v71, s65, v70
	v_bfe_u32 v71, v78, 16, 1
	v_add3_u32 v67, v74, v67, s64
	v_bfe_u32 v68, v75, 16, 1
	v_pk_mul_f32 v[82:83], v[82:83], v[164:165] op_sel_hi:[1,0]
	v_add3_u32 v71, v78, v71, s64
	v_bfe_u32 v72, v79, 16, 1
	v_lshrrev_b32_e32 v67, 16, v67
	v_add3_u32 v68, v75, v68, s64
	v_pk_mul_f32 v[82:83], v[38:39], v[82:83]
	v_lshrrev_b32_e32 v71, 16, v71
	v_add3_u32 v72, v79, v72, s64
	v_and_or_b32 v67, v68, s65, v67
	v_and_b32_sdwa v68, v128, v202 dst_sel:DWORD dst_unused:UNUSED_PAD src0_sel:WORD_1 src1_sel:DWORD
	v_and_b32_sdwa v69, v126, v202 dst_sel:DWORD dst_unused:UNUSED_PAD src0_sel:WORD_1 src1_sel:DWORD
	v_pk_fma_f32 v[156:157], v[210:211], v[82:83], v[214:215]
	v_and_or_b32 v71, v72, s65, v71
	v_add3_u32 v72, v128, v68, s64
	v_add3_u32 v73, v126, v69, s64
	v_and_b32_sdwa v68, v129, v202 dst_sel:DWORD dst_unused:UNUSED_PAD src0_sel:WORD_1 src1_sel:DWORD
	v_and_b32_sdwa v69, v127, v202 dst_sel:DWORD dst_unused:UNUSED_PAD src0_sel:WORD_1 src1_sel:DWORD
	v_pk_mul_f32 v[84:85], v[84:85], v[164:165] op_sel_hi:[1,0]
	v_bfe_u32 v82, v156, 16, 1
	global_store_dwordx2 v[124:125], v[70:71], off offset:3072
	v_add3_u32 v68, v129, v68, s64
	v_add3_u32 v70, v127, v69, s64
	v_pk_mul_f32 v[84:85], v[40:41], v[84:85]
	v_add3_u32 v82, v156, v82, s64
	v_bfe_u32 v83, v157, 16, 1
	global_store_dwordx2 v[124:125], v[66:67], off offset:3584
	v_mov_b32_e32 v66, v126
	v_mov_b32_e32 v67, v128
	v_and_b32_e32 v69, 0xffff0000, v68
	v_and_b32_e32 v68, 0xffff0000, v70
	v_and_b32_e32 v71, 0xffff0000, v72
	v_and_b32_e32 v70, 0xffff0000, v73
	v_pk_fma_f32 v[154:155], v[212:213], v[84:85], v[216:217]
	v_lshrrev_b32_e32 v82, 16, v82
	v_add3_u32 v83, v157, v83, s64
	v_mov_b32_e32 v128, v127
	v_pk_add_f32 v[66:67], v[66:67], v[70:71] neg_lo:[0,1] neg_hi:[0,1]
	v_and_or_b32 v82, v83, s65, v82
	v_bfe_u32 v83, v154, 16, 1
	v_pk_add_f32 v[70:71], v[128:129], v[68:69] neg_lo:[0,1] neg_hi:[0,1]
	v_or_b32_sdwa v68, v73, v68 dst_sel:DWORD dst_unused:UNUSED_PAD src0_sel:WORD_1 src1_sel:DWORD
	v_or_b32_sdwa v69, v72, v69 dst_sel:DWORD dst_unused:UNUSED_PAD src0_sel:WORD_1 src1_sel:DWORD
	v_and_b32_sdwa v72, v67, v202 dst_sel:DWORD dst_unused:UNUSED_PAD src0_sel:WORD_1 src1_sel:DWORD
	v_and_b32_sdwa v73, v66, v202 dst_sel:DWORD dst_unused:UNUSED_PAD src0_sel:WORD_1 src1_sel:DWORD
	v_add3_u32 v83, v154, v83, s64
	v_bfe_u32 v84, v155, 16, 1
	v_add3_u32 v66, v66, v73, s64
	v_add3_u32 v67, v67, v72, s64
	v_and_b32_sdwa v72, v71, v202 dst_sel:DWORD dst_unused:UNUSED_PAD src0_sel:WORD_1 src1_sel:DWORD
	v_and_b32_sdwa v73, v70, v202 dst_sel:DWORD dst_unused:UNUSED_PAD src0_sel:WORD_1 src1_sel:DWORD
	v_lshrrev_b32_e32 v83, 16, v83
	v_add3_u32 v84, v155, v84, s64
	v_add3_u32 v71, v71, v72, s64
	v_add3_u32 v70, v70, v73, s64
	v_and_b32_sdwa v72, v176, v202 dst_sel:DWORD dst_unused:UNUSED_PAD src0_sel:WORD_1 src1_sel:DWORD
	v_and_b32_sdwa v73, v174, v202 dst_sel:DWORD dst_unused:UNUSED_PAD src0_sel:WORD_1 src1_sel:DWORD
	v_and_or_b32 v83, v84, s65, v83
	v_add3_u32 v84, v176, v72, s64
	v_add3_u32 v85, v174, v73, s64
	v_and_b32_sdwa v72, v177, v202 dst_sel:DWORD dst_unused:UNUSED_PAD src0_sel:WORD_1 src1_sel:DWORD
	v_and_b32_sdwa v73, v175, v202 dst_sel:DWORD dst_unused:UNUSED_PAD src0_sel:WORD_1 src1_sel:DWORD
	global_store_dwordx2 v[124:125], v[82:83], off offset:1536
	v_and_b32_e32 v71, 0xffff0000, v71
	v_and_b32_e32 v70, 0xffff0000, v70
	v_add3_u32 v72, v177, v72, s64
	v_add3_u32 v82, v175, v73, s64
	v_or_b32_sdwa v67, v71, v67 dst_sel:DWORD dst_unused:UNUSED_PAD src0_sel:DWORD src1_sel:WORD_1
	v_or_b32_sdwa v66, v70, v66 dst_sel:DWORD dst_unused:UNUSED_PAD src0_sel:DWORD src1_sel:WORD_1
	v_mov_b32_e32 v70, v174
	v_mov_b32_e32 v71, v176
	v_and_b32_e32 v73, 0xffff0000, v72
	v_and_b32_e32 v72, 0xffff0000, v82
	v_and_b32_e32 v83, 0xffff0000, v84
	v_and_b32_e32 v82, 0xffff0000, v85
	v_mov_b32_e32 v176, v175
	v_pk_add_f32 v[70:71], v[70:71], v[82:83] neg_lo:[0,1] neg_hi:[0,1]
	v_pk_mul_f32 v[86:87], v[86:87], v[164:165] op_sel_hi:[1,0]
	v_pk_add_f32 v[82:83], v[176:177], v[72:73] neg_lo:[0,1] neg_hi:[0,1]
	v_or_b32_sdwa v73, v84, v73 dst_sel:DWORD dst_unused:UNUSED_PAD src0_sel:WORD_1 src1_sel:DWORD
	v_and_b32_sdwa v84, v71, v202 dst_sel:DWORD dst_unused:UNUSED_PAD src0_sel:WORD_1 src1_sel:DWORD
	v_pk_mul_f32 v[86:87], v[46:47], v[86:87]
	v_add3_u32 v71, v71, v84, s64
	v_and_b32_sdwa v84, v83, v202 dst_sel:DWORD dst_unused:UNUSED_PAD src0_sel:WORD_1 src1_sel:DWORD
	v_pk_fma_f32 v[160:161], v[206:207], v[86:87], v[178:179]
	v_add3_u32 v83, v83, v84, s64
	v_pk_mul_f32 v[88:89], v[88:89], v[164:165] op_sel_hi:[1,0]
	v_bfe_u32 v86, v160, 16, 1
	v_and_b32_e32 v83, 0xffff0000, v83
	v_pk_mul_f32 v[88:89], v[48:49], v[88:89]
	v_add3_u32 v86, v160, v86, s64
	v_bfe_u32 v87, v161, 16, 1
	v_or_b32_sdwa v71, v83, v71 dst_sel:DWORD dst_unused:UNUSED_PAD src0_sel:DWORD src1_sel:WORD_1
	v_mul_f32_e32 v83, 0x4b800000, v122
	v_cmp_gt_f32_e32 vcc, s63, v122
	v_pk_fma_f32 v[158:159], v[208:209], v[88:89], v[180:181]
	v_lshrrev_b32_e32 v86, 16, v86
	v_add3_u32 v87, v161, v87, s64
	v_cndmask_b32_e32 v83, v122, v83, vcc
	v_and_or_b32 v86, v87, s65, v86
	v_bfe_u32 v87, v158, 16, 1
	v_or_b32_sdwa v72, v85, v72 dst_sel:DWORD dst_unused:UNUSED_PAD src0_sel:WORD_1 src1_sel:DWORD
	v_and_b32_sdwa v85, v70, v202 dst_sel:DWORD dst_unused:UNUSED_PAD src0_sel:WORD_1 src1_sel:DWORD
	v_rsq_f32_e32 v83, v83
	v_add3_u32 v87, v158, v87, s64
	v_bfe_u32 v88, v159, 16, 1
	v_add3_u32 v70, v70, v85, s64
	v_and_b32_sdwa v85, v82, v202 dst_sel:DWORD dst_unused:UNUSED_PAD src0_sel:WORD_1 src1_sel:DWORD
	v_lshrrev_b32_e32 v87, 16, v87
	v_add3_u32 v88, v159, v88, s64
	v_add3_u32 v82, v82, v85, s64
	v_and_or_b32 v87, v88, s65, v87
	v_and_b32_e32 v82, 0xffff0000, v82
	global_store_dwordx2 v[124:125], v[86:87], off offset:1024
	v_or_b32_sdwa v70, v82, v70 dst_sel:DWORD dst_unused:UNUSED_PAD src0_sel:DWORD src1_sel:WORD_1
	ds_write2st64_b64 v204, v[68:69], v[72:73] offset0:36 offset1:37
	ds_write2st64_b64 v204, v[66:67], v[70:71] offset0:101 offset1:102
	v_mul_f32_e32 v66, 0x45800000, v83
	v_cndmask_b32_e32 v68, v83, v66, vcc
	ds_read_b128 v[70:73], v1
	ds_read_b128 v[82:85], v1 offset:8192
	v_pk_mul_f32 v[50:51], v[50:51], v[68:69] op_sel_hi:[1,0]
	v_pk_mul_f32 v[52:53], v[52:53], v[68:69] op_sel_hi:[1,0]
	v_pk_mul_f32 v[122:123], v[62:63], v[50:51]
	v_pk_mul_f32 v[50:51], v[64:65], v[52:53]
	s_waitcnt lgkmcnt(0)
	v_pk_fma_f32 v[52:53], v[70:71], v[122:123], v[82:83]
	v_pk_fma_f32 v[50:51], v[72:73], v[50:51], v[84:85]
	v_bfe_u32 v69, v52, 16, 1
	v_add3_u32 v69, v52, v69, s64
	v_bfe_u32 v70, v53, 16, 1
	v_lshrrev_b32_e32 v69, 16, v69
	v_add3_u32 v70, v53, v70, s64
	ds_read_b128 v[62:65], v1 offset:1024
	ds_read_b128 v[86:89], v1 offset:9216
	v_and_or_b32 v70, v70, s65, v69
	v_bfe_u32 v69, v50, 16, 1
	v_add3_u32 v69, v50, v69, s64
	v_lshrrev_b32_e32 v69, 16, v69
	v_pk_mul_f32 v[42:43], v[42:43], v[68:69] op_sel_hi:[1,0]
	v_pk_mul_f32 v[44:45], v[44:45], v[68:69] op_sel_hi:[1,0]
	v_pk_mul_f32 v[54:55], v[54:55], v[42:43]
	v_pk_mul_f32 v[42:43], v[56:57], v[44:45]
	s_waitcnt lgkmcnt(0)
	v_pk_fma_f32 v[44:45], v[62:63], v[54:55], v[86:87]
	v_pk_fma_f32 v[42:43], v[64:65], v[42:43], v[88:89]
	v_bfe_u32 v54, v44, 16, 1
	v_add3_u32 v54, v44, v54, s64
	v_bfe_u32 v55, v45, 16, 1
	v_lshrrev_b32_e32 v54, 16, v54
	v_add3_u32 v55, v45, v55, s64
	v_and_or_b32 v54, v55, s65, v54
	v_bfe_u32 v55, v42, 16, 1
	v_bfe_u32 v71, v51, 16, 1
	v_add3_u32 v55, v42, v55, s64
	v_bfe_u32 v56, v43, 16, 1
	v_add3_u32 v71, v51, v71, s64
	v_lshrrev_b32_e32 v55, 16, v55
	v_add3_u32 v56, v43, v56, s64
	v_lshl_add_u64 v[66:67], s[4:5], 0, v[166:167]
	v_and_or_b32 v71, v71, s65, v69
	v_and_or_b32 v55, v56, s65, v55
	global_store_dwordx2 v[66:67], v[70:71], off
	global_store_dwordx2 v[66:67], v[54:55], off offset:512
	v_pk_mul_f32 v[36:37], v[36:37], v[68:69] op_sel_hi:[1,0]
	v_pk_mul_f32 v[34:35], v[34:35], v[68:69] op_sel_hi:[1,0]
	ds_read_b128 v[54:57], v1 offset:2048
	ds_read_b128 v[62:65], v1 offset:10240
	v_pk_mul_f32 v[70:71], v[46:47], v[34:35]
	v_pk_mul_f32 v[72:73], v[48:49], v[36:37]
	ds_read_b128 v[34:37], v1 offset:3072
	ds_read_b128 v[46:49], v1 offset:11264
	v_pk_mul_f32 v[26:27], v[26:27], v[68:69] op_sel_hi:[1,0]
	s_waitcnt lgkmcnt(2)
	v_pk_fma_f32 v[180:181], v[54:55], v[70:71], v[62:63]
	v_pk_mul_f32 v[26:27], v[38:39], v[26:27]
	v_bfe_u32 v54, v180, 16, 1
	s_waitcnt lgkmcnt(0)
	v_pk_fma_f32 v[176:177], v[34:35], v[26:27], v[46:47]
	v_pk_mul_f32 v[28:29], v[28:29], v[68:69] op_sel_hi:[1,0]
	v_bfe_u32 v26, v176, 16, 1
	v_add3_u32 v54, v180, v54, s64
	v_bfe_u32 v55, v181, 16, 1
	v_pk_mul_f32 v[28:29], v[40:41], v[28:29]
	v_add3_u32 v26, v176, v26, s64
	v_bfe_u32 v27, v177, 16, 1
	v_pk_fma_f32 v[178:179], v[56:57], v[72:73], v[64:65]
	v_lshrrev_b32_e32 v54, 16, v54
	v_add3_u32 v55, v181, v55, s64
	v_pk_fma_f32 v[174:175], v[36:37], v[28:29], v[48:49]
	v_lshrrev_b32_e32 v26, 16, v26
	v_add3_u32 v27, v177, v27, s64
	v_and_or_b32 v54, v55, s65, v54
	v_bfe_u32 v55, v178, 16, 1
	v_and_or_b32 v26, v27, s65, v26
	v_bfe_u32 v27, v174, 16, 1
	v_add3_u32 v55, v178, v55, s64
	v_bfe_u32 v56, v179, 16, 1
	v_add3_u32 v27, v174, v27, s64
	v_bfe_u32 v28, v175, 16, 1
	v_lshrrev_b32_e32 v55, 16, v55
	v_add3_u32 v56, v179, v56, s64
	v_lshrrev_b32_e32 v27, 16, v27
	v_add3_u32 v28, v175, v28, s64
	v_and_or_b32 v55, v56, s65, v55
	v_and_or_b32 v27, v28, s65, v27
	global_store_dwordx2 v[66:67], v[54:55], off offset:1024
	global_store_dwordx2 v[66:67], v[26:27], off offset:1536
	v_pk_mul_f32 v[20:21], v[20:21], v[68:69] op_sel_hi:[1,0]
	v_pk_mul_f32 v[18:19], v[18:19], v[68:69] op_sel_hi:[1,0]
	ds_read_b128 v[26:29], v1 offset:4096
	ds_read_b128 v[34:37], v1 offset:12288
	v_pk_mul_f32 v[38:39], v[30:31], v[18:19]
	v_pk_mul_f32 v[40:41], v[32:33], v[20:21]
	ds_read_b128 v[18:21], v1 offset:5120
	ds_read_b128 v[30:33], v1 offset:13312
	v_pk_mul_f32 v[10:11], v[10:11], v[68:69] op_sel_hi:[1,0]
	s_waitcnt lgkmcnt(2)
	v_pk_fma_f32 v[128:129], v[38:39], v[26:27], v[34:35]
	v_pk_mul_f32 v[10:11], v[22:23], v[10:11]
	v_bfe_u32 v26, v128, 16, 1
	s_waitcnt lgkmcnt(0)
	v_pk_fma_f32 v[124:125], v[10:11], v[18:19], v[30:31]
	v_pk_mul_f32 v[12:13], v[12:13], v[68:69] op_sel_hi:[1,0]
	v_bfe_u32 v10, v124, 16, 1
	v_add3_u32 v26, v128, v26, s64
	v_bfe_u32 v27, v129, 16, 1
	v_pk_mul_f32 v[12:13], v[24:25], v[12:13]
	v_add3_u32 v10, v124, v10, s64
	v_bfe_u32 v11, v125, 16, 1
	v_pk_fma_f32 v[126:127], v[40:41], v[28:29], v[36:37]
	v_lshrrev_b32_e32 v26, 16, v26
	v_add3_u32 v27, v129, v27, s64
	v_pk_fma_f32 v[122:123], v[12:13], v[20:21], v[32:33]
	v_lshrrev_b32_e32 v10, 16, v10
	v_add3_u32 v11, v125, v11, s64
	v_and_or_b32 v26, v27, s65, v26
	v_bfe_u32 v27, v126, 16, 1
	v_and_or_b32 v10, v11, s65, v10
	v_bfe_u32 v11, v122, 16, 1
	v_add3_u32 v27, v126, v27, s64
	v_bfe_u32 v28, v127, 16, 1
	v_add3_u32 v11, v122, v11, s64
	v_bfe_u32 v12, v123, 16, 1
	v_lshrrev_b32_e32 v27, 16, v27
	v_add3_u32 v28, v127, v28, s64
	v_lshrrev_b32_e32 v11, 16, v11
	v_add3_u32 v12, v123, v12, s64
	v_and_or_b32 v27, v28, s65, v27
	v_and_or_b32 v11, v12, s65, v11
	global_store_dwordx2 v[66:67], v[26:27], off offset:2048
	global_store_dwordx2 v[66:67], v[10:11], off offset:2560
	v_pk_mul_f32 v[8:9], v[8:9], v[68:69] op_sel_hi:[1,0]
	v_pk_mul_f32 v[6:7], v[6:7], v[68:69] op_sel_hi:[1,0]
	ds_read_b128 v[10:13], v1 offset:6144
	ds_read_b128 v[18:21], v1 offset:14336
	v_pk_mul_f32 v[22:23], v[14:15], v[6:7]
	v_pk_mul_f32 v[24:25], v[16:17], v[8:9]
	ds_read_b128 v[6:9], v1 offset:7168
	ds_read_b128 v[14:17], v1 offset:15360
	v_pk_mul_f32 v[2:3], v[2:3], v[68:69] op_sel_hi:[1,0]
	v_pk_mul_f32 v[4:5], v[4:5], v[68:69] op_sel_hi:[1,0]
	v_pk_mul_f32 v[2:3], v[58:59], v[2:3]
	v_pk_mul_f32 v[4:5], v[60:61], v[4:5]
	s_waitcnt lgkmcnt(0)
	v_pk_fma_f32 v[84:85], v[2:3], v[6:7], v[14:15]
	v_pk_fma_f32 v[82:83], v[4:5], v[8:9], v[16:17]
	v_bfe_u32 v2, v84, 16, 1
	v_add3_u32 v2, v84, v2, s64
	v_bfe_u32 v3, v85, 16, 1
	v_lshrrev_b32_e32 v2, 16, v2
	v_add3_u32 v3, v85, v3, s64
	v_and_or_b32 v2, v3, s65, v2
	v_bfe_u32 v3, v82, 16, 1
	v_add3_u32 v3, v82, v3, s64
	v_bfe_u32 v4, v83, 16, 1
	v_lshrrev_b32_e32 v3, 16, v3
	v_add3_u32 v4, v83, v4, s64
	v_and_or_b32 v3, v4, s65, v3
	v_and_b32_sdwa v4, v50, v202 dst_sel:DWORD dst_unused:UNUSED_PAD src0_sel:WORD_1 src1_sel:DWORD
	v_and_b32_sdwa v5, v52, v202 dst_sel:DWORD dst_unused:UNUSED_PAD src0_sel:WORD_1 src1_sel:DWORD
	v_add3_u32 v8, v50, v4, s64
	v_add3_u32 v9, v52, v5, s64
	v_and_b32_sdwa v4, v51, v202 dst_sel:DWORD dst_unused:UNUSED_PAD src0_sel:WORD_1 src1_sel:DWORD
	v_and_b32_sdwa v5, v53, v202 dst_sel:DWORD dst_unused:UNUSED_PAD src0_sel:WORD_1 src1_sel:DWORD
	v_add3_u32 v4, v51, v4, s64
	v_add3_u32 v6, v53, v5, s64
	v_pk_fma_f32 v[88:89], v[22:23], v[10:11], v[18:19]
	global_store_dwordx2 v[66:67], v[2:3], off offset:3584
	v_mov_b32_e32 v2, v52
	v_mov_b32_e32 v3, v50
	v_and_b32_e32 v5, 0xffff0000, v4
	v_and_b32_e32 v4, 0xffff0000, v6
	v_and_b32_e32 v7, 0xffff0000, v8
	v_and_b32_e32 v6, 0xffff0000, v9
	v_bfe_u32 v10, v88, 16, 1
	v_mov_b32_e32 v50, v53
	v_pk_add_f32 v[2:3], v[2:3], v[6:7] neg_lo:[0,1] neg_hi:[0,1]
	v_add3_u32 v10, v88, v10, s64
	v_bfe_u32 v11, v89, 16, 1
	v_pk_add_f32 v[6:7], v[50:51], v[4:5] neg_lo:[0,1] neg_hi:[0,1]
	v_or_b32_sdwa v22, v9, v4 dst_sel:DWORD dst_unused:UNUSED_PAD src0_sel:WORD_1 src1_sel:DWORD
	v_or_b32_sdwa v23, v8, v5 dst_sel:DWORD dst_unused:UNUSED_PAD src0_sel:WORD_1 src1_sel:DWORD
	v_and_b32_sdwa v4, v3, v202 dst_sel:DWORD dst_unused:UNUSED_PAD src0_sel:WORD_1 src1_sel:DWORD
	v_and_b32_sdwa v5, v2, v202 dst_sel:DWORD dst_unused:UNUSED_PAD src0_sel:WORD_1 src1_sel:DWORD
	v_pk_fma_f32 v[86:87], v[24:25], v[12:13], v[20:21]
	v_lshrrev_b32_e32 v10, 16, v10
	v_add3_u32 v11, v89, v11, s64
	v_add3_u32 v2, v2, v5, s64
	v_add3_u32 v3, v3, v4, s64
	v_and_b32_sdwa v4, v7, v202 dst_sel:DWORD dst_unused:UNUSED_PAD src0_sel:WORD_1 src1_sel:DWORD
	v_and_b32_sdwa v5, v6, v202 dst_sel:DWORD dst_unused:UNUSED_PAD src0_sel:WORD_1 src1_sel:DWORD
	s_add_u32 s4, s14, s44
	v_and_or_b32 v10, v11, s65, v10
	v_bfe_u32 v11, v86, 16, 1
	v_add3_u32 v4, v7, v4, s64
	v_add3_u32 v5, v6, v5, s64
	s_addc_u32 s5, s15, s45
	v_add3_u32 v11, v86, v11, s64
	v_bfe_u32 v12, v87, 16, 1
	v_and_b32_e32 v4, 0xffff0000, v4
	v_and_b32_e32 v5, 0xffff0000, v5
	s_add_u32 s6, s4, 0x30000
	v_lshrrev_b32_e32 v11, 16, v11
	v_add3_u32 v12, v87, v12, s64
	v_or_b32_sdwa v27, v4, v3 dst_sel:DWORD dst_unused:UNUSED_PAD src0_sel:DWORD src1_sel:WORD_1
	v_or_b32_sdwa v26, v5, v2 dst_sel:DWORD dst_unused:UNUSED_PAD src0_sel:DWORD src1_sel:WORD_1
	v_and_b32_sdwa v2, v42, v202 dst_sel:DWORD dst_unused:UNUSED_PAD src0_sel:WORD_1 src1_sel:DWORD
	v_and_b32_sdwa v3, v44, v202 dst_sel:DWORD dst_unused:UNUSED_PAD src0_sel:WORD_1 src1_sel:DWORD
	s_addc_u32 s7, s5, 0
	v_and_or_b32 v11, v12, s65, v11
	v_add3_u32 v16, v42, v2, s64
	v_add3_u32 v17, v44, v3, s64
	v_and_b32_sdwa v6, v43, v202 dst_sel:DWORD dst_unused:UNUSED_PAD src0_sel:WORD_1 src1_sel:DWORD
	v_lshl_add_u64 v[2:3], s[6:7], 0, v[168:169]
	s_add_u32 s6, s4, 0x10000
	global_store_dwordx2 v[66:67], v[10:11], off offset:3072
	v_mov_b32_e32 v10, v44
	v_mov_b32_e32 v11, v42
	v_and_b32_sdwa v12, v45, v202 dst_sel:DWORD dst_unused:UNUSED_PAD src0_sel:WORD_1 src1_sel:DWORD
	v_add3_u32 v13, v43, v6, s64
	v_and_b32_e32 v15, 0xffff0000, v16
	v_and_b32_e32 v14, 0xffff0000, v17
	s_addc_u32 s7, s5, 0
	v_add3_u32 v12, v45, v12, s64
	v_and_b32_e32 v13, 0xffff0000, v13
	v_pk_add_f32 v[14:15], v[10:11], v[14:15] neg_lo:[0,1] neg_hi:[0,1]
	s_add_u32 s8, s4, 0x40000
	v_mov_b32_e32 v42, v45
	v_and_b32_e32 v12, 0xffff0000, v12
	v_or_b32_sdwa v25, v16, v13 dst_sel:DWORD dst_unused:UNUSED_PAD src0_sel:WORD_1 src1_sel:DWORD
	v_and_b32_sdwa v16, v15, v202 dst_sel:DWORD dst_unused:UNUSED_PAD src0_sel:WORD_1 src1_sel:DWORD
	v_and_b32_sdwa v10, v14, v202 dst_sel:DWORD dst_unused:UNUSED_PAD src0_sel:WORD_1 src1_sel:DWORD
	s_addc_u32 s9, s5, 0
	v_pk_add_f32 v[18:19], v[42:43], v[12:13] neg_lo:[0,1] neg_hi:[0,1]
	v_add3_u32 v28, v14, v10, s64
	v_add3_u32 v20, v15, v16, s64
	v_lshl_add_u64 v[14:15], s[6:7], 0, v[168:169]
	s_add_u32 s6, s4, 0x20000
	v_and_b32_sdwa v21, v19, v202 dst_sel:DWORD dst_unused:UNUSED_PAD src0_sel:WORD_1 src1_sel:DWORD
	s_addc_u32 s7, s5, 0
	v_lshl_add_u64 v[10:11], s[8:9], 0, v[168:169]
	v_and_b32_sdwa v29, v18, v202 dst_sel:DWORD dst_unused:UNUSED_PAD src0_sel:WORD_1 src1_sel:DWORD
	v_add3_u32 v19, v19, v21, s64
	s_add_u32 s8, s4, 0x50000
	v_add3_u32 v18, v18, v29, s64
	v_and_b32_e32 v19, 0xffff0000, v19
	s_addc_u32 s9, s5, 0
	v_and_b32_e32 v30, 0xffff0000, v18
	v_or_b32_sdwa v29, v19, v20 dst_sel:DWORD dst_unused:UNUSED_PAD src0_sel:DWORD src1_sel:WORD_1
	v_lshl_add_u64 v[18:19], s[8:9], 0, v[168:169]
	global_load_dwordx4 v[2:5], v[2:3], off
	v_or_b32_sdwa v24, v17, v12 dst_sel:DWORD dst_unused:UNUSED_PAD src0_sel:WORD_1 src1_sel:DWORD
	global_load_dwordx4 v[10:13], v[10:11], off
	v_lshl_add_u64 v[6:7], s[4:5], 0, v[168:169]
	global_load_dwordx4 v[18:21], v[18:19], off
	ds_write2st64_b64 v205, v[22:23], v[24:25] offset0:38 offset1:39
	v_lshl_add_u64 v[22:23], s[6:7], 0, v[168:169]
	global_load_dwordx4 v[6:9], v[6:7], off
	s_add_u32 s6, s4, 64
	global_load_dwordx4 v[14:17], v[14:15], off
	s_addc_u32 s7, s5, 0
	global_load_dwordx4 v[22:25], v[22:23], off
	s_add_u32 s8, s4, 0x30040
	s_addc_u32 s9, s5, 0
	s_add_u32 s34, s4, 0x10040
	s_addc_u32 s35, s5, 0
	s_add_u32 s46, s4, 0x40040
	s_addc_u32 s47, s5, 0
	s_add_u32 s60, s4, 0x20040
	s_addc_u32 s61, s5, 0
	s_add_u32 s70, s4, 0x50040
	v_or_b32_sdwa v28, v30, v28 dst_sel:DWORD dst_unused:UNUSED_PAD src0_sel:DWORD src1_sel:WORD_1
	s_addc_u32 s71, s5, 0
	ds_write2st64_b64 v205, v[26:27], v[28:29] offset0:103 offset1:104
	v_lshl_add_u64 v[26:27], s[70:71], 0, v[168:169]
	global_load_dwordx4 v[30:33], v[26:27], off
	v_lshl_add_u64 v[26:27], s[60:61], 0, v[168:169]
	global_load_dwordx4 v[34:37], v[26:27], off
	v_lshl_add_u64 v[26:27], s[46:47], 0, v[168:169]
	global_load_dwordx4 v[38:41], v[26:27], off
	v_lshl_add_u64 v[26:27], s[34:35], 0, v[168:169]
	global_load_dwordx4 v[42:45], v[26:27], off
	v_lshl_add_u64 v[26:27], s[8:9], 0, v[168:169]
	global_load_dwordx4 v[46:49], v[26:27], off
	v_lshl_add_u64 v[26:27], s[6:7], 0, v[168:169]
	global_load_dwordx4 v[50:53], v[26:27], off
	s_waitcnt lgkmcnt(0)
	s_barrier
	ds_read_b128 v[26:29], v199 offset:49664
	ds_read_b128 v[54:57], v199 offset:49728
	s_waitcnt vmcnt(11) lgkmcnt(1)
	v_mfma_f32_16x16x32_bf16 v[58:61], v[26:29], v[2:5], 0
	ds_read_b128 v[62:65], v199 offset:16384
	ds_read_b128 v[66:69], v199 offset:16448
	s_add_u32 s6, s4, 0x400
	s_addc_u32 s7, s5, 0
	s_waitcnt vmcnt(10)
	v_mfma_f32_16x16x32_bf16 v[70:73], v[26:29], v[10:13], 0
	v_and_b32_sdwa v164, v150, v202 dst_sel:DWORD dst_unused:UNUSED_PAD src0_sel:WORD_1 src1_sel:DWORD
	v_add3_u32 v164, v150, v164, s64
	s_waitcnt vmcnt(9)
	v_mfma_f32_16x16x32_bf16 v[206:209], v[26:29], v[18:21], 0
	s_waitcnt vmcnt(8)
	v_mfma_f32_16x16x32_bf16 v[58:61], v[26:29], v[6:9], v[58:61]
	s_waitcnt vmcnt(7)
	v_mfma_f32_16x16x32_bf16 v[70:73], v[26:29], v[14:17], v[70:73]
	s_waitcnt vmcnt(6)
	v_mfma_f32_16x16x32_bf16 v[26:29], v[26:29], v[22:25], v[206:209]
	s_waitcnt lgkmcnt(1)
	v_mfma_f32_16x16x32_bf16 v[58:61], v[62:65], v[2:5], v[58:61]
	v_mfma_f32_16x16x32_bf16 v[70:73], v[62:65], v[10:13], v[70:73]
	v_mfma_f32_16x16x32_bf16 v[26:29], v[62:65], v[18:21], v[26:29]
	v_mfma_f32_16x16x32_bf16 v[58:61], v[62:65], v[6:9], v[58:61]
	v_mfma_f32_16x16x32_bf16 v[70:73], v[62:65], v[14:17], v[70:73]
	v_mfma_f32_16x16x32_bf16 v[62:65], v[62:65], v[22:25], v[26:29]
	s_nop 4
	ds_read_b128 v[26:29], v200 offset:49664
	ds_read_b128 v[206:209], v200 offset:49728
	ds_read_b128 v[214:217], v199 offset:33024
	ds_read_b128 v[218:221], v199 offset:33088
	s_waitcnt lgkmcnt(0)
	v_mfma_f32_16x16x32_bf16 v[210:213], v[26:29], v[2:5], 0
	s_barrier
	v_mfma_f32_16x16x32_bf16 v[210:213], v[26:29], v[6:9], v[210:213]
	v_mfma_f32_16x16x32_bf16 v[2:5], v[214:217], v[2:5], v[210:213]
	v_mfma_f32_16x16x32_bf16 v[2:5], v[214:217], v[6:9], v[2:5]
	v_mfma_f32_16x16x32_bf16 v[6:9], v[26:29], v[10:13], 0
	v_mfma_f32_16x16x32_bf16 v[6:9], v[26:29], v[14:17], v[6:9]
	v_mfma_f32_16x16x32_bf16 v[6:9], v[214:217], v[10:13], v[6:9]
	v_mfma_f32_16x16x32_bf16 v[10:13], v[26:29], v[18:21], 0
	v_mfma_f32_16x16x32_bf16 v[10:13], v[26:29], v[22:25], v[10:13]
	v_mfma_f32_16x16x32_bf16 v[10:13], v[214:217], v[18:21], v[10:13]
	v_mfma_f32_16x16x32_bf16 v[6:9], v[214:217], v[14:17], v[6:9]
	v_mfma_f32_16x16x32_bf16 v[14:17], v[214:217], v[22:25], v[10:13]
	s_waitcnt vmcnt(1)
	v_mfma_f32_16x16x32_bf16 v[10:13], v[54:57], v[46:49], v[58:61]
	s_waitcnt vmcnt(0)
	v_mfma_f32_16x16x32_bf16 v[10:13], v[54:57], v[50:53], v[10:13]
	v_mfma_f32_16x16x32_bf16 v[10:13], v[66:69], v[46:49], v[10:13]
	v_mfma_f32_16x16x32_bf16 v[26:29], v[66:69], v[50:53], v[10:13]
	v_mfma_f32_16x16x32_bf16 v[10:13], v[54:57], v[38:41], v[70:73]
	v_mfma_f32_16x16x32_bf16 v[10:13], v[54:57], v[42:45], v[10:13]
	v_mfma_f32_16x16x32_bf16 v[10:13], v[66:69], v[38:41], v[10:13]
	v_mfma_f32_16x16x32_bf16 v[18:21], v[66:69], v[42:45], v[10:13]
	v_mfma_f32_16x16x32_bf16 v[10:13], v[54:57], v[30:33], v[62:65]
	v_mfma_f32_16x16x32_bf16 v[2:5], v[206:209], v[46:49], v[2:5]
	v_mfma_f32_16x16x32_bf16 v[10:13], v[54:57], v[34:37], v[10:13]
	v_mfma_f32_16x16x32_bf16 v[2:5], v[206:209], v[50:53], v[2:5]
	v_mfma_f32_16x16x32_bf16 v[10:13], v[66:69], v[30:33], v[10:13]
	v_mfma_f32_16x16x32_bf16 v[2:5], v[218:221], v[46:49], v[2:5]
	v_mfma_f32_16x16x32_bf16 v[22:25], v[66:69], v[34:37], v[10:13]
	v_mfma_f32_16x16x32_bf16 v[10:13], v[218:221], v[50:53], v[2:5]
	v_mfma_f32_16x16x32_bf16 v[2:5], v[206:209], v[38:41], v[6:9]
	v_mfma_f32_16x16x32_bf16 v[6:9], v[206:209], v[30:33], v[14:17]
	v_mfma_f32_16x16x32_bf16 v[6:9], v[206:209], v[34:37], v[6:9]
	s_nop 1
	v_lshl_add_u64 v[14:15], s[6:7], 0, v[168:169]
	s_add_u32 s6, s4, 0x30400
	s_addc_u32 s7, s5, 0
	v_mfma_f32_16x16x32_bf16 v[2:5], v[206:209], v[42:45], v[2:5]
	global_load_dwordx4 v[14:17], v[14:15], off
	v_and_b32_sdwa v208, v152, v202 dst_sel:DWORD dst_unused:UNUSED_PAD src0_sel:WORD_1 src1_sel:DWORD
	v_mov_b32_e32 v206, v152
	v_mfma_f32_16x16x32_bf16 v[6:9], v[218:221], v[30:33], v[6:9]
	v_lshl_add_u64 v[30:31], s[6:7], 0, v[168:169]
	s_add_u32 s6, s4, 0x10400
	s_addc_u32 s7, s5, 0
	v_mfma_f32_16x16x32_bf16 v[2:5], v[218:221], v[38:41], v[2:5]
	global_load_dwordx4 v[30:33], v[30:31], off
	v_add3_u32 v210, v152, v208, s64
	v_and_b32_sdwa v152, v151, v202 dst_sel:DWORD dst_unused:UNUSED_PAD src0_sel:WORD_1 src1_sel:DWORD
	v_mfma_f32_16x16x32_bf16 v[6:9], v[218:221], v[34:37], v[6:9]
	v_lshl_add_u64 v[34:35], s[6:7], 0, v[168:169]
	s_add_u32 s6, s4, 0x40400
	s_addc_u32 s7, s5, 0
	v_lshl_add_u64 v[38:39], s[6:7], 0, v[168:169]
	s_add_u32 s6, s4, 0x20400
	s_addc_u32 s7, s5, 0
	v_mfma_f32_16x16x32_bf16 v[2:5], v[218:221], v[42:45], v[2:5]
	global_load_dwordx4 v[42:45], v[38:39], off
	v_lshl_add_u64 v[38:39], s[6:7], 0, v[168:169]
	s_add_u32 s6, s4, 0x50400
	s_addc_u32 s7, s5, 0
	global_load_dwordx4 v[46:49], v[38:39], off
	v_lshl_add_u64 v[38:39], s[6:7], 0, v[168:169]
	global_load_dwordx4 v[58:61], v[38:39], off
	v_and_b32_sdwa v208, v153, v202 dst_sel:DWORD dst_unused:UNUSED_PAD src0_sel:WORD_1 src1_sel:DWORD
	global_load_dwordx4 v[34:37], v[34:35], off
	v_add3_u32 v152, v151, v152, s64
	v_add3_u32 v208, v153, v208, s64
	v_mov_b32_e32 v207, v150
	v_mov_b32_e32 v150, v153
	v_and_b32_e32 v153, 0xffff0000, v152
	v_and_b32_e32 v152, 0xffff0000, v208
	v_and_b32_e32 v209, 0xffff0000, v164
	v_and_b32_e32 v208, 0xffff0000, v210
	s_add_u32 s6, s4, 0x440
	v_pk_add_f32 v[206:207], v[206:207], v[208:209] neg_lo:[0,1] neg_hi:[0,1]
	s_addc_u32 s7, s5, 0
	v_pk_add_f32 v[150:151], v[150:151], v[152:153] neg_lo:[0,1] neg_hi:[0,1]
	v_or_b32_sdwa v153, v164, v153 dst_sel:DWORD dst_unused:UNUSED_PAD src0_sel:WORD_1 src1_sel:DWORD
	v_and_b32_sdwa v164, v207, v202 dst_sel:DWORD dst_unused:UNUSED_PAD src0_sel:WORD_1 src1_sel:DWORD
	v_and_b32_sdwa v208, v206, v202 dst_sel:DWORD dst_unused:UNUSED_PAD src0_sel:WORD_1 src1_sel:DWORD
	v_lshl_add_u64 v[38:39], s[6:7], 0, v[168:169]
	s_add_u32 s6, s4, 0x30440
	v_add3_u32 v206, v206, v208, s64
	v_add3_u32 v164, v207, v164, s64
	v_and_b32_sdwa v207, v151, v202 dst_sel:DWORD dst_unused:UNUSED_PAD src0_sel:WORD_1 src1_sel:DWORD
	v_and_b32_sdwa v208, v150, v202 dst_sel:DWORD dst_unused:UNUSED_PAD src0_sel:WORD_1 src1_sel:DWORD
	s_addc_u32 s7, s5, 0
	v_add3_u32 v151, v151, v207, s64
	v_add3_u32 v150, v150, v208, s64
	v_lshl_add_u64 v[50:51], s[6:7], 0, v[168:169]
	s_add_u32 s6, s4, 0x10440
	v_and_b32_e32 v151, 0xffff0000, v151
	v_and_b32_e32 v150, 0xffff0000, v150
	v_and_b32_sdwa v208, v148, v202 dst_sel:DWORD dst_unused:UNUSED_PAD src0_sel:WORD_1 src1_sel:DWORD
	s_addc_u32 s7, s5, 0
	v_or_b32_sdwa v152, v210, v152 dst_sel:DWORD dst_unused:UNUSED_PAD src0_sel:WORD_1 src1_sel:DWORD
	v_or_b32_sdwa v151, v151, v164 dst_sel:DWORD dst_unused:UNUSED_PAD src0_sel:DWORD src1_sel:WORD_1
	v_or_b32_sdwa v150, v150, v206 dst_sel:DWORD dst_unused:UNUSED_PAD src0_sel:DWORD src1_sel:WORD_1
	v_mov_b32_e32 v206, v148
	v_and_b32_sdwa v164, v146, v202 dst_sel:DWORD dst_unused:UNUSED_PAD src0_sel:WORD_1 src1_sel:DWORD
	v_add3_u32 v210, v148, v208, s64
	v_and_b32_sdwa v148, v147, v202 dst_sel:DWORD dst_unused:UNUSED_PAD src0_sel:WORD_1 src1_sel:DWORD
	v_and_b32_sdwa v208, v149, v202 dst_sel:DWORD dst_unused:UNUSED_PAD src0_sel:WORD_1 src1_sel:DWORD
	v_lshl_add_u64 v[54:55], s[6:7], 0, v[168:169]
	s_add_u32 s6, s4, 0x40440
	v_add3_u32 v164, v146, v164, s64
	v_add3_u32 v148, v147, v148, s64
	v_add3_u32 v208, v149, v208, s64
	s_addc_u32 s7, s5, 0
	v_mov_b32_e32 v207, v146
	v_mov_b32_e32 v146, v149
	v_and_b32_e32 v149, 0xffff0000, v148
	v_and_b32_e32 v148, 0xffff0000, v208
	v_and_b32_e32 v209, 0xffff0000, v164
	v_and_b32_e32 v208, 0xffff0000, v210
	v_lshl_add_u64 v[62:63], s[6:7], 0, v[168:169]
	s_add_u32 s6, s4, 0x20440
	v_pk_add_f32 v[206:207], v[206:207], v[208:209] neg_lo:[0,1] neg_hi:[0,1]
	s_addc_u32 s7, s5, 0
	v_pk_add_f32 v[146:147], v[146:147], v[148:149] neg_lo:[0,1] neg_hi:[0,1]
	v_or_b32_sdwa v149, v164, v149 dst_sel:DWORD dst_unused:UNUSED_PAD src0_sel:WORD_1 src1_sel:DWORD
	v_and_b32_sdwa v164, v207, v202 dst_sel:DWORD dst_unused:UNUSED_PAD src0_sel:WORD_1 src1_sel:DWORD
	v_and_b32_sdwa v208, v206, v202 dst_sel:DWORD dst_unused:UNUSED_PAD src0_sel:WORD_1 src1_sel:DWORD
	v_lshl_add_u64 v[66:67], s[6:7], 0, v[168:169]
	s_add_u32 s6, s4, 0x50440
	v_add3_u32 v206, v206, v208, s64
	v_add3_u32 v164, v207, v164, s64
	v_and_b32_sdwa v207, v147, v202 dst_sel:DWORD dst_unused:UNUSED_PAD src0_sel:WORD_1 src1_sel:DWORD
	v_and_b32_sdwa v208, v146, v202 dst_sel:DWORD dst_unused:UNUSED_PAD src0_sel:WORD_1 src1_sel:DWORD
	s_addc_u32 s7, s5, 0
	v_add3_u32 v147, v147, v207, s64
	v_add3_u32 v146, v146, v208, s64
	v_lshl_add_u64 v[70:71], s[6:7], 0, v[168:169]
	v_or_b32_sdwa v148, v210, v148 dst_sel:DWORD dst_unused:UNUSED_PAD src0_sel:WORD_1 src1_sel:DWORD
	v_and_b32_e32 v147, 0xffff0000, v147
	v_and_b32_e32 v146, 0xffff0000, v146
	global_load_dwordx4 v[38:41], v[38:39], off
	v_or_b32_sdwa v147, v147, v164 dst_sel:DWORD dst_unused:UNUSED_PAD src0_sel:DWORD src1_sel:WORD_1
	global_load_dwordx4 v[50:53], v[50:51], off
	v_or_b32_sdwa v146, v146, v206 dst_sel:DWORD dst_unused:UNUSED_PAD src0_sel:DWORD src1_sel:WORD_1
	global_load_dwordx4 v[54:57], v[54:55], off
	s_add_u32 s6, s4, 0x800
	global_load_dwordx4 v[62:65], v[62:63], off
	s_addc_u32 s7, s5, 0
	global_load_dwordx4 v[66:69], v[66:67], off
	s_nop 0
	global_load_dwordx4 v[70:73], v[70:71], off
	ds_write2st64_b64 v198, v[152:153], v[148:149] offset0:32 offset1:33
	ds_write2st64_b64 v198, v[150:151], v[146:147] offset0:97 offset1:98
	v_and_b32_sdwa v148, v118, v202 dst_sel:DWORD dst_unused:UNUSED_PAD src0_sel:WORD_1 src1_sel:DWORD
	v_and_b32_sdwa v149, v120, v202 dst_sel:DWORD dst_unused:UNUSED_PAD src0_sel:WORD_1 src1_sel:DWORD
	v_mov_b32_e32 v146, v120
	v_add3_u32 v150, v118, v148, s64
	v_add3_u32 v151, v120, v149, s64
	v_and_b32_sdwa v120, v119, v202 dst_sel:DWORD dst_unused:UNUSED_PAD src0_sel:WORD_1 src1_sel:DWORD
	v_and_b32_sdwa v148, v121, v202 dst_sel:DWORD dst_unused:UNUSED_PAD src0_sel:WORD_1 src1_sel:DWORD
	v_add3_u32 v120, v119, v120, s64
	v_add3_u32 v148, v121, v148, s64
	v_mov_b32_e32 v147, v118
	v_mov_b32_e32 v118, v121
	v_and_b32_e32 v121, 0xffff0000, v120
	v_and_b32_e32 v120, 0xffff0000, v148
	v_and_b32_e32 v149, 0xffff0000, v150
	v_and_b32_e32 v148, 0xffff0000, v151
	v_pk_add_f32 v[146:147], v[146:147], v[148:149] neg_lo:[0,1] neg_hi:[0,1]
	v_pk_add_f32 v[118:119], v[118:119], v[120:121] neg_lo:[0,1] neg_hi:[0,1]
	v_and_b32_sdwa v149, v146, v202 dst_sel:DWORD dst_unused:UNUSED_PAD src0_sel:WORD_1 src1_sel:DWORD
	v_and_b32_sdwa v148, v147, v202 dst_sel:DWORD dst_unused:UNUSED_PAD src0_sel:WORD_1 src1_sel:DWORD
	v_add3_u32 v146, v146, v149, s64
	v_and_b32_sdwa v149, v118, v202 dst_sel:DWORD dst_unused:UNUSED_PAD src0_sel:WORD_1 src1_sel:DWORD
	v_add3_u32 v147, v147, v148, s64
	v_and_b32_sdwa v148, v119, v202 dst_sel:DWORD dst_unused:UNUSED_PAD src0_sel:WORD_1 src1_sel:DWORD
	v_add3_u32 v118, v118, v149, s64
	v_add3_u32 v119, v119, v148, s64
	v_and_b32_e32 v118, 0xffff0000, v118
	v_and_b32_sdwa v148, v114, v202 dst_sel:DWORD dst_unused:UNUSED_PAD src0_sel:WORD_1 src1_sel:DWORD
	v_and_b32_sdwa v149, v116, v202 dst_sel:DWORD dst_unused:UNUSED_PAD src0_sel:WORD_1 src1_sel:DWORD
	v_or_b32_sdwa v120, v151, v120 dst_sel:DWORD dst_unused:UNUSED_PAD src0_sel:WORD_1 src1_sel:DWORD
	v_or_b32_sdwa v121, v150, v121 dst_sel:DWORD dst_unused:UNUSED_PAD src0_sel:WORD_1 src1_sel:DWORD
	v_or_b32_sdwa v118, v118, v146 dst_sel:DWORD dst_unused:UNUSED_PAD src0_sel:DWORD src1_sel:WORD_1
	v_mov_b32_e32 v146, v116
	v_add3_u32 v150, v114, v148, s64
	v_add3_u32 v151, v116, v149, s64
	v_and_b32_sdwa v116, v115, v202 dst_sel:DWORD dst_unused:UNUSED_PAD src0_sel:WORD_1 src1_sel:DWORD
	v_and_b32_sdwa v148, v117, v202 dst_sel:DWORD dst_unused:UNUSED_PAD src0_sel:WORD_1 src1_sel:DWORD
	v_and_b32_e32 v119, 0xffff0000, v119
	v_add3_u32 v116, v115, v116, s64
	v_add3_u32 v148, v117, v148, s64
	v_or_b32_sdwa v119, v119, v147 dst_sel:DWORD dst_unused:UNUSED_PAD src0_sel:DWORD src1_sel:WORD_1
	v_mov_b32_e32 v147, v114
	v_mov_b32_e32 v114, v117
	v_and_b32_e32 v117, 0xffff0000, v116
	v_and_b32_e32 v116, 0xffff0000, v148
	v_and_b32_e32 v149, 0xffff0000, v150
	v_and_b32_e32 v148, 0xffff0000, v151
	v_pk_add_f32 v[146:147], v[146:147], v[148:149] neg_lo:[0,1] neg_hi:[0,1]
	v_pk_add_f32 v[114:115], v[114:115], v[116:117] neg_lo:[0,1] neg_hi:[0,1]
	v_and_b32_sdwa v148, v147, v202 dst_sel:DWORD dst_unused:UNUSED_PAD src0_sel:WORD_1 src1_sel:DWORD
	v_and_b32_sdwa v149, v146, v202 dst_sel:DWORD dst_unused:UNUSED_PAD src0_sel:WORD_1 src1_sel:DWORD
	v_add3_u32 v146, v146, v149, s64
	v_add3_u32 v147, v147, v148, s64
	v_and_b32_sdwa v148, v115, v202 dst_sel:DWORD dst_unused:UNUSED_PAD src0_sel:WORD_1 src1_sel:DWORD
	v_and_b32_sdwa v149, v114, v202 dst_sel:DWORD dst_unused:UNUSED_PAD src0_sel:WORD_1 src1_sel:DWORD
	v_add3_u32 v115, v115, v148, s64
	v_add3_u32 v114, v114, v149, s64
	v_or_b32_sdwa v116, v151, v116 dst_sel:DWORD dst_unused:UNUSED_PAD src0_sel:WORD_1 src1_sel:DWORD
	v_or_b32_sdwa v117, v150, v117 dst_sel:DWORD dst_unused:UNUSED_PAD src0_sel:WORD_1 src1_sel:DWORD
	v_and_b32_e32 v115, 0xffff0000, v115
	v_and_b32_e32 v114, 0xffff0000, v114
	v_or_b32_sdwa v115, v115, v147 dst_sel:DWORD dst_unused:UNUSED_PAD src0_sel:DWORD src1_sel:WORD_1
	v_or_b32_sdwa v114, v114, v146 dst_sel:DWORD dst_unused:UNUSED_PAD src0_sel:DWORD src1_sel:WORD_1
	ds_write2st64_b64 v203, v[120:121], v[116:117] offset0:34 offset1:35
	ds_write2st64_b64 v203, v[118:119], v[114:115] offset0:99 offset1:100
	v_and_b32_sdwa v116, v158, v202 dst_sel:DWORD dst_unused:UNUSED_PAD src0_sel:WORD_1 src1_sel:DWORD
	v_and_b32_sdwa v117, v160, v202 dst_sel:DWORD dst_unused:UNUSED_PAD src0_sel:WORD_1 src1_sel:DWORD
	v_add3_u32 v120, v158, v116, s64
	v_add3_u32 v121, v160, v117, s64
	v_and_b32_sdwa v116, v159, v202 dst_sel:DWORD dst_unused:UNUSED_PAD src0_sel:WORD_1 src1_sel:DWORD
	v_and_b32_sdwa v117, v161, v202 dst_sel:DWORD dst_unused:UNUSED_PAD src0_sel:WORD_1 src1_sel:DWORD
	v_add3_u32 v116, v159, v116, s64
	v_add3_u32 v118, v161, v117, s64
	v_mov_b32_e32 v114, v160
	v_mov_b32_e32 v115, v158
	v_and_b32_e32 v117, 0xffff0000, v116
	v_and_b32_e32 v116, 0xffff0000, v118
	v_and_b32_e32 v119, 0xffff0000, v120
	v_and_b32_e32 v118, 0xffff0000, v121
	v_mov_b32_e32 v158, v161
	v_pk_add_f32 v[114:115], v[114:115], v[118:119] neg_lo:[0,1] neg_hi:[0,1]
	v_pk_add_f32 v[118:119], v[158:159], v[116:117] neg_lo:[0,1] neg_hi:[0,1]
	v_or_b32_sdwa v116, v121, v116 dst_sel:DWORD dst_unused:UNUSED_PAD src0_sel:WORD_1 src1_sel:DWORD
	v_or_b32_sdwa v117, v120, v117 dst_sel:DWORD dst_unused:UNUSED_PAD src0_sel:WORD_1 src1_sel:DWORD
	v_and_b32_sdwa v120, v115, v202 dst_sel:DWORD dst_unused:UNUSED_PAD src0_sel:WORD_1 src1_sel:DWORD
	v_and_b32_sdwa v121, v114, v202 dst_sel:DWORD dst_unused:UNUSED_PAD src0_sel:WORD_1 src1_sel:DWORD
	v_add3_u32 v114, v114, v121, s64
	v_add3_u32 v115, v115, v120, s64
	v_and_b32_sdwa v120, v119, v202 dst_sel:DWORD dst_unused:UNUSED_PAD src0_sel:WORD_1 src1_sel:DWORD
	v_and_b32_sdwa v121, v118, v202 dst_sel:DWORD dst_unused:UNUSED_PAD src0_sel:WORD_1 src1_sel:DWORD
	v_add3_u32 v119, v119, v120, s64
	v_add3_u32 v118, v118, v121, s64
	v_and_b32_sdwa v120, v154, v202 dst_sel:DWORD dst_unused:UNUSED_PAD src0_sel:WORD_1 src1_sel:DWORD
	v_and_b32_sdwa v121, v156, v202 dst_sel:DWORD dst_unused:UNUSED_PAD src0_sel:WORD_1 src1_sel:DWORD
	v_add3_u32 v148, v154, v120, s64
	v_add3_u32 v149, v156, v121, s64
	v_and_b32_sdwa v120, v155, v202 dst_sel:DWORD dst_unused:UNUSED_PAD src0_sel:WORD_1 src1_sel:DWORD
	v_and_b32_sdwa v121, v157, v202 dst_sel:DWORD dst_unused:UNUSED_PAD src0_sel:WORD_1 src1_sel:DWORD
	v_and_b32_e32 v119, 0xffff0000, v119
	v_and_b32_e32 v118, 0xffff0000, v118
	v_add3_u32 v120, v155, v120, s64
	v_add3_u32 v146, v157, v121, s64
	v_or_b32_sdwa v115, v119, v115 dst_sel:DWORD dst_unused:UNUSED_PAD src0_sel:DWORD src1_sel:WORD_1
	v_or_b32_sdwa v114, v118, v114 dst_sel:DWORD dst_unused:UNUSED_PAD src0_sel:DWORD src1_sel:WORD_1
	v_mov_b32_e32 v118, v156
	v_mov_b32_e32 v119, v154
	v_and_b32_e32 v121, 0xffff0000, v120
	v_and_b32_e32 v120, 0xffff0000, v146
	v_and_b32_e32 v147, 0xffff0000, v148
	v_and_b32_e32 v146, 0xffff0000, v149
	v_mov_b32_e32 v154, v157
	v_pk_add_f32 v[118:119], v[118:119], v[146:147] neg_lo:[0,1] neg_hi:[0,1]
	v_pk_add_f32 v[146:147], v[154:155], v[120:121] neg_lo:[0,1] neg_hi:[0,1]
	v_or_b32_sdwa v120, v149, v120 dst_sel:DWORD dst_unused:UNUSED_PAD src0_sel:WORD_1 src1_sel:DWORD
	v_or_b32_sdwa v121, v148, v121 dst_sel:DWORD dst_unused:UNUSED_PAD src0_sel:WORD_1 src1_sel:DWORD
	v_and_b32_sdwa v148, v119, v202 dst_sel:DWORD dst_unused:UNUSED_PAD src0_sel:WORD_1 src1_sel:DWORD
	v_and_b32_sdwa v149, v118, v202 dst_sel:DWORD dst_unused:UNUSED_PAD src0_sel:WORD_1 src1_sel:DWORD
	v_add3_u32 v118, v118, v149, s64
	v_add3_u32 v119, v119, v148, s64
	v_and_b32_sdwa v148, v147, v202 dst_sel:DWORD dst_unused:UNUSED_PAD src0_sel:WORD_1 src1_sel:DWORD
	v_and_b32_sdwa v149, v146, v202 dst_sel:DWORD dst_unused:UNUSED_PAD src0_sel:WORD_1 src1_sel:DWORD
	v_add3_u32 v147, v147, v148, s64
	v_add3_u32 v146, v146, v149, s64
	v_and_b32_e32 v147, 0xffff0000, v147
	v_and_b32_e32 v146, 0xffff0000, v146
	v_or_b32_sdwa v119, v147, v119 dst_sel:DWORD dst_unused:UNUSED_PAD src0_sel:DWORD src1_sel:WORD_1
	v_or_b32_sdwa v118, v146, v118 dst_sel:DWORD dst_unused:UNUSED_PAD src0_sel:DWORD src1_sel:WORD_1
	ds_write2st64_b64 v204, v[116:117], v[120:121] offset0:36 offset1:37
	ds_write2st64_b64 v204, v[114:115], v[118:119] offset0:101 offset1:102
	v_and_b32_sdwa v116, v178, v202 dst_sel:DWORD dst_unused:UNUSED_PAD src0_sel:WORD_1 src1_sel:DWORD
	v_and_b32_sdwa v117, v180, v202 dst_sel:DWORD dst_unused:UNUSED_PAD src0_sel:WORD_1 src1_sel:DWORD
	v_add3_u32 v120, v178, v116, s64
	v_add3_u32 v121, v180, v117, s64
	v_and_b32_sdwa v116, v179, v202 dst_sel:DWORD dst_unused:UNUSED_PAD src0_sel:WORD_1 src1_sel:DWORD
	v_and_b32_sdwa v117, v181, v202 dst_sel:DWORD dst_unused:UNUSED_PAD src0_sel:WORD_1 src1_sel:DWORD
	v_add3_u32 v116, v179, v116, s64
	v_add3_u32 v118, v181, v117, s64
	v_mov_b32_e32 v114, v180
	v_mov_b32_e32 v115, v178
	v_and_b32_e32 v117, 0xffff0000, v116
	v_and_b32_e32 v116, 0xffff0000, v118
	v_and_b32_e32 v119, 0xffff0000, v120
	v_and_b32_e32 v118, 0xffff0000, v121
	v_mov_b32_e32 v178, v181
	v_pk_add_f32 v[114:115], v[114:115], v[118:119] neg_lo:[0,1] neg_hi:[0,1]
	v_pk_add_f32 v[118:119], v[178:179], v[116:117] neg_lo:[0,1] neg_hi:[0,1]
	v_or_b32_sdwa v116, v121, v116 dst_sel:DWORD dst_unused:UNUSED_PAD src0_sel:WORD_1 src1_sel:DWORD
	v_or_b32_sdwa v117, v120, v117 dst_sel:DWORD dst_unused:UNUSED_PAD src0_sel:WORD_1 src1_sel:DWORD
	v_and_b32_sdwa v120, v115, v202 dst_sel:DWORD dst_unused:UNUSED_PAD src0_sel:WORD_1 src1_sel:DWORD
	v_and_b32_sdwa v121, v114, v202 dst_sel:DWORD dst_unused:UNUSED_PAD src0_sel:WORD_1 src1_sel:DWORD
	v_add3_u32 v114, v114, v121, s64
	v_add3_u32 v115, v115, v120, s64
	v_and_b32_sdwa v120, v119, v202 dst_sel:DWORD dst_unused:UNUSED_PAD src0_sel:WORD_1 src1_sel:DWORD
	v_and_b32_sdwa v121, v118, v202 dst_sel:DWORD dst_unused:UNUSED_PAD src0_sel:WORD_1 src1_sel:DWORD
	v_add3_u32 v119, v119, v120, s64
	v_add3_u32 v118, v118, v121, s64
	v_and_b32_sdwa v120, v174, v202 dst_sel:DWORD dst_unused:UNUSED_PAD src0_sel:WORD_1 src1_sel:DWORD
	v_and_b32_sdwa v121, v176, v202 dst_sel:DWORD dst_unused:UNUSED_PAD src0_sel:WORD_1 src1_sel:DWORD
	v_add3_u32 v148, v174, v120, s64
	v_add3_u32 v149, v176, v121, s64
	v_and_b32_sdwa v120, v175, v202 dst_sel:DWORD dst_unused:UNUSED_PAD src0_sel:WORD_1 src1_sel:DWORD
	v_and_b32_sdwa v121, v177, v202 dst_sel:DWORD dst_unused:UNUSED_PAD src0_sel:WORD_1 src1_sel:DWORD
	v_and_b32_e32 v119, 0xffff0000, v119
	v_and_b32_e32 v118, 0xffff0000, v118
	v_add3_u32 v120, v175, v120, s64
	v_add3_u32 v146, v177, v121, s64
	v_or_b32_sdwa v115, v119, v115 dst_sel:DWORD dst_unused:UNUSED_PAD src0_sel:DWORD src1_sel:WORD_1
	v_or_b32_sdwa v114, v118, v114 dst_sel:DWORD dst_unused:UNUSED_PAD src0_sel:DWORD src1_sel:WORD_1
	v_mov_b32_e32 v118, v176
	v_mov_b32_e32 v119, v174
	v_and_b32_e32 v121, 0xffff0000, v120
	v_and_b32_e32 v120, 0xffff0000, v146
	v_and_b32_e32 v147, 0xffff0000, v148
	v_and_b32_e32 v146, 0xffff0000, v149
	v_mov_b32_e32 v174, v177
	v_pk_add_f32 v[118:119], v[118:119], v[146:147] neg_lo:[0,1] neg_hi:[0,1]
	v_pk_add_f32 v[146:147], v[174:175], v[120:121] neg_lo:[0,1] neg_hi:[0,1]
	v_or_b32_sdwa v120, v149, v120 dst_sel:DWORD dst_unused:UNUSED_PAD src0_sel:WORD_1 src1_sel:DWORD
	v_or_b32_sdwa v121, v148, v121 dst_sel:DWORD dst_unused:UNUSED_PAD src0_sel:WORD_1 src1_sel:DWORD
	v_and_b32_sdwa v148, v119, v202 dst_sel:DWORD dst_unused:UNUSED_PAD src0_sel:WORD_1 src1_sel:DWORD
	v_and_b32_sdwa v149, v118, v202 dst_sel:DWORD dst_unused:UNUSED_PAD src0_sel:WORD_1 src1_sel:DWORD
	v_add3_u32 v118, v118, v149, s64
	v_add3_u32 v119, v119, v148, s64
	v_and_b32_sdwa v148, v147, v202 dst_sel:DWORD dst_unused:UNUSED_PAD src0_sel:WORD_1 src1_sel:DWORD
	v_and_b32_sdwa v149, v146, v202 dst_sel:DWORD dst_unused:UNUSED_PAD src0_sel:WORD_1 src1_sel:DWORD
	v_add3_u32 v147, v147, v148, s64
	v_add3_u32 v146, v146, v149, s64
	v_and_b32_e32 v147, 0xffff0000, v147
	v_and_b32_e32 v146, 0xffff0000, v146
	v_or_b32_sdwa v119, v147, v119 dst_sel:DWORD dst_unused:UNUSED_PAD src0_sel:DWORD src1_sel:WORD_1
	v_or_b32_sdwa v118, v146, v118 dst_sel:DWORD dst_unused:UNUSED_PAD src0_sel:DWORD src1_sel:WORD_1
	ds_write2st64_b64 v205, v[116:117], v[120:121] offset0:38 offset1:39
	ds_write2st64_b64 v205, v[114:115], v[118:119] offset0:103 offset1:104
	s_waitcnt lgkmcnt(0)
	s_barrier
	ds_read_b128 v[114:117], v199 offset:49664
	ds_read_b128 v[118:121], v199 offset:49728
	s_waitcnt vmcnt(10) lgkmcnt(1)
	v_mfma_f32_16x16x32_bf16 v[26:29], v[114:117], v[30:33], v[26:29]
	ds_read_b128 v[146:149], v199 offset:16384
	ds_read_b128 v[150:153], v199 offset:16448
	s_waitcnt vmcnt(9)
	v_mfma_f32_16x16x32_bf16 v[18:21], v[114:117], v[42:45], v[18:21]
	s_waitcnt vmcnt(7)
	v_mfma_f32_16x16x32_bf16 v[22:25], v[114:117], v[58:61], v[22:25]
	v_mfma_f32_16x16x32_bf16 v[26:29], v[114:117], v[14:17], v[26:29]
	s_waitcnt vmcnt(6)
	v_mfma_f32_16x16x32_bf16 v[18:21], v[114:117], v[34:37], v[18:21]
	v_mfma_f32_16x16x32_bf16 v[22:25], v[114:117], v[46:49], v[22:25]
	s_waitcnt lgkmcnt(1)
	v_mfma_f32_16x16x32_bf16 v[26:29], v[146:149], v[30:33], v[26:29]
	v_mfma_f32_16x16x32_bf16 v[18:21], v[146:149], v[42:45], v[18:21]
	v_mfma_f32_16x16x32_bf16 v[22:25], v[146:149], v[58:61], v[22:25]
	v_mfma_f32_16x16x32_bf16 v[26:29], v[146:149], v[14:17], v[26:29]
	v_mfma_f32_16x16x32_bf16 v[18:21], v[146:149], v[34:37], v[18:21]
	v_mfma_f32_16x16x32_bf16 v[22:25], v[146:149], v[46:49], v[22:25]
	ds_read_b128 v[114:117], v200 offset:49664
	ds_read_b128 v[146:149], v200 offset:49728
	ds_read_b128 v[154:157], v199 offset:33024
	ds_read_b128 v[158:161], v199 offset:33088
	s_waitcnt lgkmcnt(0)
	v_mfma_f32_16x16x32_bf16 v[10:13], v[114:117], v[30:33], v[10:13]
	s_barrier
	v_mfma_f32_16x16x32_bf16 v[10:13], v[114:117], v[14:17], v[10:13]
	v_mfma_f32_16x16x32_bf16 v[10:13], v[154:157], v[30:33], v[10:13]
	v_mfma_f32_16x16x32_bf16 v[10:13], v[154:157], v[14:17], v[10:13]
	s_waitcnt vmcnt(4)
	v_mfma_f32_16x16x32_bf16 v[14:17], v[118:121], v[50:53], v[26:29]
	v_mfma_f32_16x16x32_bf16 v[14:17], v[118:121], v[38:41], v[14:17]
	v_mfma_f32_16x16x32_bf16 v[14:17], v[150:153], v[50:53], v[14:17]
	v_mfma_f32_16x16x32_bf16 v[26:29], v[150:153], v[38:41], v[14:17]
	s_waitcnt vmcnt(2)
	v_mfma_f32_16x16x32_bf16 v[14:17], v[118:121], v[62:65], v[18:21]
	v_mfma_f32_16x16x32_bf16 v[14:17], v[118:121], v[54:57], v[14:17]
	v_mfma_f32_16x16x32_bf16 v[14:17], v[150:153], v[62:65], v[14:17]
	v_mfma_f32_16x16x32_bf16 v[18:21], v[150:153], v[54:57], v[14:17]
	s_waitcnt vmcnt(0)
	v_mfma_f32_16x16x32_bf16 v[14:17], v[118:121], v[70:73], v[22:25]
	v_mfma_f32_16x16x32_bf16 v[2:5], v[114:117], v[42:45], v[2:5]
	v_mfma_f32_16x16x32_bf16 v[14:17], v[118:121], v[66:69], v[14:17]
	v_mfma_f32_16x16x32_bf16 v[10:13], v[146:149], v[50:53], v[10:13]
	v_mfma_f32_16x16x32_bf16 v[2:5], v[114:117], v[34:37], v[2:5]
	v_mfma_f32_16x16x32_bf16 v[14:17], v[150:153], v[70:73], v[14:17]
	v_mfma_f32_16x16x32_bf16 v[6:9], v[114:117], v[58:61], v[6:9]
	v_mfma_f32_16x16x32_bf16 v[10:13], v[146:149], v[38:41], v[10:13]
	v_mfma_f32_16x16x32_bf16 v[2:5], v[154:157], v[42:45], v[2:5]
	v_mfma_f32_16x16x32_bf16 v[22:25], v[150:153], v[66:69], v[14:17]
	s_nop 3
	v_lshl_add_u64 v[14:15], s[6:7], 0, v[168:169]
	s_add_u32 s6, s4, 0x30800
	s_addc_u32 s7, s5, 0
	v_mfma_f32_16x16x32_bf16 v[6:9], v[114:117], v[46:49], v[6:9]
	v_lshl_add_u64 v[30:31], s[6:7], 0, v[168:169]
	s_add_u32 s6, s4, 0x10800
	s_addc_u32 s7, s5, 0
	v_mfma_f32_16x16x32_bf16 v[10:13], v[158:161], v[50:53], v[10:13]
	global_load_dwordx4 v[30:33], v[30:31], off
	v_and_b32_sdwa v116, v142, v202 dst_sel:DWORD dst_unused:UNUSED_PAD src0_sel:WORD_1 src1_sel:DWORD
	global_load_dwordx4 v[14:17], v[14:15], off
	v_mfma_f32_16x16x32_bf16 v[2:5], v[154:157], v[34:37], v[2:5]
	v_lshl_add_u64 v[34:35], s[6:7], 0, v[168:169]
	s_add_u32 s6, s4, 0x40800
	s_addc_u32 s7, s5, 0
	v_mfma_f32_16x16x32_bf16 v[6:9], v[154:157], v[58:61], v[6:9]
	global_load_dwordx4 v[34:37], v[34:35], off
	v_and_b32_sdwa v117, v144, v202 dst_sel:DWORD dst_unused:UNUSED_PAD src0_sel:WORD_1 src1_sel:DWORD
	v_add3_u32 v120, v142, v116, s64
	v_mfma_f32_16x16x32_bf16 v[10:13], v[158:161], v[38:41], v[10:13]
	v_lshl_add_u64 v[38:39], s[6:7], 0, v[168:169]
	s_add_u32 s6, s4, 0x20800
	s_addc_u32 s7, s5, 0
	global_load_dwordx4 v[42:45], v[38:39], off
	v_lshl_add_u64 v[38:39], s[6:7], 0, v[168:169]
	s_add_u32 s6, s4, 0x50800
	s_addc_u32 s7, s5, 0
	v_mfma_f32_16x16x32_bf16 v[6:9], v[154:157], v[46:49], v[6:9]
	global_load_dwordx4 v[46:49], v[38:39], off
	v_lshl_add_u64 v[38:39], s[6:7], 0, v[168:169]
	global_load_dwordx4 v[58:61], v[38:39], off
	v_mfma_f32_16x16x32_bf16 v[2:5], v[146:149], v[62:65], v[2:5]
	v_add3_u32 v121, v144, v117, s64
	v_and_b32_sdwa v116, v143, v202 dst_sel:DWORD dst_unused:UNUSED_PAD src0_sel:WORD_1 src1_sel:DWORD
	v_and_b32_sdwa v117, v145, v202 dst_sel:DWORD dst_unused:UNUSED_PAD src0_sel:WORD_1 src1_sel:DWORD
	v_mfma_f32_16x16x32_bf16 v[2:5], v[146:149], v[54:57], v[2:5]
	v_add3_u32 v116, v143, v116, s64
	v_add3_u32 v118, v145, v117, s64
	s_add_u32 s6, s4, 0x840
	v_mfma_f32_16x16x32_bf16 v[6:9], v[146:149], v[70:73], v[6:9]
	v_mov_b32_e32 v114, v144
	v_mov_b32_e32 v115, v142
	v_and_b32_e32 v117, 0xffff0000, v116
	v_and_b32_e32 v116, 0xffff0000, v118
	v_and_b32_e32 v119, 0xffff0000, v120
	v_and_b32_e32 v118, 0xffff0000, v121
	s_addc_u32 s7, s5, 0
	v_mov_b32_e32 v142, v145
	v_pk_add_f32 v[114:115], v[114:115], v[118:119] neg_lo:[0,1] neg_hi:[0,1]
	v_mfma_f32_16x16x32_bf16 v[2:5], v[158:161], v[62:65], v[2:5]
	v_lshl_add_u64 v[38:39], s[6:7], 0, v[168:169]
	s_add_u32 s6, s4, 0x30840
	v_pk_add_f32 v[118:119], v[142:143], v[116:117] neg_lo:[0,1] neg_hi:[0,1]
	v_mfma_f32_16x16x32_bf16 v[6:9], v[146:149], v[66:69], v[6:9]
	v_or_b32_sdwa v116, v121, v116 dst_sel:DWORD dst_unused:UNUSED_PAD src0_sel:WORD_1 src1_sel:DWORD
	v_or_b32_sdwa v117, v120, v117 dst_sel:DWORD dst_unused:UNUSED_PAD src0_sel:WORD_1 src1_sel:DWORD
	v_and_b32_sdwa v120, v115, v202 dst_sel:DWORD dst_unused:UNUSED_PAD src0_sel:WORD_1 src1_sel:DWORD
	v_and_b32_sdwa v121, v114, v202 dst_sel:DWORD dst_unused:UNUSED_PAD src0_sel:WORD_1 src1_sel:DWORD
	s_addc_u32 s7, s5, 0
	v_add3_u32 v114, v114, v121, s64
	v_add3_u32 v115, v115, v120, s64
	v_and_b32_sdwa v120, v119, v202 dst_sel:DWORD dst_unused:UNUSED_PAD src0_sel:WORD_1 src1_sel:DWORD
	v_and_b32_sdwa v121, v118, v202 dst_sel:DWORD dst_unused:UNUSED_PAD src0_sel:WORD_1 src1_sel:DWORD
	v_lshl_add_u64 v[50:51], s[6:7], 0, v[168:169]
	s_add_u32 s6, s4, 0x10840
	v_add3_u32 v119, v119, v120, s64
	v_add3_u32 v118, v118, v121, s64
	v_and_b32_sdwa v120, v138, v202 dst_sel:DWORD dst_unused:UNUSED_PAD src0_sel:WORD_1 src1_sel:DWORD
	v_and_b32_sdwa v121, v140, v202 dst_sel:DWORD dst_unused:UNUSED_PAD src0_sel:WORD_1 src1_sel:DWORD
	s_addc_u32 s7, s5, 0
	v_and_b32_e32 v118, 0xffff0000, v118
	v_add3_u32 v142, v138, v120, s64
	v_add3_u32 v143, v140, v121, s64
	v_and_b32_sdwa v120, v139, v202 dst_sel:DWORD dst_unused:UNUSED_PAD src0_sel:WORD_1 src1_sel:DWORD
	v_and_b32_sdwa v121, v141, v202 dst_sel:DWORD dst_unused:UNUSED_PAD src0_sel:WORD_1 src1_sel:DWORD
	v_mfma_f32_16x16x32_bf16 v[2:5], v[158:161], v[54:57], v[2:5]
	v_lshl_add_u64 v[54:55], s[6:7], 0, v[168:169]
	s_add_u32 s6, s4, 0x40840
	v_and_b32_e32 v119, 0xffff0000, v119
	v_mfma_f32_16x16x32_bf16 v[6:9], v[158:161], v[70:73], v[6:9]
	v_or_b32_sdwa v114, v118, v114 dst_sel:DWORD dst_unused:UNUSED_PAD src0_sel:DWORD src1_sel:WORD_1
	v_mov_b32_e32 v118, v140
	v_add3_u32 v120, v139, v120, s64
	v_add3_u32 v140, v141, v121, s64
	s_addc_u32 s7, s5, 0
	v_or_b32_sdwa v115, v119, v115 dst_sel:DWORD dst_unused:UNUSED_PAD src0_sel:DWORD src1_sel:WORD_1
	v_mov_b32_e32 v119, v138
	v_mov_b32_e32 v138, v141
	v_and_b32_e32 v121, 0xffff0000, v120
	v_and_b32_e32 v120, 0xffff0000, v140
	v_and_b32_e32 v141, 0xffff0000, v142
	v_and_b32_e32 v140, 0xffff0000, v143
	v_lshl_add_u64 v[62:63], s[6:7], 0, v[168:169]
	s_add_u32 s6, s4, 0x20840
	v_pk_add_f32 v[118:119], v[118:119], v[140:141] neg_lo:[0,1] neg_hi:[0,1]
	s_addc_u32 s7, s5, 0
	v_pk_add_f32 v[138:139], v[138:139], v[120:121] neg_lo:[0,1] neg_hi:[0,1]
	v_and_b32_sdwa v140, v119, v202 dst_sel:DWORD dst_unused:UNUSED_PAD src0_sel:WORD_1 src1_sel:DWORD
	v_and_b32_sdwa v141, v118, v202 dst_sel:DWORD dst_unused:UNUSED_PAD src0_sel:WORD_1 src1_sel:DWORD
	v_mfma_f32_16x16x32_bf16 v[6:9], v[158:161], v[66:69], v[6:9]
	v_lshl_add_u64 v[66:67], s[6:7], 0, v[168:169]
	s_add_u32 s6, s4, 0x50840
	v_add3_u32 v118, v118, v141, s64
	v_add3_u32 v119, v119, v140, s64
	v_and_b32_sdwa v140, v139, v202 dst_sel:DWORD dst_unused:UNUSED_PAD src0_sel:WORD_1 src1_sel:DWORD
	v_and_b32_sdwa v141, v138, v202 dst_sel:DWORD dst_unused:UNUSED_PAD src0_sel:WORD_1 src1_sel:DWORD
	s_addc_u32 s7, s5, 0
	v_add3_u32 v139, v139, v140, s64
	v_add3_u32 v138, v138, v141, s64
	v_lshl_add_u64 v[70:71], s[6:7], 0, v[168:169]
	v_or_b32_sdwa v120, v143, v120 dst_sel:DWORD dst_unused:UNUSED_PAD src0_sel:WORD_1 src1_sel:DWORD
	v_or_b32_sdwa v121, v142, v121 dst_sel:DWORD dst_unused:UNUSED_PAD src0_sel:WORD_1 src1_sel:DWORD
	v_and_b32_e32 v139, 0xffff0000, v139
	v_and_b32_e32 v138, 0xffff0000, v138
	global_load_dwordx4 v[38:41], v[38:39], off
	v_or_b32_sdwa v119, v139, v119 dst_sel:DWORD dst_unused:UNUSED_PAD src0_sel:DWORD src1_sel:WORD_1
	global_load_dwordx4 v[50:53], v[50:51], off
	v_or_b32_sdwa v118, v138, v118 dst_sel:DWORD dst_unused:UNUSED_PAD src0_sel:DWORD src1_sel:WORD_1
	global_load_dwordx4 v[54:57], v[54:55], off
	s_add_u32 s6, s4, 0xc00
	global_load_dwordx4 v[62:65], v[62:63], off
	s_addc_u32 s7, s5, 0
	global_load_dwordx4 v[66:69], v[66:67], off
	s_nop 0
	global_load_dwordx4 v[70:73], v[70:71], off
	ds_write2st64_b64 v198, v[116:117], v[120:121] offset0:32 offset1:33
	ds_write2st64_b64 v198, v[114:115], v[118:119] offset0:97 offset1:98
	v_and_b32_sdwa v116, v110, v202 dst_sel:DWORD dst_unused:UNUSED_PAD src0_sel:WORD_1 src1_sel:DWORD
	v_and_b32_sdwa v117, v112, v202 dst_sel:DWORD dst_unused:UNUSED_PAD src0_sel:WORD_1 src1_sel:DWORD
	v_mov_b32_e32 v114, v112
	v_add3_u32 v118, v110, v116, s64
	v_add3_u32 v119, v112, v117, s64
	v_and_b32_sdwa v112, v111, v202 dst_sel:DWORD dst_unused:UNUSED_PAD src0_sel:WORD_1 src1_sel:DWORD
	v_and_b32_sdwa v116, v113, v202 dst_sel:DWORD dst_unused:UNUSED_PAD src0_sel:WORD_1 src1_sel:DWORD
	v_add3_u32 v112, v111, v112, s64
	v_add3_u32 v116, v113, v116, s64
	v_mov_b32_e32 v115, v110
	v_mov_b32_e32 v110, v113
	v_and_b32_e32 v113, 0xffff0000, v112
	v_and_b32_e32 v112, 0xffff0000, v116
	v_and_b32_e32 v117, 0xffff0000, v118
	v_and_b32_e32 v116, 0xffff0000, v119
	v_pk_add_f32 v[114:115], v[114:115], v[116:117] neg_lo:[0,1] neg_hi:[0,1]
	v_pk_add_f32 v[110:111], v[110:111], v[112:113] neg_lo:[0,1] neg_hi:[0,1]
	v_and_b32_sdwa v117, v114, v202 dst_sel:DWORD dst_unused:UNUSED_PAD src0_sel:WORD_1 src1_sel:DWORD
	v_and_b32_sdwa v116, v115, v202 dst_sel:DWORD dst_unused:UNUSED_PAD src0_sel:WORD_1 src1_sel:DWORD
	v_add3_u32 v114, v114, v117, s64
	v_and_b32_sdwa v117, v110, v202 dst_sel:DWORD dst_unused:UNUSED_PAD src0_sel:WORD_1 src1_sel:DWORD
	v_add3_u32 v115, v115, v116, s64
	v_and_b32_sdwa v116, v111, v202 dst_sel:DWORD dst_unused:UNUSED_PAD src0_sel:WORD_1 src1_sel:DWORD
	v_add3_u32 v110, v110, v117, s64
	v_add3_u32 v111, v111, v116, s64
	v_and_b32_e32 v110, 0xffff0000, v110
	v_and_b32_sdwa v116, v106, v202 dst_sel:DWORD dst_unused:UNUSED_PAD src0_sel:WORD_1 src1_sel:DWORD
	v_and_b32_sdwa v117, v108, v202 dst_sel:DWORD dst_unused:UNUSED_PAD src0_sel:WORD_1 src1_sel:DWORD
	v_or_b32_sdwa v112, v119, v112 dst_sel:DWORD dst_unused:UNUSED_PAD src0_sel:WORD_1 src1_sel:DWORD
	v_or_b32_sdwa v113, v118, v113 dst_sel:DWORD dst_unused:UNUSED_PAD src0_sel:WORD_1 src1_sel:DWORD
	v_or_b32_sdwa v110, v110, v114 dst_sel:DWORD dst_unused:UNUSED_PAD src0_sel:DWORD src1_sel:WORD_1
	v_mov_b32_e32 v114, v108
	v_add3_u32 v118, v106, v116, s64
	v_add3_u32 v119, v108, v117, s64
	v_and_b32_sdwa v108, v107, v202 dst_sel:DWORD dst_unused:UNUSED_PAD src0_sel:WORD_1 src1_sel:DWORD
	v_and_b32_sdwa v116, v109, v202 dst_sel:DWORD dst_unused:UNUSED_PAD src0_sel:WORD_1 src1_sel:DWORD
	v_and_b32_e32 v111, 0xffff0000, v111
	v_add3_u32 v108, v107, v108, s64
	v_add3_u32 v116, v109, v116, s64
	v_or_b32_sdwa v111, v111, v115 dst_sel:DWORD dst_unused:UNUSED_PAD src0_sel:DWORD src1_sel:WORD_1
	v_mov_b32_e32 v115, v106
	v_mov_b32_e32 v106, v109
	v_and_b32_e32 v109, 0xffff0000, v108
	v_and_b32_e32 v108, 0xffff0000, v116
	v_and_b32_e32 v117, 0xffff0000, v118
	v_and_b32_e32 v116, 0xffff0000, v119
	v_pk_add_f32 v[114:115], v[114:115], v[116:117] neg_lo:[0,1] neg_hi:[0,1]
	v_pk_add_f32 v[106:107], v[106:107], v[108:109] neg_lo:[0,1] neg_hi:[0,1]
	v_and_b32_sdwa v116, v115, v202 dst_sel:DWORD dst_unused:UNUSED_PAD src0_sel:WORD_1 src1_sel:DWORD
	v_and_b32_sdwa v117, v114, v202 dst_sel:DWORD dst_unused:UNUSED_PAD src0_sel:WORD_1 src1_sel:DWORD
	v_add3_u32 v114, v114, v117, s64
	v_add3_u32 v115, v115, v116, s64
	v_and_b32_sdwa v116, v107, v202 dst_sel:DWORD dst_unused:UNUSED_PAD src0_sel:WORD_1 src1_sel:DWORD
	v_and_b32_sdwa v117, v106, v202 dst_sel:DWORD dst_unused:UNUSED_PAD src0_sel:WORD_1 src1_sel:DWORD
	v_add3_u32 v107, v107, v116, s64
	v_add3_u32 v106, v106, v117, s64
	v_or_b32_sdwa v108, v119, v108 dst_sel:DWORD dst_unused:UNUSED_PAD src0_sel:WORD_1 src1_sel:DWORD
	v_or_b32_sdwa v109, v118, v109 dst_sel:DWORD dst_unused:UNUSED_PAD src0_sel:WORD_1 src1_sel:DWORD
	v_and_b32_e32 v107, 0xffff0000, v107
	v_and_b32_e32 v106, 0xffff0000, v106
	v_or_b32_sdwa v107, v107, v115 dst_sel:DWORD dst_unused:UNUSED_PAD src0_sel:DWORD src1_sel:WORD_1
	v_or_b32_sdwa v106, v106, v114 dst_sel:DWORD dst_unused:UNUSED_PAD src0_sel:DWORD src1_sel:WORD_1
	ds_write2st64_b64 v203, v[112:113], v[108:109] offset0:34 offset1:35
	ds_write2st64_b64 v203, v[110:111], v[106:107] offset0:99 offset1:100
	v_and_b32_sdwa v108, v94, v202 dst_sel:DWORD dst_unused:UNUSED_PAD src0_sel:WORD_1 src1_sel:DWORD
	v_and_b32_sdwa v109, v96, v202 dst_sel:DWORD dst_unused:UNUSED_PAD src0_sel:WORD_1 src1_sel:DWORD
	v_mov_b32_e32 v106, v96
	v_add3_u32 v110, v94, v108, s64
	v_add3_u32 v111, v96, v109, s64
	v_and_b32_sdwa v96, v95, v202 dst_sel:DWORD dst_unused:UNUSED_PAD src0_sel:WORD_1 src1_sel:DWORD
	v_and_b32_sdwa v108, v97, v202 dst_sel:DWORD dst_unused:UNUSED_PAD src0_sel:WORD_1 src1_sel:DWORD
	v_add3_u32 v96, v95, v96, s64
	v_add3_u32 v108, v97, v108, s64
	v_mov_b32_e32 v107, v94
	v_mov_b32_e32 v94, v97
	v_and_b32_e32 v97, 0xffff0000, v96
	v_and_b32_e32 v96, 0xffff0000, v108
	v_and_b32_e32 v109, 0xffff0000, v110
	v_and_b32_e32 v108, 0xffff0000, v111
	v_pk_add_f32 v[106:107], v[106:107], v[108:109] neg_lo:[0,1] neg_hi:[0,1]
	v_pk_add_f32 v[94:95], v[94:95], v[96:97] neg_lo:[0,1] neg_hi:[0,1]
	v_and_b32_sdwa v109, v106, v202 dst_sel:DWORD dst_unused:UNUSED_PAD src0_sel:WORD_1 src1_sel:DWORD
	v_and_b32_sdwa v108, v107, v202 dst_sel:DWORD dst_unused:UNUSED_PAD src0_sel:WORD_1 src1_sel:DWORD
	v_add3_u32 v106, v106, v109, s64
	v_and_b32_sdwa v109, v94, v202 dst_sel:DWORD dst_unused:UNUSED_PAD src0_sel:WORD_1 src1_sel:DWORD
	v_add3_u32 v107, v107, v108, s64
	v_and_b32_sdwa v108, v95, v202 dst_sel:DWORD dst_unused:UNUSED_PAD src0_sel:WORD_1 src1_sel:DWORD
	v_add3_u32 v94, v94, v109, s64
	v_add3_u32 v95, v95, v108, s64
	v_and_b32_e32 v94, 0xffff0000, v94
	v_and_b32_sdwa v108, v90, v202 dst_sel:DWORD dst_unused:UNUSED_PAD src0_sel:WORD_1 src1_sel:DWORD
	v_and_b32_sdwa v109, v92, v202 dst_sel:DWORD dst_unused:UNUSED_PAD src0_sel:WORD_1 src1_sel:DWORD
	v_or_b32_sdwa v96, v111, v96 dst_sel:DWORD dst_unused:UNUSED_PAD src0_sel:WORD_1 src1_sel:DWORD
	v_or_b32_sdwa v97, v110, v97 dst_sel:DWORD dst_unused:UNUSED_PAD src0_sel:WORD_1 src1_sel:DWORD
	v_or_b32_sdwa v94, v94, v106 dst_sel:DWORD dst_unused:UNUSED_PAD src0_sel:DWORD src1_sel:WORD_1
	v_mov_b32_e32 v106, v92
	v_add3_u32 v110, v90, v108, s64
	v_add3_u32 v111, v92, v109, s64
	v_and_b32_sdwa v92, v91, v202 dst_sel:DWORD dst_unused:UNUSED_PAD src0_sel:WORD_1 src1_sel:DWORD
	v_and_b32_sdwa v108, v93, v202 dst_sel:DWORD dst_unused:UNUSED_PAD src0_sel:WORD_1 src1_sel:DWORD
	v_and_b32_e32 v95, 0xffff0000, v95
	v_add3_u32 v92, v91, v92, s64
	v_add3_u32 v108, v93, v108, s64
	v_or_b32_sdwa v95, v95, v107 dst_sel:DWORD dst_unused:UNUSED_PAD src0_sel:DWORD src1_sel:WORD_1
	v_mov_b32_e32 v107, v90
	v_mov_b32_e32 v90, v93
	v_and_b32_e32 v93, 0xffff0000, v92
	v_and_b32_e32 v92, 0xffff0000, v108
	v_and_b32_e32 v109, 0xffff0000, v110
	v_and_b32_e32 v108, 0xffff0000, v111
	v_pk_add_f32 v[106:107], v[106:107], v[108:109] neg_lo:[0,1] neg_hi:[0,1]
	v_pk_add_f32 v[90:91], v[90:91], v[92:93] neg_lo:[0,1] neg_hi:[0,1]
	v_and_b32_sdwa v108, v107, v202 dst_sel:DWORD dst_unused:UNUSED_PAD src0_sel:WORD_1 src1_sel:DWORD
	v_and_b32_sdwa v109, v106, v202 dst_sel:DWORD dst_unused:UNUSED_PAD src0_sel:WORD_1 src1_sel:DWORD
	v_add3_u32 v106, v106, v109, s64
	v_add3_u32 v107, v107, v108, s64
	v_and_b32_sdwa v108, v91, v202 dst_sel:DWORD dst_unused:UNUSED_PAD src0_sel:WORD_1 src1_sel:DWORD
	v_and_b32_sdwa v109, v90, v202 dst_sel:DWORD dst_unused:UNUSED_PAD src0_sel:WORD_1 src1_sel:DWORD
	v_add3_u32 v91, v91, v108, s64
	v_add3_u32 v90, v90, v109, s64
	v_or_b32_sdwa v92, v111, v92 dst_sel:DWORD dst_unused:UNUSED_PAD src0_sel:WORD_1 src1_sel:DWORD
	v_or_b32_sdwa v93, v110, v93 dst_sel:DWORD dst_unused:UNUSED_PAD src0_sel:WORD_1 src1_sel:DWORD
	v_and_b32_e32 v91, 0xffff0000, v91
	v_and_b32_e32 v90, 0xffff0000, v90
	v_or_b32_sdwa v91, v91, v107 dst_sel:DWORD dst_unused:UNUSED_PAD src0_sel:DWORD src1_sel:WORD_1
	v_or_b32_sdwa v90, v90, v106 dst_sel:DWORD dst_unused:UNUSED_PAD src0_sel:DWORD src1_sel:WORD_1
	ds_write2st64_b64 v204, v[96:97], v[92:93] offset0:36 offset1:37
	ds_write2st64_b64 v204, v[94:95], v[90:91] offset0:101 offset1:102
	v_and_b32_sdwa v92, v126, v202 dst_sel:DWORD dst_unused:UNUSED_PAD src0_sel:WORD_1 src1_sel:DWORD
	v_and_b32_sdwa v93, v128, v202 dst_sel:DWORD dst_unused:UNUSED_PAD src0_sel:WORD_1 src1_sel:DWORD
	v_add3_u32 v96, v126, v92, s64
	v_add3_u32 v97, v128, v93, s64
	v_and_b32_sdwa v92, v127, v202 dst_sel:DWORD dst_unused:UNUSED_PAD src0_sel:WORD_1 src1_sel:DWORD
	v_and_b32_sdwa v93, v129, v202 dst_sel:DWORD dst_unused:UNUSED_PAD src0_sel:WORD_1 src1_sel:DWORD
	v_add3_u32 v92, v127, v92, s64
	v_add3_u32 v94, v129, v93, s64
	v_mov_b32_e32 v90, v128
	v_mov_b32_e32 v91, v126
	v_and_b32_e32 v93, 0xffff0000, v92
	v_and_b32_e32 v92, 0xffff0000, v94
	v_and_b32_e32 v95, 0xffff0000, v96
	v_and_b32_e32 v94, 0xffff0000, v97
	v_mov_b32_e32 v126, v129
	v_pk_add_f32 v[90:91], v[90:91], v[94:95] neg_lo:[0,1] neg_hi:[0,1]
	v_pk_add_f32 v[94:95], v[126:127], v[92:93] neg_lo:[0,1] neg_hi:[0,1]
	v_or_b32_sdwa v92, v97, v92 dst_sel:DWORD dst_unused:UNUSED_PAD src0_sel:WORD_1 src1_sel:DWORD
	v_or_b32_sdwa v93, v96, v93 dst_sel:DWORD dst_unused:UNUSED_PAD src0_sel:WORD_1 src1_sel:DWORD
	v_and_b32_sdwa v96, v91, v202 dst_sel:DWORD dst_unused:UNUSED_PAD src0_sel:WORD_1 src1_sel:DWORD
	v_and_b32_sdwa v97, v90, v202 dst_sel:DWORD dst_unused:UNUSED_PAD src0_sel:WORD_1 src1_sel:DWORD
	v_add3_u32 v90, v90, v97, s64
	v_add3_u32 v91, v91, v96, s64
	v_and_b32_sdwa v96, v95, v202 dst_sel:DWORD dst_unused:UNUSED_PAD src0_sel:WORD_1 src1_sel:DWORD
	v_and_b32_sdwa v97, v94, v202 dst_sel:DWORD dst_unused:UNUSED_PAD src0_sel:WORD_1 src1_sel:DWORD
	v_add3_u32 v95, v95, v96, s64
	v_add3_u32 v94, v94, v97, s64
	v_and_b32_sdwa v96, v122, v202 dst_sel:DWORD dst_unused:UNUSED_PAD src0_sel:WORD_1 src1_sel:DWORD
	v_and_b32_sdwa v97, v124, v202 dst_sel:DWORD dst_unused:UNUSED_PAD src0_sel:WORD_1 src1_sel:DWORD
	v_add3_u32 v108, v122, v96, s64
	v_add3_u32 v109, v124, v97, s64
	v_and_b32_sdwa v96, v123, v202 dst_sel:DWORD dst_unused:UNUSED_PAD src0_sel:WORD_1 src1_sel:DWORD
	v_and_b32_sdwa v97, v125, v202 dst_sel:DWORD dst_unused:UNUSED_PAD src0_sel:WORD_1 src1_sel:DWORD
	v_and_b32_e32 v95, 0xffff0000, v95
	v_and_b32_e32 v94, 0xffff0000, v94
	v_add3_u32 v96, v123, v96, s64
	v_add3_u32 v106, v125, v97, s64
	v_or_b32_sdwa v91, v95, v91 dst_sel:DWORD dst_unused:UNUSED_PAD src0_sel:DWORD src1_sel:WORD_1
	v_or_b32_sdwa v90, v94, v90 dst_sel:DWORD dst_unused:UNUSED_PAD src0_sel:DWORD src1_sel:WORD_1
	v_mov_b32_e32 v94, v124
	v_mov_b32_e32 v95, v122
	v_and_b32_e32 v97, 0xffff0000, v96
	v_and_b32_e32 v96, 0xffff0000, v106
	v_and_b32_e32 v107, 0xffff0000, v108
	v_and_b32_e32 v106, 0xffff0000, v109
	v_mov_b32_e32 v122, v125
	v_pk_add_f32 v[94:95], v[94:95], v[106:107] neg_lo:[0,1] neg_hi:[0,1]
	v_pk_add_f32 v[106:107], v[122:123], v[96:97] neg_lo:[0,1] neg_hi:[0,1]
	v_or_b32_sdwa v96, v109, v96 dst_sel:DWORD dst_unused:UNUSED_PAD src0_sel:WORD_1 src1_sel:DWORD
	v_or_b32_sdwa v97, v108, v97 dst_sel:DWORD dst_unused:UNUSED_PAD src0_sel:WORD_1 src1_sel:DWORD
	v_and_b32_sdwa v108, v95, v202 dst_sel:DWORD dst_unused:UNUSED_PAD src0_sel:WORD_1 src1_sel:DWORD
	v_and_b32_sdwa v109, v94, v202 dst_sel:DWORD dst_unused:UNUSED_PAD src0_sel:WORD_1 src1_sel:DWORD
	v_add3_u32 v94, v94, v109, s64
	v_add3_u32 v95, v95, v108, s64
	v_and_b32_sdwa v108, v107, v202 dst_sel:DWORD dst_unused:UNUSED_PAD src0_sel:WORD_1 src1_sel:DWORD
	v_and_b32_sdwa v109, v106, v202 dst_sel:DWORD dst_unused:UNUSED_PAD src0_sel:WORD_1 src1_sel:DWORD
	v_add3_u32 v107, v107, v108, s64
	v_add3_u32 v106, v106, v109, s64
	v_and_b32_e32 v107, 0xffff0000, v107
	v_and_b32_e32 v106, 0xffff0000, v106
	v_or_b32_sdwa v95, v107, v95 dst_sel:DWORD dst_unused:UNUSED_PAD src0_sel:DWORD src1_sel:WORD_1
	v_or_b32_sdwa v94, v106, v94 dst_sel:DWORD dst_unused:UNUSED_PAD src0_sel:DWORD src1_sel:WORD_1
	ds_write2st64_b64 v205, v[92:93], v[96:97] offset0:38 offset1:39
	ds_write2st64_b64 v205, v[90:91], v[94:95] offset0:103 offset1:104
	s_waitcnt lgkmcnt(0)
	s_barrier
	ds_read_b128 v[90:93], v199 offset:49664
	ds_read_b128 v[94:97], v199 offset:49728
	s_waitcnt vmcnt(11) lgkmcnt(1)
	v_mfma_f32_16x16x32_bf16 v[26:29], v[90:93], v[30:33], v[26:29]
	ds_read_b128 v[106:109], v199 offset:16384
	ds_read_b128 v[110:113], v199 offset:16448
	s_waitcnt vmcnt(8)
	v_mfma_f32_16x16x32_bf16 v[18:21], v[90:93], v[42:45], v[18:21]
	s_waitcnt vmcnt(6)
	v_mfma_f32_16x16x32_bf16 v[22:25], v[90:93], v[58:61], v[22:25]
	v_mfma_f32_16x16x32_bf16 v[26:29], v[90:93], v[14:17], v[26:29]
	v_mfma_f32_16x16x32_bf16 v[18:21], v[90:93], v[34:37], v[18:21]
	v_mfma_f32_16x16x32_bf16 v[22:25], v[90:93], v[46:49], v[22:25]
	s_waitcnt lgkmcnt(1)
	v_mfma_f32_16x16x32_bf16 v[26:29], v[106:109], v[30:33], v[26:29]
	v_mfma_f32_16x16x32_bf16 v[18:21], v[106:109], v[42:45], v[18:21]
	v_mfma_f32_16x16x32_bf16 v[22:25], v[106:109], v[58:61], v[22:25]
	v_mfma_f32_16x16x32_bf16 v[26:29], v[106:109], v[14:17], v[26:29]
	v_mfma_f32_16x16x32_bf16 v[18:21], v[106:109], v[34:37], v[18:21]
	v_mfma_f32_16x16x32_bf16 v[22:25], v[106:109], v[46:49], v[22:25]
	ds_read_b128 v[90:93], v200 offset:49664
	ds_read_b128 v[106:109], v200 offset:49728
	ds_read_b128 v[114:117], v199 offset:33024
	ds_read_b128 v[118:121], v199 offset:33088
	s_waitcnt lgkmcnt(0)
	v_mfma_f32_16x16x32_bf16 v[10:13], v[90:93], v[30:33], v[10:13]
	s_barrier
	v_mfma_f32_16x16x32_bf16 v[10:13], v[90:93], v[14:17], v[10:13]
	v_mfma_f32_16x16x32_bf16 v[10:13], v[114:117], v[30:33], v[10:13]
	v_mfma_f32_16x16x32_bf16 v[10:13], v[114:117], v[14:17], v[10:13]
	s_waitcnt vmcnt(4)
	v_mfma_f32_16x16x32_bf16 v[14:17], v[94:97], v[50:53], v[26:29]
	v_mfma_f32_16x16x32_bf16 v[14:17], v[94:97], v[38:41], v[14:17]
	v_mfma_f32_16x16x32_bf16 v[14:17], v[110:113], v[50:53], v[14:17]
	v_mfma_f32_16x16x32_bf16 v[26:29], v[110:113], v[38:41], v[14:17]
	s_waitcnt vmcnt(2)
	v_mfma_f32_16x16x32_bf16 v[14:17], v[94:97], v[62:65], v[18:21]
	v_mfma_f32_16x16x32_bf16 v[14:17], v[94:97], v[54:57], v[14:17]
	v_mfma_f32_16x16x32_bf16 v[14:17], v[110:113], v[62:65], v[14:17]
	v_mfma_f32_16x16x32_bf16 v[18:21], v[110:113], v[54:57], v[14:17]
	s_waitcnt vmcnt(0)
	v_mfma_f32_16x16x32_bf16 v[14:17], v[94:97], v[70:73], v[22:25]
	v_mfma_f32_16x16x32_bf16 v[2:5], v[90:93], v[42:45], v[2:5]
	v_mfma_f32_16x16x32_bf16 v[14:17], v[94:97], v[66:69], v[14:17]
	v_mfma_f32_16x16x32_bf16 v[10:13], v[106:109], v[50:53], v[10:13]
	v_mfma_f32_16x16x32_bf16 v[2:5], v[90:93], v[34:37], v[2:5]
	v_mfma_f32_16x16x32_bf16 v[14:17], v[110:113], v[70:73], v[14:17]
	v_mfma_f32_16x16x32_bf16 v[6:9], v[90:93], v[58:61], v[6:9]
	v_mfma_f32_16x16x32_bf16 v[10:13], v[106:109], v[38:41], v[10:13]
	v_mfma_f32_16x16x32_bf16 v[2:5], v[114:117], v[42:45], v[2:5]
	v_mfma_f32_16x16x32_bf16 v[22:25], v[110:113], v[66:69], v[14:17]
	s_nop 3
	v_lshl_add_u64 v[14:15], s[6:7], 0, v[168:169]
	s_add_u32 s6, s4, 0x30c00
	s_addc_u32 s7, s5, 0
	v_mfma_f32_16x16x32_bf16 v[6:9], v[90:93], v[46:49], v[6:9]
	v_lshl_add_u64 v[30:31], s[6:7], 0, v[168:169]
	s_add_u32 s6, s4, 0x10c00
	s_addc_u32 s7, s5, 0
	v_mfma_f32_16x16x32_bf16 v[10:13], v[118:121], v[50:53], v[10:13]
	global_load_dwordx4 v[30:33], v[30:31], off
	v_and_b32_sdwa v92, v134, v202 dst_sel:DWORD dst_unused:UNUSED_PAD src0_sel:WORD_1 src1_sel:DWORD
	global_load_dwordx4 v[14:17], v[14:15], off
	v_mfma_f32_16x16x32_bf16 v[2:5], v[114:117], v[34:37], v[2:5]
	v_lshl_add_u64 v[34:35], s[6:7], 0, v[168:169]
	s_add_u32 s6, s4, 0x40c00
	s_addc_u32 s7, s5, 0
	v_mfma_f32_16x16x32_bf16 v[6:9], v[114:117], v[58:61], v[6:9]
	global_load_dwordx4 v[34:37], v[34:35], off
	v_and_b32_sdwa v93, v136, v202 dst_sel:DWORD dst_unused:UNUSED_PAD src0_sel:WORD_1 src1_sel:DWORD
	v_add3_u32 v96, v134, v92, s64
	v_mfma_f32_16x16x32_bf16 v[10:13], v[118:121], v[38:41], v[10:13]
	v_lshl_add_u64 v[38:39], s[6:7], 0, v[168:169]
	s_add_u32 s6, s4, 0x20c00
	s_addc_u32 s7, s5, 0
	global_load_dwordx4 v[42:45], v[38:39], off
	v_lshl_add_u64 v[38:39], s[6:7], 0, v[168:169]
	s_add_u32 s6, s4, 0x50c00
	s_addc_u32 s7, s5, 0
	v_mfma_f32_16x16x32_bf16 v[6:9], v[114:117], v[46:49], v[6:9]
	global_load_dwordx4 v[46:49], v[38:39], off
	v_lshl_add_u64 v[38:39], s[6:7], 0, v[168:169]
	global_load_dwordx4 v[58:61], v[38:39], off
	v_mfma_f32_16x16x32_bf16 v[2:5], v[106:109], v[62:65], v[2:5]
	v_add3_u32 v97, v136, v93, s64
	v_and_b32_sdwa v92, v135, v202 dst_sel:DWORD dst_unused:UNUSED_PAD src0_sel:WORD_1 src1_sel:DWORD
	v_and_b32_sdwa v93, v137, v202 dst_sel:DWORD dst_unused:UNUSED_PAD src0_sel:WORD_1 src1_sel:DWORD
	v_mfma_f32_16x16x32_bf16 v[2:5], v[106:109], v[54:57], v[2:5]
	v_add3_u32 v92, v135, v92, s64
	v_add3_u32 v94, v137, v93, s64
	s_add_u32 s6, s4, 0xc40
	v_mfma_f32_16x16x32_bf16 v[6:9], v[106:109], v[70:73], v[6:9]
	v_mov_b32_e32 v90, v136
	v_mov_b32_e32 v91, v134
	v_and_b32_e32 v93, 0xffff0000, v92
	v_and_b32_e32 v92, 0xffff0000, v94
	v_and_b32_e32 v95, 0xffff0000, v96
	v_and_b32_e32 v94, 0xffff0000, v97
	s_addc_u32 s7, s5, 0
	v_mov_b32_e32 v134, v137
	v_pk_add_f32 v[90:91], v[90:91], v[94:95] neg_lo:[0,1] neg_hi:[0,1]
	v_mfma_f32_16x16x32_bf16 v[2:5], v[118:121], v[62:65], v[2:5]
	v_lshl_add_u64 v[38:39], s[6:7], 0, v[168:169]
	s_add_u32 s6, s4, 0x30c40
	v_pk_add_f32 v[94:95], v[134:135], v[92:93] neg_lo:[0,1] neg_hi:[0,1]
	v_or_b32_sdwa v92, v97, v92 dst_sel:DWORD dst_unused:UNUSED_PAD src0_sel:WORD_1 src1_sel:DWORD
	v_or_b32_sdwa v93, v96, v93 dst_sel:DWORD dst_unused:UNUSED_PAD src0_sel:WORD_1 src1_sel:DWORD
	v_and_b32_sdwa v96, v91, v202 dst_sel:DWORD dst_unused:UNUSED_PAD src0_sel:WORD_1 src1_sel:DWORD
	v_and_b32_sdwa v97, v90, v202 dst_sel:DWORD dst_unused:UNUSED_PAD src0_sel:WORD_1 src1_sel:DWORD
	s_addc_u32 s7, s5, 0
	v_add3_u32 v90, v90, v97, s64
	v_add3_u32 v91, v91, v96, s64
	v_and_b32_sdwa v96, v95, v202 dst_sel:DWORD dst_unused:UNUSED_PAD src0_sel:WORD_1 src1_sel:DWORD
	v_and_b32_sdwa v97, v94, v202 dst_sel:DWORD dst_unused:UNUSED_PAD src0_sel:WORD_1 src1_sel:DWORD
	v_mfma_f32_16x16x32_bf16 v[6:9], v[106:109], v[66:69], v[6:9]
	v_lshl_add_u64 v[50:51], s[6:7], 0, v[168:169]
	s_add_u32 s6, s4, 0x10c40
	v_add3_u32 v95, v95, v96, s64
	v_add3_u32 v94, v94, v97, s64
	v_and_b32_sdwa v96, v130, v202 dst_sel:DWORD dst_unused:UNUSED_PAD src0_sel:WORD_1 src1_sel:DWORD
	v_and_b32_sdwa v97, v132, v202 dst_sel:DWORD dst_unused:UNUSED_PAD src0_sel:WORD_1 src1_sel:DWORD
	s_addc_u32 s7, s5, 0
	v_add3_u32 v108, v130, v96, s64
	v_add3_u32 v109, v132, v97, s64
	v_and_b32_sdwa v96, v131, v202 dst_sel:DWORD dst_unused:UNUSED_PAD src0_sel:WORD_1 src1_sel:DWORD
	v_and_b32_sdwa v97, v133, v202 dst_sel:DWORD dst_unused:UNUSED_PAD src0_sel:WORD_1 src1_sel:DWORD
	v_mfma_f32_16x16x32_bf16 v[2:5], v[118:121], v[54:57], v[2:5]
	v_lshl_add_u64 v[54:55], s[6:7], 0, v[168:169]
	s_add_u32 s6, s4, 0x40c40
	v_and_b32_e32 v95, 0xffff0000, v95
	v_and_b32_e32 v94, 0xffff0000, v94
	v_add3_u32 v96, v131, v96, s64
	v_add3_u32 v106, v133, v97, s64
	s_addc_u32 s7, s5, 0
	v_or_b32_sdwa v91, v95, v91 dst_sel:DWORD dst_unused:UNUSED_PAD src0_sel:DWORD src1_sel:WORD_1
	v_or_b32_sdwa v90, v94, v90 dst_sel:DWORD dst_unused:UNUSED_PAD src0_sel:DWORD src1_sel:WORD_1
	v_mov_b32_e32 v94, v132
	v_mov_b32_e32 v95, v130
	v_and_b32_e32 v97, 0xffff0000, v96
	v_and_b32_e32 v96, 0xffff0000, v106
	v_and_b32_e32 v107, 0xffff0000, v108
	v_and_b32_e32 v106, 0xffff0000, v109
	v_mfma_f32_16x16x32_bf16 v[6:9], v[118:121], v[70:73], v[6:9]
	v_lshl_add_u64 v[62:63], s[6:7], 0, v[168:169]
	s_add_u32 s6, s4, 0x20c40
	v_mov_b32_e32 v130, v133
	v_pk_add_f32 v[94:95], v[94:95], v[106:107] neg_lo:[0,1] neg_hi:[0,1]
	s_addc_u32 s7, s5, 0
	v_pk_add_f32 v[106:107], v[130:131], v[96:97] neg_lo:[0,1] neg_hi:[0,1]
	v_or_b32_sdwa v96, v109, v96 dst_sel:DWORD dst_unused:UNUSED_PAD src0_sel:WORD_1 src1_sel:DWORD
	v_or_b32_sdwa v97, v108, v97 dst_sel:DWORD dst_unused:UNUSED_PAD src0_sel:WORD_1 src1_sel:DWORD
	v_and_b32_sdwa v108, v95, v202 dst_sel:DWORD dst_unused:UNUSED_PAD src0_sel:WORD_1 src1_sel:DWORD
	v_and_b32_sdwa v109, v94, v202 dst_sel:DWORD dst_unused:UNUSED_PAD src0_sel:WORD_1 src1_sel:DWORD
	s_add_u32 s4, s4, 0x50c40
	v_add3_u32 v94, v94, v109, s64
	v_add3_u32 v95, v95, v108, s64
	v_and_b32_sdwa v108, v107, v202 dst_sel:DWORD dst_unused:UNUSED_PAD src0_sel:WORD_1 src1_sel:DWORD
	v_and_b32_sdwa v109, v106, v202 dst_sel:DWORD dst_unused:UNUSED_PAD src0_sel:WORD_1 src1_sel:DWORD
	s_addc_u32 s5, s5, 0
	v_add3_u32 v107, v107, v108, s64
	v_add3_u32 v106, v106, v109, s64
	v_mfma_f32_16x16x32_bf16 v[6:9], v[118:121], v[66:69], v[6:9]
	v_lshl_add_u64 v[66:67], s[6:7], 0, v[168:169]
	v_lshl_add_u64 v[70:71], s[4:5], 0, v[168:169]
	v_and_b32_e32 v107, 0xffff0000, v107
	v_and_b32_e32 v106, 0xffff0000, v106
	global_load_dwordx4 v[38:41], v[38:39], off
	v_or_b32_sdwa v95, v107, v95 dst_sel:DWORD dst_unused:UNUSED_PAD src0_sel:DWORD src1_sel:WORD_1
	global_load_dwordx4 v[50:53], v[50:51], off
	v_or_b32_sdwa v94, v106, v94 dst_sel:DWORD dst_unused:UNUSED_PAD src0_sel:DWORD src1_sel:WORD_1
	global_load_dwordx4 v[54:57], v[54:55], off
	s_mov_b64 s[4:5], 0
	global_load_dwordx4 v[62:65], v[62:63], off
	s_nop 0
	global_load_dwordx4 v[66:69], v[66:67], off
	s_nop 0
	global_load_dwordx4 v[70:73], v[70:71], off
	ds_write2st64_b64 v198, v[92:93], v[96:97] offset0:32 offset1:33
	ds_write2st64_b64 v198, v[90:91], v[94:95] offset0:97 offset1:98
	v_and_b32_sdwa v92, v102, v202 dst_sel:DWORD dst_unused:UNUSED_PAD src0_sel:WORD_1 src1_sel:DWORD
	v_and_b32_sdwa v93, v104, v202 dst_sel:DWORD dst_unused:UNUSED_PAD src0_sel:WORD_1 src1_sel:DWORD
	v_add3_u32 v96, v102, v92, s64
	v_add3_u32 v97, v104, v93, s64
	v_and_b32_sdwa v92, v103, v202 dst_sel:DWORD dst_unused:UNUSED_PAD src0_sel:WORD_1 src1_sel:DWORD
	v_and_b32_sdwa v93, v105, v202 dst_sel:DWORD dst_unused:UNUSED_PAD src0_sel:WORD_1 src1_sel:DWORD
	v_add3_u32 v92, v103, v92, s64
	v_add3_u32 v94, v105, v93, s64
	v_mov_b32_e32 v90, v104
	v_mov_b32_e32 v91, v102
	v_and_b32_e32 v93, 0xffff0000, v92
	v_and_b32_e32 v92, 0xffff0000, v94
	v_and_b32_e32 v95, 0xffff0000, v96
	v_and_b32_e32 v94, 0xffff0000, v97
	v_mov_b32_e32 v102, v105
	v_pk_add_f32 v[90:91], v[90:91], v[94:95] neg_lo:[0,1] neg_hi:[0,1]
	v_pk_add_f32 v[94:95], v[102:103], v[92:93] neg_lo:[0,1] neg_hi:[0,1]
	v_or_b32_sdwa v92, v97, v92 dst_sel:DWORD dst_unused:UNUSED_PAD src0_sel:WORD_1 src1_sel:DWORD
	v_or_b32_sdwa v93, v96, v93 dst_sel:DWORD dst_unused:UNUSED_PAD src0_sel:WORD_1 src1_sel:DWORD
	v_and_b32_sdwa v96, v91, v202 dst_sel:DWORD dst_unused:UNUSED_PAD src0_sel:WORD_1 src1_sel:DWORD
	v_and_b32_sdwa v97, v90, v202 dst_sel:DWORD dst_unused:UNUSED_PAD src0_sel:WORD_1 src1_sel:DWORD
	v_add3_u32 v90, v90, v97, s64
	v_add3_u32 v91, v91, v96, s64
	v_and_b32_sdwa v96, v95, v202 dst_sel:DWORD dst_unused:UNUSED_PAD src0_sel:WORD_1 src1_sel:DWORD
	v_and_b32_sdwa v97, v94, v202 dst_sel:DWORD dst_unused:UNUSED_PAD src0_sel:WORD_1 src1_sel:DWORD
	v_add3_u32 v95, v95, v96, s64
	v_add3_u32 v94, v94, v97, s64
	v_and_b32_sdwa v96, v98, v202 dst_sel:DWORD dst_unused:UNUSED_PAD src0_sel:WORD_1 src1_sel:DWORD
	v_and_b32_sdwa v97, v100, v202 dst_sel:DWORD dst_unused:UNUSED_PAD src0_sel:WORD_1 src1_sel:DWORD
	v_and_b32_e32 v94, 0xffff0000, v94
	v_add3_u32 v102, v98, v96, s64
	v_add3_u32 v103, v100, v97, s64
	v_and_b32_sdwa v96, v99, v202 dst_sel:DWORD dst_unused:UNUSED_PAD src0_sel:WORD_1 src1_sel:DWORD
	v_and_b32_sdwa v97, v101, v202 dst_sel:DWORD dst_unused:UNUSED_PAD src0_sel:WORD_1 src1_sel:DWORD
	v_and_b32_e32 v95, 0xffff0000, v95
	v_or_b32_sdwa v90, v94, v90 dst_sel:DWORD dst_unused:UNUSED_PAD src0_sel:DWORD src1_sel:WORD_1
	v_mov_b32_e32 v94, v100
	v_add3_u32 v96, v99, v96, s64
	v_add3_u32 v100, v101, v97, s64
	v_or_b32_sdwa v91, v95, v91 dst_sel:DWORD dst_unused:UNUSED_PAD src0_sel:DWORD src1_sel:WORD_1
	v_mov_b32_e32 v95, v98
	v_mov_b32_e32 v98, v101
	v_and_b32_e32 v97, 0xffff0000, v96
	v_and_b32_e32 v96, 0xffff0000, v100
	v_and_b32_e32 v101, 0xffff0000, v102
	v_and_b32_e32 v100, 0xffff0000, v103
	v_pk_add_f32 v[94:95], v[94:95], v[100:101] neg_lo:[0,1] neg_hi:[0,1]
	v_pk_add_f32 v[98:99], v[98:99], v[96:97] neg_lo:[0,1] neg_hi:[0,1]
	v_and_b32_sdwa v100, v95, v202 dst_sel:DWORD dst_unused:UNUSED_PAD src0_sel:WORD_1 src1_sel:DWORD
	v_and_b32_sdwa v101, v94, v202 dst_sel:DWORD dst_unused:UNUSED_PAD src0_sel:WORD_1 src1_sel:DWORD
	v_add3_u32 v94, v94, v101, s64
	v_add3_u32 v95, v95, v100, s64
	v_and_b32_sdwa v100, v99, v202 dst_sel:DWORD dst_unused:UNUSED_PAD src0_sel:WORD_1 src1_sel:DWORD
	v_and_b32_sdwa v101, v98, v202 dst_sel:DWORD dst_unused:UNUSED_PAD src0_sel:WORD_1 src1_sel:DWORD
	v_add3_u32 v99, v99, v100, s64
	v_add3_u32 v98, v98, v101, s64
	v_or_b32_sdwa v96, v103, v96 dst_sel:DWORD dst_unused:UNUSED_PAD src0_sel:WORD_1 src1_sel:DWORD
	v_or_b32_sdwa v97, v102, v97 dst_sel:DWORD dst_unused:UNUSED_PAD src0_sel:WORD_1 src1_sel:DWORD
	v_and_b32_e32 v99, 0xffff0000, v99
	v_and_b32_e32 v98, 0xffff0000, v98
	v_or_b32_sdwa v95, v99, v95 dst_sel:DWORD dst_unused:UNUSED_PAD src0_sel:DWORD src1_sel:WORD_1
	v_or_b32_sdwa v94, v98, v94 dst_sel:DWORD dst_unused:UNUSED_PAD src0_sel:DWORD src1_sel:WORD_1
	ds_write2st64_b64 v203, v[92:93], v[96:97] offset0:34 offset1:35
	ds_write2st64_b64 v203, v[90:91], v[94:95] offset0:99 offset1:100
	v_and_b32_sdwa v92, v78, v202 dst_sel:DWORD dst_unused:UNUSED_PAD src0_sel:WORD_1 src1_sel:DWORD
	v_and_b32_sdwa v93, v80, v202 dst_sel:DWORD dst_unused:UNUSED_PAD src0_sel:WORD_1 src1_sel:DWORD
	v_mov_b32_e32 v90, v80
	v_add3_u32 v94, v78, v92, s64
	v_add3_u32 v95, v80, v93, s64
	v_and_b32_sdwa v80, v79, v202 dst_sel:DWORD dst_unused:UNUSED_PAD src0_sel:WORD_1 src1_sel:DWORD
	v_and_b32_sdwa v92, v81, v202 dst_sel:DWORD dst_unused:UNUSED_PAD src0_sel:WORD_1 src1_sel:DWORD
	v_add3_u32 v80, v79, v80, s64
	v_add3_u32 v92, v81, v92, s64
	v_mov_b32_e32 v91, v78
	v_mov_b32_e32 v78, v81
	v_and_b32_e32 v81, 0xffff0000, v80
	v_and_b32_e32 v80, 0xffff0000, v92
	v_and_b32_e32 v93, 0xffff0000, v94
	v_and_b32_e32 v92, 0xffff0000, v95
	v_pk_add_f32 v[90:91], v[90:91], v[92:93] neg_lo:[0,1] neg_hi:[0,1]
	v_pk_add_f32 v[78:79], v[78:79], v[80:81] neg_lo:[0,1] neg_hi:[0,1]
	v_and_b32_sdwa v93, v90, v202 dst_sel:DWORD dst_unused:UNUSED_PAD src0_sel:WORD_1 src1_sel:DWORD
	v_and_b32_sdwa v92, v91, v202 dst_sel:DWORD dst_unused:UNUSED_PAD src0_sel:WORD_1 src1_sel:DWORD
	v_add3_u32 v90, v90, v93, s64
	v_and_b32_sdwa v93, v78, v202 dst_sel:DWORD dst_unused:UNUSED_PAD src0_sel:WORD_1 src1_sel:DWORD
	v_add3_u32 v91, v91, v92, s64
	v_and_b32_sdwa v92, v79, v202 dst_sel:DWORD dst_unused:UNUSED_PAD src0_sel:WORD_1 src1_sel:DWORD
	v_add3_u32 v78, v78, v93, s64
	v_add3_u32 v79, v79, v92, s64
	v_and_b32_e32 v78, 0xffff0000, v78
	v_and_b32_sdwa v92, v74, v202 dst_sel:DWORD dst_unused:UNUSED_PAD src0_sel:WORD_1 src1_sel:DWORD
	v_and_b32_sdwa v93, v76, v202 dst_sel:DWORD dst_unused:UNUSED_PAD src0_sel:WORD_1 src1_sel:DWORD
	v_or_b32_sdwa v80, v95, v80 dst_sel:DWORD dst_unused:UNUSED_PAD src0_sel:WORD_1 src1_sel:DWORD
	v_or_b32_sdwa v81, v94, v81 dst_sel:DWORD dst_unused:UNUSED_PAD src0_sel:WORD_1 src1_sel:DWORD
	v_or_b32_sdwa v78, v78, v90 dst_sel:DWORD dst_unused:UNUSED_PAD src0_sel:DWORD src1_sel:WORD_1
	v_mov_b32_e32 v90, v76
	v_add3_u32 v94, v74, v92, s64
	v_add3_u32 v95, v76, v93, s64
	v_and_b32_sdwa v76, v75, v202 dst_sel:DWORD dst_unused:UNUSED_PAD src0_sel:WORD_1 src1_sel:DWORD
	v_and_b32_sdwa v92, v77, v202 dst_sel:DWORD dst_unused:UNUSED_PAD src0_sel:WORD_1 src1_sel:DWORD
	v_and_b32_e32 v79, 0xffff0000, v79
	v_add3_u32 v76, v75, v76, s64
	v_add3_u32 v92, v77, v92, s64
	v_or_b32_sdwa v79, v79, v91 dst_sel:DWORD dst_unused:UNUSED_PAD src0_sel:DWORD src1_sel:WORD_1
	v_mov_b32_e32 v91, v74
	v_mov_b32_e32 v74, v77
	v_and_b32_e32 v77, 0xffff0000, v76
	v_and_b32_e32 v76, 0xffff0000, v92
	v_and_b32_e32 v93, 0xffff0000, v94
	v_and_b32_e32 v92, 0xffff0000, v95
	v_pk_add_f32 v[90:91], v[90:91], v[92:93] neg_lo:[0,1] neg_hi:[0,1]
	v_pk_add_f32 v[74:75], v[74:75], v[76:77] neg_lo:[0,1] neg_hi:[0,1]
	v_and_b32_sdwa v92, v91, v202 dst_sel:DWORD dst_unused:UNUSED_PAD src0_sel:WORD_1 src1_sel:DWORD
	v_and_b32_sdwa v93, v90, v202 dst_sel:DWORD dst_unused:UNUSED_PAD src0_sel:WORD_1 src1_sel:DWORD
	v_add3_u32 v90, v90, v93, s64
	v_add3_u32 v91, v91, v92, s64
	v_and_b32_sdwa v92, v75, v202 dst_sel:DWORD dst_unused:UNUSED_PAD src0_sel:WORD_1 src1_sel:DWORD
	v_and_b32_sdwa v93, v74, v202 dst_sel:DWORD dst_unused:UNUSED_PAD src0_sel:WORD_1 src1_sel:DWORD
	v_add3_u32 v75, v75, v92, s64
	v_add3_u32 v74, v74, v93, s64
	v_or_b32_sdwa v76, v95, v76 dst_sel:DWORD dst_unused:UNUSED_PAD src0_sel:WORD_1 src1_sel:DWORD
	v_or_b32_sdwa v77, v94, v77 dst_sel:DWORD dst_unused:UNUSED_PAD src0_sel:WORD_1 src1_sel:DWORD
	v_and_b32_e32 v75, 0xffff0000, v75
	v_and_b32_e32 v74, 0xffff0000, v74
	v_or_b32_sdwa v75, v75, v91 dst_sel:DWORD dst_unused:UNUSED_PAD src0_sel:DWORD src1_sel:WORD_1
	v_or_b32_sdwa v74, v74, v90 dst_sel:DWORD dst_unused:UNUSED_PAD src0_sel:DWORD src1_sel:WORD_1
	ds_write2st64_b64 v204, v[80:81], v[76:77] offset0:36 offset1:37
	ds_write2st64_b64 v204, v[78:79], v[74:75] offset0:101 offset1:102
	v_and_b32_sdwa v76, v86, v202 dst_sel:DWORD dst_unused:UNUSED_PAD src0_sel:WORD_1 src1_sel:DWORD
	v_and_b32_sdwa v77, v88, v202 dst_sel:DWORD dst_unused:UNUSED_PAD src0_sel:WORD_1 src1_sel:DWORD
	v_add3_u32 v80, v86, v76, s64
	v_add3_u32 v81, v88, v77, s64
	v_and_b32_sdwa v76, v87, v202 dst_sel:DWORD dst_unused:UNUSED_PAD src0_sel:WORD_1 src1_sel:DWORD
	v_and_b32_sdwa v77, v89, v202 dst_sel:DWORD dst_unused:UNUSED_PAD src0_sel:WORD_1 src1_sel:DWORD
	v_add3_u32 v76, v87, v76, s64
	v_add3_u32 v78, v89, v77, s64
	v_mov_b32_e32 v74, v88
	v_mov_b32_e32 v75, v86
	v_and_b32_e32 v77, 0xffff0000, v76
	v_and_b32_e32 v76, 0xffff0000, v78
	v_and_b32_e32 v79, 0xffff0000, v80
	v_and_b32_e32 v78, 0xffff0000, v81
	v_mov_b32_e32 v86, v89
	v_pk_add_f32 v[74:75], v[74:75], v[78:79] neg_lo:[0,1] neg_hi:[0,1]
	v_pk_add_f32 v[78:79], v[86:87], v[76:77] neg_lo:[0,1] neg_hi:[0,1]
	v_or_b32_sdwa v76, v81, v76 dst_sel:DWORD dst_unused:UNUSED_PAD src0_sel:WORD_1 src1_sel:DWORD
	v_or_b32_sdwa v77, v80, v77 dst_sel:DWORD dst_unused:UNUSED_PAD src0_sel:WORD_1 src1_sel:DWORD
	v_and_b32_sdwa v80, v75, v202 dst_sel:DWORD dst_unused:UNUSED_PAD src0_sel:WORD_1 src1_sel:DWORD
	v_and_b32_sdwa v81, v74, v202 dst_sel:DWORD dst_unused:UNUSED_PAD src0_sel:WORD_1 src1_sel:DWORD
	v_add3_u32 v74, v74, v81, s64
	v_add3_u32 v75, v75, v80, s64
	v_and_b32_sdwa v80, v79, v202 dst_sel:DWORD dst_unused:UNUSED_PAD src0_sel:WORD_1 src1_sel:DWORD
	v_and_b32_sdwa v81, v78, v202 dst_sel:DWORD dst_unused:UNUSED_PAD src0_sel:WORD_1 src1_sel:DWORD
	v_add3_u32 v79, v79, v80, s64
	v_add3_u32 v78, v78, v81, s64
	v_and_b32_sdwa v80, v82, v202 dst_sel:DWORD dst_unused:UNUSED_PAD src0_sel:WORD_1 src1_sel:DWORD
	v_and_b32_sdwa v81, v84, v202 dst_sel:DWORD dst_unused:UNUSED_PAD src0_sel:WORD_1 src1_sel:DWORD
	v_and_b32_e32 v78, 0xffff0000, v78
	v_add3_u32 v86, v82, v80, s64
	v_add3_u32 v87, v84, v81, s64
	v_and_b32_sdwa v80, v83, v202 dst_sel:DWORD dst_unused:UNUSED_PAD src0_sel:WORD_1 src1_sel:DWORD
	v_and_b32_sdwa v81, v85, v202 dst_sel:DWORD dst_unused:UNUSED_PAD src0_sel:WORD_1 src1_sel:DWORD
	v_and_b32_e32 v79, 0xffff0000, v79
	v_or_b32_sdwa v74, v78, v74 dst_sel:DWORD dst_unused:UNUSED_PAD src0_sel:DWORD src1_sel:WORD_1
	v_mov_b32_e32 v78, v84
	v_add3_u32 v80, v83, v80, s64
	v_add3_u32 v84, v85, v81, s64
	v_or_b32_sdwa v75, v79, v75 dst_sel:DWORD dst_unused:UNUSED_PAD src0_sel:DWORD src1_sel:WORD_1
	v_mov_b32_e32 v79, v82
	v_mov_b32_e32 v82, v85
	v_and_b32_e32 v81, 0xffff0000, v80
	v_and_b32_e32 v80, 0xffff0000, v84
	v_and_b32_e32 v85, 0xffff0000, v86
	v_and_b32_e32 v84, 0xffff0000, v87
	v_pk_add_f32 v[78:79], v[78:79], v[84:85] neg_lo:[0,1] neg_hi:[0,1]
	v_pk_add_f32 v[82:83], v[82:83], v[80:81] neg_lo:[0,1] neg_hi:[0,1]
	v_and_b32_sdwa v84, v79, v202 dst_sel:DWORD dst_unused:UNUSED_PAD src0_sel:WORD_1 src1_sel:DWORD
	v_and_b32_sdwa v85, v78, v202 dst_sel:DWORD dst_unused:UNUSED_PAD src0_sel:WORD_1 src1_sel:DWORD
	v_add3_u32 v78, v78, v85, s64
	v_add3_u32 v79, v79, v84, s64
	v_and_b32_sdwa v84, v83, v202 dst_sel:DWORD dst_unused:UNUSED_PAD src0_sel:WORD_1 src1_sel:DWORD
	v_and_b32_sdwa v85, v82, v202 dst_sel:DWORD dst_unused:UNUSED_PAD src0_sel:WORD_1 src1_sel:DWORD
	v_add3_u32 v83, v83, v84, s64
	v_add3_u32 v82, v82, v85, s64
	v_and_b32_e32 v83, 0xffff0000, v83
	v_and_b32_e32 v82, 0xffff0000, v82
	v_or_b32_sdwa v80, v87, v80 dst_sel:DWORD dst_unused:UNUSED_PAD src0_sel:WORD_1 src1_sel:DWORD
	v_or_b32_sdwa v81, v86, v81 dst_sel:DWORD dst_unused:UNUSED_PAD src0_sel:WORD_1 src1_sel:DWORD
	v_or_b32_sdwa v79, v83, v79 dst_sel:DWORD dst_unused:UNUSED_PAD src0_sel:DWORD src1_sel:WORD_1
	v_or_b32_sdwa v78, v82, v78 dst_sel:DWORD dst_unused:UNUSED_PAD src0_sel:DWORD src1_sel:WORD_1
	ds_write2st64_b64 v205, v[76:77], v[80:81] offset0:38 offset1:39
	ds_write2st64_b64 v205, v[74:75], v[78:79] offset0:103 offset1:104
	s_waitcnt lgkmcnt(0)
	s_barrier
	ds_read_b128 v[74:77], v199 offset:49664
	ds_read_b128 v[78:81], v199 offset:49728
	s_waitcnt vmcnt(11) lgkmcnt(1)
	v_mfma_f32_16x16x32_bf16 v[26:29], v[74:77], v[30:33], v[26:29]
	ds_read_b128 v[82:85], v199 offset:16384
	ds_read_b128 v[86:89], v199 offset:16448
	s_waitcnt vmcnt(8)
	v_mfma_f32_16x16x32_bf16 v[18:21], v[74:77], v[42:45], v[18:21]
	s_waitcnt vmcnt(6)
	v_mfma_f32_16x16x32_bf16 v[22:25], v[74:77], v[58:61], v[22:25]
	v_mfma_f32_16x16x32_bf16 v[26:29], v[74:77], v[14:17], v[26:29]
	v_mfma_f32_16x16x32_bf16 v[18:21], v[74:77], v[34:37], v[18:21]
	v_mfma_f32_16x16x32_bf16 v[22:25], v[74:77], v[46:49], v[22:25]
	s_waitcnt lgkmcnt(1)
	v_mfma_f32_16x16x32_bf16 v[26:29], v[82:85], v[30:33], v[26:29]
	v_mfma_f32_16x16x32_bf16 v[18:21], v[82:85], v[42:45], v[18:21]
	v_mfma_f32_16x16x32_bf16 v[22:25], v[82:85], v[58:61], v[22:25]
	v_mfma_f32_16x16x32_bf16 v[26:29], v[82:85], v[14:17], v[26:29]
	v_mfma_f32_16x16x32_bf16 v[18:21], v[82:85], v[34:37], v[18:21]
	v_mfma_f32_16x16x32_bf16 v[22:25], v[82:85], v[46:49], v[22:25]
	ds_read_b128 v[74:77], v200 offset:49664
	ds_read_b128 v[82:85], v200 offset:49728
	ds_read_b128 v[90:93], v199 offset:33024
	ds_read_b128 v[94:97], v199 offset:33088
	s_waitcnt lgkmcnt(0)
	v_mfma_f32_16x16x32_bf16 v[10:13], v[74:77], v[30:33], v[10:13]
	s_barrier
	v_mfma_f32_16x16x32_bf16 v[2:5], v[74:77], v[42:45], v[2:5]
	v_mfma_f32_16x16x32_bf16 v[6:9], v[74:77], v[58:61], v[6:9]
	v_mfma_f32_16x16x32_bf16 v[10:13], v[74:77], v[14:17], v[10:13]
	v_mfma_f32_16x16x32_bf16 v[2:5], v[74:77], v[34:37], v[2:5]
	v_mfma_f32_16x16x32_bf16 v[6:9], v[74:77], v[46:49], v[6:9]
	v_mfma_f32_16x16x32_bf16 v[10:13], v[90:93], v[30:33], v[10:13]
	v_mfma_f32_16x16x32_bf16 v[2:5], v[90:93], v[42:45], v[2:5]
	v_mfma_f32_16x16x32_bf16 v[6:9], v[90:93], v[58:61], v[6:9]
	v_mfma_f32_16x16x32_bf16 v[10:13], v[90:93], v[14:17], v[10:13]
	v_mfma_f32_16x16x32_bf16 v[2:5], v[90:93], v[34:37], v[2:5]
	v_mfma_f32_16x16x32_bf16 v[6:9], v[90:93], v[46:49], v[6:9]
	s_waitcnt vmcnt(4)
	v_mfma_f32_16x16x32_bf16 v[14:17], v[78:81], v[50:53], v[26:29]
	s_waitcnt vmcnt(2)
	v_mfma_f32_16x16x32_bf16 v[18:21], v[78:81], v[62:65], v[18:21]
	s_waitcnt vmcnt(0)
	v_mfma_f32_16x16x32_bf16 v[22:25], v[78:81], v[70:73], v[22:25]
	v_mfma_f32_16x16x32_bf16 v[10:13], v[82:85], v[50:53], v[10:13]
	v_mfma_f32_16x16x32_bf16 v[14:17], v[78:81], v[38:41], v[14:17]
	v_mfma_f32_16x16x32_bf16 v[2:5], v[82:85], v[62:65], v[2:5]
	v_mfma_f32_16x16x32_bf16 v[6:9], v[82:85], v[70:73], v[6:9]
	v_mfma_f32_16x16x32_bf16 v[18:21], v[78:81], v[54:57], v[18:21]
	v_mfma_f32_16x16x32_bf16 v[22:25], v[78:81], v[66:69], v[22:25]
	v_mfma_f32_16x16x32_bf16 v[10:13], v[82:85], v[38:41], v[10:13]
	v_mfma_f32_16x16x32_bf16 v[14:17], v[86:89], v[50:53], v[14:17]
	v_mfma_f32_16x16x32_bf16 v[2:5], v[82:85], v[54:57], v[2:5]
	v_mfma_f32_16x16x32_bf16 v[6:9], v[82:85], v[66:69], v[6:9]
	v_mfma_f32_16x16x32_bf16 v[18:21], v[86:89], v[62:65], v[18:21]
	v_mfma_f32_16x16x32_bf16 v[22:25], v[86:89], v[70:73], v[22:25]
	v_mfma_f32_16x16x32_bf16 v[10:13], v[94:97], v[50:53], v[10:13]
	v_mfma_f32_16x16x32_bf16 v[14:17], v[86:89], v[38:41], v[14:17]
	v_mfma_f32_16x16x32_bf16 v[2:5], v[94:97], v[62:65], v[2:5]
	v_mfma_f32_16x16x32_bf16 v[6:9], v[94:97], v[70:73], v[6:9]
	v_mfma_f32_16x16x32_bf16 v[18:21], v[86:89], v[54:57], v[18:21]
	v_mfma_f32_16x16x32_bf16 v[22:25], v[86:89], v[66:69], v[22:25]
	v_mfma_f32_16x16x32_bf16 v[10:13], v[94:97], v[38:41], v[10:13]
	v_mfma_f32_16x16x32_bf16 v[2:5], v[94:97], v[54:57], v[2:5]
	v_mfma_f32_16x16x32_bf16 v[6:9], v[94:97], v[66:69], v[6:9]
	s_nop 0
	ds_write_b128 v201, v[14:17]
	s_nop 1
	ds_write_b128 v201, v[18:21] offset:1024
	ds_write_b128 v201, v[22:25] offset:2048
	ds_write_b128 v201, v[10:13] offset:3072
	ds_write_b128 v201, v[2:5] offset:4096
	ds_write_b128 v201, v[6:9] offset:5120
	v_mov_b32_e32 v10, v189
	v_mov_b32_e32 v11, v187
	v_mov_b32_e32 v12, v185
	v_mov_b32_e32 v13, v186
	v_mov_b32_e32 v14, v0
	s_waitcnt lgkmcnt(0)
	s_barrier
	s_branch .LBB0_615
